# MFMA snake order: consecutive MFMAs share accumulator or one operand quad; second block of each pair walks m downward; k-order flipped for half the accumulators
# speedup vs baseline: 1.0188x; 1.0188x over previous
; #define PG8_STAGE(bufoff, gbase, voff) do { const char* _gb = (const char*)(gbase); asm volatile("" : "+s"(_gb)); _Pragma("unroll") for (int _i = 0; _i < 2; ++_i) \
;         __builtin_amdgcn_global_load_lds((const unsigned*)(_gb + (voff)[_i]), (PG8_LAS unsigned*)(lds + (bufoff) + ldsw + _i * 8192), 16, 0, 0); } while (0)
; #define PG8_LDA(dst, b, h) do { _Pragma("unroll") for (int m = 0; m < 4; ++m) _Pragma("unroll") for (int k = 0; k < 2; ++k) dst[m][k] = *(const PG8_LAS bf16x8*)(lds + PG8_SA(b, h) + aoff + m * 2048 + k * 1024); } while (0)
; #define PG8_MMA(ai, bj, At, Bt) do { __builtin_amdgcn_s_setprio(1); _Pragma("unroll") for (int m = 0; m < 4; ++m) _Pragma("unroll") for (int n = 0; n < 2; ++n) _Pragma("unroll") for (int k = 0; k < 2; ++k) \
;         acc[ai][bj][m][n] = __builtin_amdgcn_mfma_f32_16x16x32_bf16(Bt[n][k], At[m][k], acc[ai][bj][m][n], 0, 0, 0); __builtin_amdgcn_s_setprio(0); } while (0)
; #define PG8_WAIT_L(n) asm volatile("s_waitcnt lgkmcnt(" #n ")" ::: "memory")
; #define PG8_BAR __builtin_amdgcn_s_barrier()
; #define PG8_SCHED __builtin_amdgcn_sched_barrier(0)
; template <class Epi, class Sched, bool ALIGN_EPI = false, bool SP2 = false, bool HALFM = false>
; __device__ __forceinline__ void gemm_phase(PG8_LAS unsigned char* lds, const Gemm g, const Sched& S, const Epi& E) {
;     ...
;             PG8_WAIT_V8R; PG8_WAIT_L(0); PG8_BAR; PG8_MMA(0, 0, At, B0); PG8_MMA(0, 1, At, B1); PG8_BAR; PG8_SCHED;
;             if constexpr (!HALFM) { PG8_LDA(At, 0, 1); } PG8_STAGE(PG8_SB(0, 0), b2, voffB); PG8_STAGE(PG8_SB(0, 1), b2 + hstep, voffB); PG8_STAGE(PG8_SA(0, 0), a2, voffA);
;             PG8_WAIT_V8R; PG8_WAIT_L(0); PG8_BAR; if constexpr (!HALFM) { PG8_MMA(1, 0, At, B0); PG8_MMA(1, 1, At, B1); } PG8_BAR; PG8_SCHED;
.Lry0:
	s_waitcnt lgkmcnt(0)
	s_barrier
	s_setprio 1
	s_waitcnt lgkmcnt(0)
	v_mfma_f32_16x16x32_bf16 v[126:129], v[130:133], v[162:165], v[126:129]
	v_mfma_f32_16x16x32_bf16 v[126:129], v[134:137], v[166:169], v[126:129]
	v_mfma_f32_16x16x32_bf16 v[122:125], v[142:145], v[166:169], v[122:125]
	v_mfma_f32_16x16x32_bf16 v[122:125], v[138:141], v[162:165], v[122:125]
	v_mfma_f32_16x16x32_bf16 v[106:109], v[138:141], v[170:173], v[106:109]
	v_mfma_f32_16x16x32_bf16 v[106:109], v[142:145], v[174:177], v[106:109]
	v_mfma_f32_16x16x32_bf16 v[110:113], v[134:137], v[174:177], v[110:113]
	v_mfma_f32_16x16x32_bf16 v[110:113], v[130:133], v[170:173], v[110:113]
	v_mfma_f32_16x16x32_bf16 v[94:97], v[130:133], v[194:197], v[94:97]
	v_mfma_f32_16x16x32_bf16 v[94:97], v[134:137], v[198:201], v[94:97]
	v_mfma_f32_16x16x32_bf16 v[90:93], v[142:145], v[198:201], v[90:93]
	v_mfma_f32_16x16x32_bf16 v[90:93], v[138:141], v[194:197], v[90:93]
	v_mfma_f32_16x16x32_bf16 v[74:77], v[138:141], v[202:205], v[74:77]
	v_mfma_f32_16x16x32_bf16 v[74:77], v[142:145], v[206:209], v[74:77]
	v_mfma_f32_16x16x32_bf16 v[78:81], v[134:137], v[206:209], v[78:81]
	v_mfma_f32_16x16x32_bf16 v[78:81], v[130:133], v[202:205], v[78:81]
	s_setprio 0
	s_setprio 1
	v_mfma_f32_16x16x32_bf16 v[70:73], v[146:149], v[202:205], v[70:73]
	v_mfma_f32_16x16x32_bf16 v[70:73], v[150:153], v[206:209], v[70:73]
	v_mfma_f32_16x16x32_bf16 v[66:69], v[158:161], v[206:209], v[66:69]
	v_mfma_f32_16x16x32_bf16 v[66:69], v[154:157], v[202:205], v[66:69]
	v_mfma_f32_16x16x32_bf16 v[82:85], v[154:157], v[194:197], v[82:85]
	v_mfma_f32_16x16x32_bf16 v[82:85], v[158:161], v[198:201], v[82:85]
	v_mfma_f32_16x16x32_bf16 v[86:89], v[150:153], v[198:201], v[86:89]
	v_mfma_f32_16x16x32_bf16 v[86:89], v[146:149], v[194:197], v[86:89]
	v_mfma_f32_16x16x32_bf16 v[102:105], v[146:149], v[170:173], v[102:105]
	v_mfma_f32_16x16x32_bf16 v[102:105], v[150:153], v[174:177], v[102:105]
	v_mfma_f32_16x16x32_bf16 v[98:101], v[158:161], v[174:177], v[98:101]
	v_mfma_f32_16x16x32_bf16 v[98:101], v[154:157], v[170:173], v[98:101]
	v_mfma_f32_16x16x32_bf16 v[114:117], v[154:157], v[162:165], v[114:117]
	v_mfma_f32_16x16x32_bf16 v[114:117], v[158:161], v[166:169], v[114:117]
	v_mfma_f32_16x16x32_bf16 v[118:121], v[150:153], v[166:169], v[118:121]
	v_mfma_f32_16x16x32_bf16 v[118:121], v[146:149], v[162:165], v[118:121]
	s_setprio 0
	s_barrier
	s_add_i32 s89, s46, s41
	s_mov_b64 s[86:87], s[38:39]
	s_mov_b32 m0, s89
	ds_read_b128 v[162:165], v218 offset:16384
	ds_read_b128 v[166:169], v218 offset:17408
	ds_read_b128 v[170:173], v218 offset:18432
	ds_read_b128 v[174:177], v218 offset:19456
	ds_read_b128 v[194:197], v218 offset:20480
	ds_read_b128 v[198:201], v218 offset:21504
	ds_read_b128 v[202:205], v218 offset:22528
	ds_read_b128 v[206:209], v218 offset:23552
	s_nop 0
	global_load_lds_dwordx4 v221, s[86:87]
	s_add_i32 m0, s89, 0x2000
	s_nop 0
	global_load_lds_dwordx4 v181, s[86:87]
	s_add_u32 s86, s38, 0x4000
	s_addc_u32 s87, s39, 0
	s_add_i32 s89, s47, s41
	s_mov_b32 m0, s89
	s_nop 0
	global_load_lds_dwordx4 v221, s[86:87]
	s_add_i32 m0, s89, 0x2000
	s_nop 0
	global_load_lds_dwordx4 v181, s[86:87]
	s_mov_b64 s[86:87], s[0:1]
	s_mov_b32 m0, s37
	s_nop 0
	global_load_lds_dwordx4 v221, s[86:87]
	s_mov_b32 m0, s52
	s_nop 0
	global_load_lds_dwordx4 v181, s[86:87]
	s_cmp_eq_u32 s88, 0
	s_cbranch_scc1 .Lrx1
	s_waitcnt vmcnt(32)
	s_branch .Lry1

; #define PG8_STAGE(bufoff, gbase, voff) do { const char* _gb = (const char*)(gbase); asm volatile("" : "+s"(_gb)); _Pragma("unroll") for (int _i = 0; _i < 2; ++_i) \
;         __builtin_amdgcn_global_load_lds((const unsigned*)(_gb + (voff)[_i]), (PG8_LAS unsigned*)(lds + (bufoff) + ldsw + _i * 8192), 16, 0, 0); } while (0)
; #define PG8_LDA(dst, b, h) do { _Pragma("unroll") for (int m = 0; m < 4; ++m) _Pragma("unroll") for (int k = 0; k < 2; ++k) dst[m][k] = *(const PG8_LAS bf16x8*)(lds + PG8_SA(b, h) + aoff + m * 2048 + k * 1024); } while (0)
; #define PG8_LDB(dst, b, h) do { _Pragma("unroll") for (int n = 0; n < 2; ++n) _Pragma("unroll") for (int k = 0; k < 2; ++k) dst[n][k] = *(const PG8_LAS bf16x8*)(lds + PG8_SB(b, h) + boff + n * 2048 + k * 1024); } while (0)
; #define PG8_MMA(ai, bj, At, Bt) do { __builtin_amdgcn_s_setprio(1); _Pragma("unroll") for (int m = 0; m < 4; ++m) _Pragma("unroll") for (int n = 0; n < 2; ++n) _Pragma("unroll") for (int k = 0; k < 2; ++k) \
;         acc[ai][bj][m][n] = __builtin_amdgcn_mfma_f32_16x16x32_bf16(Bt[n][k], At[m][k], acc[ai][bj][m][n], 0, 0, 0); __builtin_amdgcn_s_setprio(0); } while (0)
; #define PG8_WAIT_L(n) asm volatile("s_waitcnt lgkmcnt(" #n ")" ::: "memory")
; #define PG8_BAR __builtin_amdgcn_s_barrier()
; #define PG8_SCHED __builtin_amdgcn_sched_barrier(0)
; template <class Epi, class Sched, bool ALIGN_EPI = false, bool SP2 = false, bool HALFM = false>
; __device__ __forceinline__ void gemm_phase(PG8_LAS unsigned char* lds, const Gemm g, const Sched& S, const Epi& E) {
;     ...
;             PG8_WAIT_V8R; PG8_WAIT_L(0); PG8_BAR; if constexpr (!HALFM) { PG8_MMA(1, 0, At, B0); PG8_MMA(1, 1, At, B1); } PG8_BAR; PG8_SCHED;
;             PG8_LDB(B0, 1, 0); PG8_LDB(B1, 1, 1); PG8_SCHED; PG8_LDA(At, 1, 0); PG8_STAGE(PG8_SA(0, 1), a2 + hstepA, voffA);
;             PG8_WAIT_V8R; PG8_WAIT_L(0); PG8_BAR; PG8_MMA(0, 0, At, B0); PG8_MMA(0, 1, At, B1); PG8_BAR; PG8_SCHED;
.Lry1:
	s_waitcnt lgkmcnt(0)
	s_barrier
	s_setprio 1
	s_waitcnt lgkmcnt(0)
	v_mfma_f32_16x16x32_bf16 v[62:65], v[130:133], v[162:165], v[62:65]
	v_mfma_f32_16x16x32_bf16 v[62:65], v[134:137], v[166:169], v[62:65]
	v_mfma_f32_16x16x32_bf16 v[58:61], v[142:145], v[166:169], v[58:61]
	v_mfma_f32_16x16x32_bf16 v[58:61], v[138:141], v[162:165], v[58:61]
	v_mfma_f32_16x16x32_bf16 v[42:45], v[138:141], v[170:173], v[42:45]
	v_mfma_f32_16x16x32_bf16 v[42:45], v[142:145], v[174:177], v[42:45]
	v_mfma_f32_16x16x32_bf16 v[46:49], v[134:137], v[174:177], v[46:49]
	v_mfma_f32_16x16x32_bf16 v[46:49], v[130:133], v[170:173], v[46:49]
	v_mfma_f32_16x16x32_bf16 v[30:33], v[130:133], v[194:197], v[30:33]
	v_mfma_f32_16x16x32_bf16 v[30:33], v[134:137], v[198:201], v[30:33]
	v_mfma_f32_16x16x32_bf16 v[26:29], v[142:145], v[198:201], v[26:29]
	v_mfma_f32_16x16x32_bf16 v[26:29], v[138:141], v[194:197], v[26:29]
	v_mfma_f32_16x16x32_bf16 v[10:13], v[138:141], v[202:205], v[10:13]
	v_mfma_f32_16x16x32_bf16 v[10:13], v[142:145], v[206:209], v[10:13]
	v_mfma_f32_16x16x32_bf16 v[14:17], v[134:137], v[206:209], v[14:17]
	v_mfma_f32_16x16x32_bf16 v[14:17], v[130:133], v[202:205], v[14:17]
	s_setprio 0
	s_setprio 1
	v_mfma_f32_16x16x32_bf16 v[6:9], v[146:149], v[202:205], v[6:9]
	v_mfma_f32_16x16x32_bf16 v[6:9], v[150:153], v[206:209], v[6:9]
	v_mfma_f32_16x16x32_bf16 v[2:5], v[158:161], v[206:209], v[2:5]
	v_mfma_f32_16x16x32_bf16 v[2:5], v[154:157], v[202:205], v[2:5]
	v_mfma_f32_16x16x32_bf16 v[18:21], v[154:157], v[194:197], v[18:21]
	v_mfma_f32_16x16x32_bf16 v[18:21], v[158:161], v[198:201], v[18:21]
	v_mfma_f32_16x16x32_bf16 v[22:25], v[150:153], v[198:201], v[22:25]
	v_mfma_f32_16x16x32_bf16 v[22:25], v[146:149], v[194:197], v[22:25]
	v_mfma_f32_16x16x32_bf16 v[38:41], v[146:149], v[170:173], v[38:41]
	v_mfma_f32_16x16x32_bf16 v[38:41], v[150:153], v[174:177], v[38:41]
	v_mfma_f32_16x16x32_bf16 v[34:37], v[158:161], v[174:177], v[34:37]
	v_mfma_f32_16x16x32_bf16 v[34:37], v[154:157], v[170:173], v[34:37]
	v_mfma_f32_16x16x32_bf16 v[50:53], v[154:157], v[162:165], v[50:53]
	v_mfma_f32_16x16x32_bf16 v[50:53], v[158:161], v[166:169], v[50:53]
	v_mfma_f32_16x16x32_bf16 v[54:57], v[150:153], v[166:169], v[54:57]
	v_mfma_f32_16x16x32_bf16 v[54:57], v[146:149], v[162:165], v[54:57]
	s_setprio 0
	s_barrier
	s_add_i32 s89, 0, 0x18000
	s_add_i32 s90, 0, 0x1c000
	v_add_u32_e32 v142, s89, v214
	v_add_u32_e32 v158, s90, v214
	ds_read_b128 v[130:133], v142
	ds_read_b128 v[134:137], v142 offset:1024
	ds_read_b128 v[138:141], v142 offset:2048
	ds_read_b128 v[142:145], v142 offset:3072
	ds_read_b128 v[146:149], v158
	ds_read_b128 v[150:153], v158 offset:1024
	ds_read_b128 v[154:157], v158 offset:2048
	ds_read_b128 v[158:161], v158 offset:3072
	s_add_u32 s86, s0, 0x4000
	s_addc_u32 s87, s1, 0
	s_mov_b32 m0, s53
	ds_read_b128 v[162:165], v218 offset:32768
	ds_read_b128 v[166:169], v218 offset:33792
	ds_read_b128 v[170:173], v218 offset:34816
	ds_read_b128 v[174:177], v218 offset:35840
	ds_read_b128 v[194:197], v218 offset:36864
	ds_read_b128 v[198:201], v218 offset:37888
	ds_read_b128 v[202:205], v218 offset:38912
	ds_read_b128 v[206:209], v218 offset:39936
	s_nop 0
	global_load_lds_dwordx4 v221, s[86:87]
	s_mov_b32 m0, s54
	s_nop 0
	global_load_lds_dwordx4 v181, s[86:87]
	s_cmp_eq_u32 s88, 0
	s_cbranch_scc1 .Lrx2
	s_waitcnt vmcnt(32)
	s_branch .Lry2

; #define PG8_STAGE(bufoff, gbase, voff) do { const char* _gb = (const char*)(gbase); asm volatile("" : "+s"(_gb)); _Pragma("unroll") for (int _i = 0; _i < 2; ++_i) \
;         __builtin_amdgcn_global_load_lds((const unsigned*)(_gb + (voff)[_i]), (PG8_LAS unsigned*)(lds + (bufoff) + ldsw + _i * 8192), 16, 0, 0); } while (0)
; #define PG8_LDA(dst, b, h) do { _Pragma("unroll") for (int m = 0; m < 4; ++m) _Pragma("unroll") for (int k = 0; k < 2; ++k) dst[m][k] = *(const PG8_LAS bf16x8*)(lds + PG8_SA(b, h) + aoff + m * 2048 + k * 1024); } while (0)
; #define PG8_MMA(ai, bj, At, Bt) do { __builtin_amdgcn_s_setprio(1); _Pragma("unroll") for (int m = 0; m < 4; ++m) _Pragma("unroll") for (int n = 0; n < 2; ++n) _Pragma("unroll") for (int k = 0; k < 2; ++k) \
;         acc[ai][bj][m][n] = __builtin_amdgcn_mfma_f32_16x16x32_bf16(Bt[n][k], At[m][k], acc[ai][bj][m][n], 0, 0, 0); __builtin_amdgcn_s_setprio(0); } while (0)
; #define PG8_WAIT_V(n) asm volatile("s_waitcnt vmcnt(" #n ")" ::: "memory")
; #define PG8_WAIT_L(n) asm volatile("s_waitcnt lgkmcnt(" #n ")" ::: "memory")
; #define PG8_BAR __builtin_amdgcn_s_barrier()
; #define PG8_SCHED __builtin_amdgcn_sched_barrier(0)
; template <class Epi, class Sched, bool ALIGN_EPI = false, bool SP2 = false, bool HALFM = false>
; __device__ __forceinline__ void gemm_phase(PG8_LAS unsigned char* lds, const Gemm g, const Sched& S, const Epi& E) {
;     ...
;             PG8_WAIT_V8R; PG8_WAIT_L(0); PG8_BAR; PG8_MMA(0, 0, At, B0); PG8_MMA(0, 1, At, B1); PG8_BAR; PG8_SCHED;
;             if constexpr (!HALFM) { PG8_LDA(At, 1, 1); } PG8_STAGE(PG8_SB(1, 0), b3, voffB); PG8_STAGE(PG8_SB(1, 1), b3 + hstep, voffB); PG8_STAGE(PG8_SA(1, 0), a3, voffA);
;             PG8_WAIT_V(8); PG8_WAIT_L(0); PG8_BAR; if constexpr (!HALFM) { PG8_MMA(1, 0, At, B0); PG8_MMA(1, 1, At, B1); } PG8_BAR; PG8_SCHED;
;             PG8_STAGE(PG8_SA(1, 1), a3 + hstepA, voffA);
.Lry2:
	s_waitcnt lgkmcnt(0)
	s_barrier
	s_setprio 1
	s_waitcnt lgkmcnt(0)
	v_mfma_f32_16x16x32_bf16 v[126:129], v[130:133], v[162:165], v[126:129]
	v_mfma_f32_16x16x32_bf16 v[126:129], v[134:137], v[166:169], v[126:129]
	v_mfma_f32_16x16x32_bf16 v[122:125], v[142:145], v[166:169], v[122:125]
	v_mfma_f32_16x16x32_bf16 v[122:125], v[138:141], v[162:165], v[122:125]
	v_mfma_f32_16x16x32_bf16 v[106:109], v[138:141], v[170:173], v[106:109]
	v_mfma_f32_16x16x32_bf16 v[106:109], v[142:145], v[174:177], v[106:109]
	v_mfma_f32_16x16x32_bf16 v[110:113], v[134:137], v[174:177], v[110:113]
	v_mfma_f32_16x16x32_bf16 v[110:113], v[130:133], v[170:173], v[110:113]
	v_mfma_f32_16x16x32_bf16 v[94:97], v[130:133], v[194:197], v[94:97]
	v_mfma_f32_16x16x32_bf16 v[94:97], v[134:137], v[198:201], v[94:97]
	v_mfma_f32_16x16x32_bf16 v[90:93], v[142:145], v[198:201], v[90:93]
	v_mfma_f32_16x16x32_bf16 v[90:93], v[138:141], v[194:197], v[90:93]
	v_mfma_f32_16x16x32_bf16 v[74:77], v[138:141], v[202:205], v[74:77]
	v_mfma_f32_16x16x32_bf16 v[74:77], v[142:145], v[206:209], v[74:77]
	v_mfma_f32_16x16x32_bf16 v[78:81], v[134:137], v[206:209], v[78:81]
	v_mfma_f32_16x16x32_bf16 v[78:81], v[130:133], v[202:205], v[78:81]
	s_setprio 0
	s_setprio 1
	v_mfma_f32_16x16x32_bf16 v[70:73], v[146:149], v[202:205], v[70:73]
	v_mfma_f32_16x16x32_bf16 v[70:73], v[150:153], v[206:209], v[70:73]
	v_mfma_f32_16x16x32_bf16 v[66:69], v[158:161], v[206:209], v[66:69]
	v_mfma_f32_16x16x32_bf16 v[66:69], v[154:157], v[202:205], v[66:69]
	v_mfma_f32_16x16x32_bf16 v[82:85], v[154:157], v[194:197], v[82:85]
	v_mfma_f32_16x16x32_bf16 v[82:85], v[158:161], v[198:201], v[82:85]
	v_mfma_f32_16x16x32_bf16 v[86:89], v[150:153], v[198:201], v[86:89]
	v_mfma_f32_16x16x32_bf16 v[86:89], v[146:149], v[194:197], v[86:89]
	v_mfma_f32_16x16x32_bf16 v[102:105], v[146:149], v[170:173], v[102:105]
	v_mfma_f32_16x16x32_bf16 v[102:105], v[150:153], v[174:177], v[102:105]
	v_mfma_f32_16x16x32_bf16 v[98:101], v[158:161], v[174:177], v[98:101]
	v_mfma_f32_16x16x32_bf16 v[98:101], v[154:157], v[170:173], v[98:101]
	v_mfma_f32_16x16x32_bf16 v[114:117], v[154:157], v[162:165], v[114:117]
	v_mfma_f32_16x16x32_bf16 v[114:117], v[158:161], v[166:169], v[114:117]
	v_mfma_f32_16x16x32_bf16 v[118:121], v[150:153], v[166:169], v[118:121]
	v_mfma_f32_16x16x32_bf16 v[118:121], v[146:149], v[162:165], v[118:121]
	s_setprio 0
	s_barrier
	s_add_u32 s86, s38, 0x8000
	s_addc_u32 s87, s39, 0
	s_add_i32 s88, s89, s41
	s_mov_b32 m0, s88
	ds_read_b128 v[162:165], v218 offset:49152
	ds_read_b128 v[166:169], v218 offset:50176
	ds_read_b128 v[170:173], v218 offset:51200
	ds_read_b128 v[174:177], v218 offset:52224
	ds_read_b128 v[194:197], v218 offset:53248
	ds_read_b128 v[198:201], v218 offset:54272
	ds_read_b128 v[202:205], v218 offset:55296
	ds_read_b128 v[206:209], v218 offset:56320
	s_nop 0
	global_load_lds_dwordx4 v221, s[86:87]
	s_add_i32 m0, s88, 0x2000
	s_add_u32 s38, s38, 0xc000
	global_load_lds_dwordx4 v181, s[86:87]
	s_addc_u32 s39, s39, 0
	s_add_i32 s86, s90, s41
	s_mov_b32 m0, s86
	s_nop 0
	global_load_lds_dwordx4 v221, s[38:39]
	s_add_i32 m0, s86, 0x2000
	s_nop 0
	global_load_lds_dwordx4 v181, s[38:39]
	s_mov_b32 m0, s56
	s_nop 0
	global_load_lds_dwordx4 v221, s[10:11]
	s_mov_b32 m0, s57
	s_nop 0
	global_load_lds_dwordx4 v181, s[10:11]
	s_waitcnt vmcnt(8)
	s_waitcnt lgkmcnt(0)
	s_barrier
	s_setprio 1
	s_waitcnt lgkmcnt(0)
	v_mfma_f32_16x16x32_bf16 v[62:65], v[130:133], v[162:165], v[62:65]
	v_mfma_f32_16x16x32_bf16 v[62:65], v[134:137], v[166:169], v[62:65]
	v_mfma_f32_16x16x32_bf16 v[58:61], v[142:145], v[166:169], v[58:61]
	v_mfma_f32_16x16x32_bf16 v[58:61], v[138:141], v[162:165], v[58:61]
	v_mfma_f32_16x16x32_bf16 v[42:45], v[138:141], v[170:173], v[42:45]
	v_mfma_f32_16x16x32_bf16 v[42:45], v[142:145], v[174:177], v[42:45]
	v_mfma_f32_16x16x32_bf16 v[46:49], v[134:137], v[174:177], v[46:49]
	v_mfma_f32_16x16x32_bf16 v[46:49], v[130:133], v[170:173], v[46:49]
	v_mfma_f32_16x16x32_bf16 v[30:33], v[130:133], v[194:197], v[30:33]
	v_mfma_f32_16x16x32_bf16 v[30:33], v[134:137], v[198:201], v[30:33]
	v_mfma_f32_16x16x32_bf16 v[26:29], v[142:145], v[198:201], v[26:29]
	v_mfma_f32_16x16x32_bf16 v[26:29], v[138:141], v[194:197], v[26:29]
	v_mfma_f32_16x16x32_bf16 v[10:13], v[138:141], v[202:205], v[10:13]
	v_mfma_f32_16x16x32_bf16 v[10:13], v[142:145], v[206:209], v[10:13]
	v_mfma_f32_16x16x32_bf16 v[14:17], v[134:137], v[206:209], v[14:17]
	v_mfma_f32_16x16x32_bf16 v[14:17], v[130:133], v[202:205], v[14:17]
	s_setprio 0
	s_setprio 1
	v_mfma_f32_16x16x32_bf16 v[6:9], v[146:149], v[202:205], v[6:9]
	v_mfma_f32_16x16x32_bf16 v[6:9], v[150:153], v[206:209], v[6:9]
	v_mfma_f32_16x16x32_bf16 v[2:5], v[158:161], v[206:209], v[2:5]
	v_mfma_f32_16x16x32_bf16 v[2:5], v[154:157], v[202:205], v[2:5]
	v_mfma_f32_16x16x32_bf16 v[18:21], v[154:157], v[194:197], v[18:21]
	v_mfma_f32_16x16x32_bf16 v[18:21], v[158:161], v[198:201], v[18:21]
	v_mfma_f32_16x16x32_bf16 v[22:25], v[150:153], v[198:201], v[22:25]
	v_mfma_f32_16x16x32_bf16 v[22:25], v[146:149], v[194:197], v[22:25]
	v_mfma_f32_16x16x32_bf16 v[38:41], v[146:149], v[170:173], v[38:41]
	v_mfma_f32_16x16x32_bf16 v[38:41], v[150:153], v[174:177], v[38:41]
	v_mfma_f32_16x16x32_bf16 v[34:37], v[158:161], v[174:177], v[34:37]
	v_mfma_f32_16x16x32_bf16 v[34:37], v[154:157], v[170:173], v[34:37]
	v_mfma_f32_16x16x32_bf16 v[50:53], v[154:157], v[162:165], v[50:53]
	v_mfma_f32_16x16x32_bf16 v[50:53], v[158:161], v[166:169], v[50:53]
	v_mfma_f32_16x16x32_bf16 v[54:57], v[150:153], v[166:169], v[54:57]
	v_mfma_f32_16x16x32_bf16 v[54:57], v[146:149], v[162:165], v[54:57]
	s_setprio 0
	s_barrier
	s_add_u32 s0, s0, 0xc000
	s_mov_b32 m0, s58
	s_addc_u32 s1, s1, 0
	s_add_i32 s81, s81, 2
	global_load_lds_dwordx4 v221, s[0:1]
	s_mov_b32 m0, s59
	s_add_u32 s33, s33, 0x10000
	global_load_lds_dwordx4 v181, s[0:1]
	s_addc_u32 s65, s65, 0
	s_add_u32 s66, s66, 0x10000
	s_addc_u32 s67, s67, 0
	s_cmp_gt_u32 s81, 61
	s_cbranch_scc0 .LBB0_248
	s_and_b64 vcc, exec, s[20:21]
	s_cbranch_vccz .LBB0_253
	s_barrier
	s_mov_b64 s[0:1], -1
	s_cmp_gt_u32 s36, 7
	v_lshl_add_u32 v194, s8, 8, v183
	s_cbranch_scc1 .LBB0_254

; #define PG8_STAGE(bufoff, gbase, voff) do { const char* _gb = (const char*)(gbase); asm volatile("" : "+s"(_gb)); _Pragma("unroll") for (int _i = 0; _i < 2; ++_i) \
;         __builtin_amdgcn_global_load_lds((const unsigned*)(_gb + (voff)[_i]), (PG8_LAS unsigned*)(lds + (bufoff) + ldsw + _i * 8192), 16, 0, 0); } while (0)
; #define PG8_LDA(dst, b, h) do { _Pragma("unroll") for (int m = 0; m < 4; ++m) _Pragma("unroll") for (int k = 0; k < 2; ++k) dst[m][k] = *(const PG8_LAS bf16x8*)(lds + PG8_SA(b, h) + aoff + m * 2048 + k * 1024); } while (0)
; #define PG8_MMA(ai, bj, At, Bt) do { __builtin_amdgcn_s_setprio(1); _Pragma("unroll") for (int m = 0; m < 4; ++m) _Pragma("unroll") for (int n = 0; n < 2; ++n) _Pragma("unroll") for (int k = 0; k < 2; ++k) \
;         acc[ai][bj][m][n] = __builtin_amdgcn_mfma_f32_16x16x32_bf16(Bt[n][k], At[m][k], acc[ai][bj][m][n], 0, 0, 0); __builtin_amdgcn_s_setprio(0); } while (0)
; #define PG8_WAIT_L(n) asm volatile("s_waitcnt lgkmcnt(" #n ")" ::: "memory")
; #define PG8_BAR __builtin_amdgcn_s_barrier()
; #define PG8_SCHED __builtin_amdgcn_sched_barrier(0)
; template <class Epi, class Sched, bool ALIGN_EPI = false, bool SP2 = false, bool HALFM = false>
; __device__ __forceinline__ void gemm_phase(PG8_LAS unsigned char* lds, const Gemm g, const Sched& S, const Epi& E) {
;     ...
;             PG8_WAIT_V8R; PG8_WAIT_L(0); PG8_BAR; PG8_MMA(0, 0, At, B0); PG8_MMA(0, 1, At, B1); PG8_BAR; PG8_SCHED;
;             if constexpr (!HALFM) { PG8_LDA(At, 0, 1); } PG8_STAGE(PG8_SB(0, 0), b2, voffB); PG8_STAGE(PG8_SB(0, 1), b2 + hstep, voffB); PG8_STAGE(PG8_SA(0, 0), a2, voffA);
;             PG8_WAIT_V8R; PG8_WAIT_L(0); PG8_BAR; if constexpr (!HALFM) { PG8_MMA(1, 0, At, B0); PG8_MMA(1, 1, At, B1); } PG8_BAR; PG8_SCHED;
.Lry3:
	s_waitcnt lgkmcnt(0)
	s_barrier
	s_setprio 1
	s_waitcnt lgkmcnt(0)
	v_mfma_f32_16x16x32_bf16 v[126:129], v[130:133], v[162:165], v[126:129]
	v_mfma_f32_16x16x32_bf16 v[126:129], v[134:137], v[166:169], v[126:129]
	v_mfma_f32_16x16x32_bf16 v[122:125], v[142:145], v[166:169], v[122:125]
	v_mfma_f32_16x16x32_bf16 v[122:125], v[138:141], v[162:165], v[122:125]
	v_mfma_f32_16x16x32_bf16 v[106:109], v[138:141], v[174:177], v[106:109]
	v_mfma_f32_16x16x32_bf16 v[106:109], v[142:145], v[178:181], v[106:109]
	v_mfma_f32_16x16x32_bf16 v[110:113], v[134:137], v[178:181], v[110:113]
	v_mfma_f32_16x16x32_bf16 v[110:113], v[130:133], v[174:177], v[110:113]
	v_mfma_f32_16x16x32_bf16 v[94:97], v[130:133], v[182:185], v[94:97]
	v_mfma_f32_16x16x32_bf16 v[94:97], v[134:137], v[186:189], v[94:97]
	v_mfma_f32_16x16x32_bf16 v[90:93], v[142:145], v[186:189], v[90:93]
	v_mfma_f32_16x16x32_bf16 v[90:93], v[138:141], v[182:185], v[90:93]
	v_mfma_f32_16x16x32_bf16 v[74:77], v[138:141], v[190:193], v[74:77]
	v_mfma_f32_16x16x32_bf16 v[74:77], v[142:145], v[194:197], v[74:77]
	v_mfma_f32_16x16x32_bf16 v[78:81], v[134:137], v[194:197], v[78:81]
	v_mfma_f32_16x16x32_bf16 v[78:81], v[130:133], v[190:193], v[78:81]
	s_setprio 0
	s_setprio 1
	v_mfma_f32_16x16x32_bf16 v[70:73], v[146:149], v[190:193], v[70:73]
	v_mfma_f32_16x16x32_bf16 v[70:73], v[150:153], v[194:197], v[70:73]
	v_mfma_f32_16x16x32_bf16 v[66:69], v[158:161], v[194:197], v[66:69]
	v_mfma_f32_16x16x32_bf16 v[66:69], v[154:157], v[190:193], v[66:69]
	v_mfma_f32_16x16x32_bf16 v[82:85], v[154:157], v[182:185], v[82:85]
	v_mfma_f32_16x16x32_bf16 v[82:85], v[158:161], v[186:189], v[82:85]
	v_mfma_f32_16x16x32_bf16 v[86:89], v[150:153], v[186:189], v[86:89]
	v_mfma_f32_16x16x32_bf16 v[86:89], v[146:149], v[182:185], v[86:89]
	v_mfma_f32_16x16x32_bf16 v[102:105], v[146:149], v[174:177], v[102:105]
	v_mfma_f32_16x16x32_bf16 v[102:105], v[150:153], v[178:181], v[102:105]
	v_mfma_f32_16x16x32_bf16 v[98:101], v[158:161], v[178:181], v[98:101]
	v_mfma_f32_16x16x32_bf16 v[98:101], v[154:157], v[174:177], v[98:101]
	v_mfma_f32_16x16x32_bf16 v[114:117], v[154:157], v[162:165], v[114:117]
	v_mfma_f32_16x16x32_bf16 v[114:117], v[158:161], v[166:169], v[114:117]
	v_mfma_f32_16x16x32_bf16 v[118:121], v[150:153], v[166:169], v[118:121]
	v_mfma_f32_16x16x32_bf16 v[118:121], v[146:149], v[162:165], v[118:121]
	s_setprio 0
	s_barrier
	s_add_i32 s65, s54, s3
	s_mov_b64 s[62:63], s[34:35]
	s_mov_b32 m0, s65
	ds_read_b128 v[162:165], v210 offset:16384
	ds_read_b128 v[166:169], v210 offset:17408
	ds_read_b128 v[174:177], v210 offset:18432
	ds_read_b128 v[178:181], v210 offset:19456
	ds_read_b128 v[182:185], v210 offset:20480
	ds_read_b128 v[186:189], v210 offset:21504
	ds_read_b128 v[190:193], v210 offset:22528
	ds_read_b128 v[194:197], v210 offset:23552
	s_nop 0
	global_load_lds_dwordx4 v170, s[62:63]
	s_add_i32 m0, s65, 0x2000
	s_nop 0
	global_load_lds_dwordx4 v171, s[62:63]
	s_add_u32 s62, s34, 0x4000
	s_addc_u32 s63, s35, 0
	s_add_i32 s65, s55, s3
	s_mov_b32 m0, s65
	s_nop 0
	global_load_lds_dwordx4 v170, s[62:63]
	s_add_i32 m0, s65, 0x2000
	s_nop 0
	global_load_lds_dwordx4 v171, s[62:63]
	s_mov_b64 s[62:63], s[28:29]
	s_mov_b32 m0, s25
	s_nop 0
	global_load_lds_dwordx4 v170, s[62:63]
	s_mov_b32 m0, s27
	s_nop 0
	global_load_lds_dwordx4 v171, s[62:63]
	s_cmp_eq_u32 s64, 0
	s_cbranch_scc1 .Lrx4
	s_waitcnt vmcnt(40)
	s_branch .Lry4

; #define PG8_STAGE(bufoff, gbase, voff) do { const char* _gb = (const char*)(gbase); asm volatile("" : "+s"(_gb)); _Pragma("unroll") for (int _i = 0; _i < 2; ++_i) \
;         __builtin_amdgcn_global_load_lds((const unsigned*)(_gb + (voff)[_i]), (PG8_LAS unsigned*)(lds + (bufoff) + ldsw + _i * 8192), 16, 0, 0); } while (0)
; #define PG8_LDA(dst, b, h) do { _Pragma("unroll") for (int m = 0; m < 4; ++m) _Pragma("unroll") for (int k = 0; k < 2; ++k) dst[m][k] = *(const PG8_LAS bf16x8*)(lds + PG8_SA(b, h) + aoff + m * 2048 + k * 1024); } while (0)
; #define PG8_LDB(dst, b, h) do { _Pragma("unroll") for (int n = 0; n < 2; ++n) _Pragma("unroll") for (int k = 0; k < 2; ++k) dst[n][k] = *(const PG8_LAS bf16x8*)(lds + PG8_SB(b, h) + boff + n * 2048 + k * 1024); } while (0)
; #define PG8_MMA(ai, bj, At, Bt) do { __builtin_amdgcn_s_setprio(1); _Pragma("unroll") for (int m = 0; m < 4; ++m) _Pragma("unroll") for (int n = 0; n < 2; ++n) _Pragma("unroll") for (int k = 0; k < 2; ++k) \
;         acc[ai][bj][m][n] = __builtin_amdgcn_mfma_f32_16x16x32_bf16(Bt[n][k], At[m][k], acc[ai][bj][m][n], 0, 0, 0); __builtin_amdgcn_s_setprio(0); } while (0)
; #define PG8_WAIT_L(n) asm volatile("s_waitcnt lgkmcnt(" #n ")" ::: "memory")
; #define PG8_BAR __builtin_amdgcn_s_barrier()
; #define PG8_SCHED __builtin_amdgcn_sched_barrier(0)
; template <class Epi, class Sched, bool ALIGN_EPI = false, bool SP2 = false, bool HALFM = false>
; __device__ __forceinline__ void gemm_phase(PG8_LAS unsigned char* lds, const Gemm g, const Sched& S, const Epi& E) {
;     ...
;             PG8_WAIT_V8R; PG8_WAIT_L(0); PG8_BAR; if constexpr (!HALFM) { PG8_MMA(1, 0, At, B0); PG8_MMA(1, 1, At, B1); } PG8_BAR; PG8_SCHED;
;             PG8_LDB(B0, 1, 0); PG8_LDB(B1, 1, 1); PG8_SCHED; PG8_LDA(At, 1, 0); PG8_STAGE(PG8_SA(0, 1), a2 + hstepA, voffA);
;             PG8_WAIT_V8R; PG8_WAIT_L(0); PG8_BAR; PG8_MMA(0, 0, At, B0); PG8_MMA(0, 1, At, B1); PG8_BAR; PG8_SCHED;
.Lry4:
	s_waitcnt lgkmcnt(0)
	s_barrier
	s_setprio 1
	s_waitcnt lgkmcnt(0)
	v_mfma_f32_16x16x32_bf16 v[62:65], v[130:133], v[162:165], v[62:65]
	v_mfma_f32_16x16x32_bf16 v[62:65], v[134:137], v[166:169], v[62:65]
	v_mfma_f32_16x16x32_bf16 v[58:61], v[142:145], v[166:169], v[58:61]
	v_mfma_f32_16x16x32_bf16 v[58:61], v[138:141], v[162:165], v[58:61]
	v_mfma_f32_16x16x32_bf16 v[42:45], v[138:141], v[174:177], v[42:45]
	v_mfma_f32_16x16x32_bf16 v[42:45], v[142:145], v[178:181], v[42:45]
	v_mfma_f32_16x16x32_bf16 v[46:49], v[134:137], v[178:181], v[46:49]
	v_mfma_f32_16x16x32_bf16 v[46:49], v[130:133], v[174:177], v[46:49]
	v_mfma_f32_16x16x32_bf16 v[30:33], v[130:133], v[182:185], v[30:33]
	v_mfma_f32_16x16x32_bf16 v[30:33], v[134:137], v[186:189], v[30:33]
	v_mfma_f32_16x16x32_bf16 v[26:29], v[142:145], v[186:189], v[26:29]
	v_mfma_f32_16x16x32_bf16 v[26:29], v[138:141], v[182:185], v[26:29]
	v_mfma_f32_16x16x32_bf16 v[10:13], v[138:141], v[190:193], v[10:13]
	v_mfma_f32_16x16x32_bf16 v[10:13], v[142:145], v[194:197], v[10:13]
	v_mfma_f32_16x16x32_bf16 v[14:17], v[134:137], v[194:197], v[14:17]
	v_mfma_f32_16x16x32_bf16 v[14:17], v[130:133], v[190:193], v[14:17]
	s_setprio 0
	s_setprio 1
	v_mfma_f32_16x16x32_bf16 v[6:9], v[146:149], v[190:193], v[6:9]
	v_mfma_f32_16x16x32_bf16 v[6:9], v[150:153], v[194:197], v[6:9]
	v_mfma_f32_16x16x32_bf16 v[2:5], v[158:161], v[194:197], v[2:5]
	v_mfma_f32_16x16x32_bf16 v[2:5], v[154:157], v[190:193], v[2:5]
	v_mfma_f32_16x16x32_bf16 v[18:21], v[154:157], v[182:185], v[18:21]
	v_mfma_f32_16x16x32_bf16 v[18:21], v[158:161], v[186:189], v[18:21]
	v_mfma_f32_16x16x32_bf16 v[22:25], v[150:153], v[186:189], v[22:25]
	v_mfma_f32_16x16x32_bf16 v[22:25], v[146:149], v[182:185], v[22:25]
	v_mfma_f32_16x16x32_bf16 v[38:41], v[146:149], v[174:177], v[38:41]
	v_mfma_f32_16x16x32_bf16 v[38:41], v[150:153], v[178:181], v[38:41]
	v_mfma_f32_16x16x32_bf16 v[34:37], v[158:161], v[178:181], v[34:37]
	v_mfma_f32_16x16x32_bf16 v[34:37], v[154:157], v[174:177], v[34:37]
	v_mfma_f32_16x16x32_bf16 v[50:53], v[154:157], v[162:165], v[50:53]
	v_mfma_f32_16x16x32_bf16 v[50:53], v[158:161], v[166:169], v[50:53]
	v_mfma_f32_16x16x32_bf16 v[54:57], v[150:153], v[166:169], v[54:57]
	v_mfma_f32_16x16x32_bf16 v[54:57], v[146:149], v[162:165], v[54:57]
	s_setprio 0
	s_barrier
	s_add_i32 s65, 0, 0x18000
	s_add_i32 s70, 0, 0x1c000
	v_add_u32_e32 v142, s65, v205
	v_add_u32_e32 v158, s70, v205
	ds_read_b128 v[130:133], v142
	ds_read_b128 v[134:137], v142 offset:1024
	ds_read_b128 v[138:141], v142 offset:2048
	ds_read_b128 v[142:145], v142 offset:3072
	ds_read_b128 v[146:149], v158
	ds_read_b128 v[150:153], v158 offset:1024
	ds_read_b128 v[154:157], v158 offset:2048
	ds_read_b128 v[158:161], v158 offset:3072
	s_add_u32 s62, s28, 0x4000
	s_addc_u32 s63, s29, 0
	s_mov_b32 m0, s39
	ds_read_b128 v[162:165], v210 offset:32768
	ds_read_b128 v[166:169], v210 offset:33792
	ds_read_b128 v[174:177], v210 offset:34816
	ds_read_b128 v[178:181], v210 offset:35840
	ds_read_b128 v[182:185], v210 offset:36864
	ds_read_b128 v[186:189], v210 offset:37888
	ds_read_b128 v[190:193], v210 offset:38912
	ds_read_b128 v[194:197], v210 offset:39936
	s_nop 0
	global_load_lds_dwordx4 v170, s[62:63]
	s_mov_b32 m0, s40
	s_nop 0
	global_load_lds_dwordx4 v171, s[62:63]
	s_cmp_eq_u32 s64, 0
	s_cbranch_scc1 .Lrx5
	s_waitcnt vmcnt(40)
	s_branch .Lry5

; #define PG8_STAGE(bufoff, gbase, voff) do { const char* _gb = (const char*)(gbase); asm volatile("" : "+s"(_gb)); _Pragma("unroll") for (int _i = 0; _i < 2; ++_i) \
;         __builtin_amdgcn_global_load_lds((const unsigned*)(_gb + (voff)[_i]), (PG8_LAS unsigned*)(lds + (bufoff) + ldsw + _i * 8192), 16, 0, 0); } while (0)
; #define PG8_LDA(dst, b, h) do { _Pragma("unroll") for (int m = 0; m < 4; ++m) _Pragma("unroll") for (int k = 0; k < 2; ++k) dst[m][k] = *(const PG8_LAS bf16x8*)(lds + PG8_SA(b, h) + aoff + m * 2048 + k * 1024); } while (0)
; #define PG8_MMA(ai, bj, At, Bt) do { __builtin_amdgcn_s_setprio(1); _Pragma("unroll") for (int m = 0; m < 4; ++m) _Pragma("unroll") for (int n = 0; n < 2; ++n) _Pragma("unroll") for (int k = 0; k < 2; ++k) \
;         acc[ai][bj][m][n] = __builtin_amdgcn_mfma_f32_16x16x32_bf16(Bt[n][k], At[m][k], acc[ai][bj][m][n], 0, 0, 0); __builtin_amdgcn_s_setprio(0); } while (0)
; #define PG8_WAIT_V(n) asm volatile("s_waitcnt vmcnt(" #n ")" ::: "memory")
; #define PG8_WAIT_L(n) asm volatile("s_waitcnt lgkmcnt(" #n ")" ::: "memory")
; #define PG8_BAR __builtin_amdgcn_s_barrier()
; #define PG8_SCHED __builtin_amdgcn_sched_barrier(0)
; template <class Epi, class Sched, bool ALIGN_EPI = false, bool SP2 = false, bool HALFM = false>
; __device__ __forceinline__ void gemm_phase(PG8_LAS unsigned char* lds, const Gemm g, const Sched& S, const Epi& E) {
;     ...
;             PG8_WAIT_V8R; PG8_WAIT_L(0); PG8_BAR; PG8_MMA(0, 0, At, B0); PG8_MMA(0, 1, At, B1); PG8_BAR; PG8_SCHED;
;             if constexpr (!HALFM) { PG8_LDA(At, 1, 1); } PG8_STAGE(PG8_SB(1, 0), b3, voffB); PG8_STAGE(PG8_SB(1, 1), b3 + hstep, voffB); PG8_STAGE(PG8_SA(1, 0), a3, voffA);
;             PG8_WAIT_V(8); PG8_WAIT_L(0); PG8_BAR; if constexpr (!HALFM) { PG8_MMA(1, 0, At, B0); PG8_MMA(1, 1, At, B1); } PG8_BAR; PG8_SCHED;
;             PG8_STAGE(PG8_SA(1, 1), a3 + hstepA, voffA);
.Lry5:
	s_waitcnt lgkmcnt(0)
	s_barrier
	s_setprio 1
	s_waitcnt lgkmcnt(0)
	v_mfma_f32_16x16x32_bf16 v[126:129], v[130:133], v[162:165], v[126:129]
	v_mfma_f32_16x16x32_bf16 v[126:129], v[134:137], v[166:169], v[126:129]
	v_mfma_f32_16x16x32_bf16 v[122:125], v[142:145], v[166:169], v[122:125]
	v_mfma_f32_16x16x32_bf16 v[122:125], v[138:141], v[162:165], v[122:125]
	v_mfma_f32_16x16x32_bf16 v[106:109], v[138:141], v[174:177], v[106:109]
	v_mfma_f32_16x16x32_bf16 v[106:109], v[142:145], v[178:181], v[106:109]
	v_mfma_f32_16x16x32_bf16 v[110:113], v[134:137], v[178:181], v[110:113]
	v_mfma_f32_16x16x32_bf16 v[110:113], v[130:133], v[174:177], v[110:113]
	v_mfma_f32_16x16x32_bf16 v[94:97], v[130:133], v[182:185], v[94:97]
	v_mfma_f32_16x16x32_bf16 v[94:97], v[134:137], v[186:189], v[94:97]
	v_mfma_f32_16x16x32_bf16 v[90:93], v[142:145], v[186:189], v[90:93]
	v_mfma_f32_16x16x32_bf16 v[90:93], v[138:141], v[182:185], v[90:93]
	v_mfma_f32_16x16x32_bf16 v[74:77], v[138:141], v[190:193], v[74:77]
	v_mfma_f32_16x16x32_bf16 v[74:77], v[142:145], v[194:197], v[74:77]
	v_mfma_f32_16x16x32_bf16 v[78:81], v[134:137], v[194:197], v[78:81]
	v_mfma_f32_16x16x32_bf16 v[78:81], v[130:133], v[190:193], v[78:81]
	s_setprio 0
	s_setprio 1
	v_mfma_f32_16x16x32_bf16 v[70:73], v[146:149], v[190:193], v[70:73]
	v_mfma_f32_16x16x32_bf16 v[70:73], v[150:153], v[194:197], v[70:73]
	v_mfma_f32_16x16x32_bf16 v[66:69], v[158:161], v[194:197], v[66:69]
	v_mfma_f32_16x16x32_bf16 v[66:69], v[154:157], v[190:193], v[66:69]
	v_mfma_f32_16x16x32_bf16 v[82:85], v[154:157], v[182:185], v[82:85]
	v_mfma_f32_16x16x32_bf16 v[82:85], v[158:161], v[186:189], v[82:85]
	v_mfma_f32_16x16x32_bf16 v[86:89], v[150:153], v[186:189], v[86:89]
	v_mfma_f32_16x16x32_bf16 v[86:89], v[146:149], v[182:185], v[86:89]
	v_mfma_f32_16x16x32_bf16 v[102:105], v[146:149], v[174:177], v[102:105]
	v_mfma_f32_16x16x32_bf16 v[102:105], v[150:153], v[178:181], v[102:105]
	v_mfma_f32_16x16x32_bf16 v[98:101], v[158:161], v[178:181], v[98:101]
	v_mfma_f32_16x16x32_bf16 v[98:101], v[154:157], v[174:177], v[98:101]
	v_mfma_f32_16x16x32_bf16 v[114:117], v[154:157], v[162:165], v[114:117]
	v_mfma_f32_16x16x32_bf16 v[114:117], v[158:161], v[166:169], v[114:117]
	v_mfma_f32_16x16x32_bf16 v[118:121], v[150:153], v[166:169], v[118:121]
	v_mfma_f32_16x16x32_bf16 v[118:121], v[146:149], v[162:165], v[118:121]
	s_setprio 0
	s_barrier
	s_add_u32 s62, s34, 0x8000
	s_addc_u32 s63, s35, 0
	s_add_i32 s64, s65, s3
	s_mov_b32 m0, s64
	ds_read_b128 v[162:165], v210 offset:49152
	ds_read_b128 v[166:169], v210 offset:50176
	ds_read_b128 v[174:177], v210 offset:51200
	ds_read_b128 v[178:181], v210 offset:52224
	ds_read_b128 v[182:185], v210 offset:53248
	ds_read_b128 v[186:189], v210 offset:54272
	ds_read_b128 v[190:193], v210 offset:55296
	ds_read_b128 v[194:197], v210 offset:56320
	s_nop 0
	global_load_lds_dwordx4 v170, s[62:63]
	s_add_i32 m0, s64, 0x2000
	s_add_u32 s34, s34, 0xc000
	global_load_lds_dwordx4 v171, s[62:63]
	s_addc_u32 s35, s35, 0
	s_add_i32 s62, s70, s3
	s_mov_b32 m0, s62
	s_nop 0
	global_load_lds_dwordx4 v170, s[34:35]
	s_add_i32 m0, s62, 0x2000
	s_nop 0
	global_load_lds_dwordx4 v171, s[34:35]
	s_mov_b32 m0, s45
	s_nop 0
	global_load_lds_dwordx4 v170, s[30:31]
	s_mov_b32 m0, s46
	s_nop 0
	global_load_lds_dwordx4 v171, s[30:31]
	s_waitcnt vmcnt(8)
	s_waitcnt lgkmcnt(0)
	s_barrier
	s_setprio 1
	s_waitcnt lgkmcnt(0)
	v_mfma_f32_16x16x32_bf16 v[62:65], v[130:133], v[162:165], v[62:65]
	v_mfma_f32_16x16x32_bf16 v[62:65], v[134:137], v[166:169], v[62:65]
	v_mfma_f32_16x16x32_bf16 v[58:61], v[142:145], v[166:169], v[58:61]
	v_mfma_f32_16x16x32_bf16 v[58:61], v[138:141], v[162:165], v[58:61]
	v_mfma_f32_16x16x32_bf16 v[42:45], v[138:141], v[174:177], v[42:45]
	v_mfma_f32_16x16x32_bf16 v[42:45], v[142:145], v[178:181], v[42:45]
	v_mfma_f32_16x16x32_bf16 v[46:49], v[134:137], v[178:181], v[46:49]
	v_mfma_f32_16x16x32_bf16 v[46:49], v[130:133], v[174:177], v[46:49]
	v_mfma_f32_16x16x32_bf16 v[30:33], v[130:133], v[182:185], v[30:33]
	v_mfma_f32_16x16x32_bf16 v[30:33], v[134:137], v[186:189], v[30:33]
	v_mfma_f32_16x16x32_bf16 v[26:29], v[142:145], v[186:189], v[26:29]
	v_mfma_f32_16x16x32_bf16 v[26:29], v[138:141], v[182:185], v[26:29]
	v_mfma_f32_16x16x32_bf16 v[10:13], v[138:141], v[190:193], v[10:13]
	v_mfma_f32_16x16x32_bf16 v[10:13], v[142:145], v[194:197], v[10:13]
	v_mfma_f32_16x16x32_bf16 v[14:17], v[134:137], v[194:197], v[14:17]
	v_mfma_f32_16x16x32_bf16 v[14:17], v[130:133], v[190:193], v[14:17]
	s_setprio 0
	s_setprio 1
	v_mfma_f32_16x16x32_bf16 v[6:9], v[146:149], v[190:193], v[6:9]
	v_mfma_f32_16x16x32_bf16 v[6:9], v[150:153], v[194:197], v[6:9]
	v_mfma_f32_16x16x32_bf16 v[2:5], v[158:161], v[194:197], v[2:5]
	v_mfma_f32_16x16x32_bf16 v[2:5], v[154:157], v[190:193], v[2:5]
	v_mfma_f32_16x16x32_bf16 v[18:21], v[154:157], v[182:185], v[18:21]
	v_mfma_f32_16x16x32_bf16 v[18:21], v[158:161], v[186:189], v[18:21]
	v_mfma_f32_16x16x32_bf16 v[22:25], v[150:153], v[186:189], v[22:25]
	v_mfma_f32_16x16x32_bf16 v[22:25], v[146:149], v[182:185], v[22:25]
	v_mfma_f32_16x16x32_bf16 v[38:41], v[146:149], v[174:177], v[38:41]
	v_mfma_f32_16x16x32_bf16 v[38:41], v[150:153], v[178:181], v[38:41]
	v_mfma_f32_16x16x32_bf16 v[34:37], v[158:161], v[178:181], v[34:37]
	v_mfma_f32_16x16x32_bf16 v[34:37], v[154:157], v[174:177], v[34:37]
	v_mfma_f32_16x16x32_bf16 v[50:53], v[154:157], v[162:165], v[50:53]
	v_mfma_f32_16x16x32_bf16 v[50:53], v[158:161], v[166:169], v[50:53]
	v_mfma_f32_16x16x32_bf16 v[54:57], v[150:153], v[166:169], v[54:57]
	v_mfma_f32_16x16x32_bf16 v[54:57], v[146:149], v[162:165], v[54:57]
	s_setprio 0
	s_barrier
	s_add_u32 s28, s28, 0xc000
	s_mov_b32 m0, s47
	s_addc_u32 s29, s29, 0
	s_add_i32 s69, s69, 2
	global_load_lds_dwordx4 v170, s[28:29]
	s_mov_b32 m0, s48
	s_add_u32 s61, s61, 0x10000
	global_load_lds_dwordx4 v171, s[28:29]
	s_addc_u32 s66, s66, 0
	s_add_u32 s67, s67, 0x10000
	s_addc_u32 s68, s68, 0
	s_cmp_gt_u32 s69, 61
	s_cbranch_scc0 .LBB0_805
	s_and_b64 vcc, exec, s[12:13]
	s_cbranch_vccz .LBB0_808
	s_barrier

; #define PG8_STAGE(bufoff, gbase, voff) do { const char* _gb = (const char*)(gbase); asm volatile("" : "+s"(_gb)); _Pragma("unroll") for (int _i = 0; _i < 2; ++_i) \
;         __builtin_amdgcn_global_load_lds((const unsigned*)(_gb + (voff)[_i]), (PG8_LAS unsigned*)(lds + (bufoff) + ldsw + _i * 8192), 16, 0, 0); } while (0)
; #define PG8_LDA(dst, b, h) do { _Pragma("unroll") for (int m = 0; m < 4; ++m) _Pragma("unroll") for (int k = 0; k < 2; ++k) dst[m][k] = *(const PG8_LAS bf16x8*)(lds + PG8_SA(b, h) + aoff + m * 2048 + k * 1024); } while (0)
; #define PG8_LDB(dst, b, h) do { _Pragma("unroll") for (int n = 0; n < 2; ++n) _Pragma("unroll") for (int k = 0; k < 2; ++k) dst[n][k] = *(const PG8_LAS bf16x8*)(lds + PG8_SB(b, h) + boff + n * 2048 + k * 1024); } while (0)
; template <class Epi, class Sched, bool ALIGN_EPI = false, bool SP2 = false, bool HALFM = false>
; __device__ __forceinline__ void gemm_phase(PG8_LAS unsigned char* lds, const Gemm g, const Sched& S, const Epi& E) {
;     ...
;         for (int t = 0; t < nt; t += 2) {
;             const bool last = (t == nt - 2);
;             const char* a1 = cA + (size_t)(t + 1) * kstep;
;             const char* a2 = last ? nA : cA + (size_t)(t + 2) * kstep; const char* b2 = last ? nB : cB + (size_t)(t + 2) * kstep;
;             const char* a3 = a2 + kstep; const char* b3 = b2 + kstep;
;             if (last && has_next) S.a_ready(nxt);
;             if constexpr (Epi::HAS_PREFETCH) { if (last) E.prefetch(cur, wid, lane); }
;             asm volatile("" : "+v"(voffA[0]), "+v"(voffA[1])); voffB[0] = voffA[0]; voffB[1] = voffA[1];
;             if constexpr (SP2) {
;             PG8_LDB(B0, 0, 0); PG8_LDB(B1, 0, 1); PG8_SCHED; PG8_LDA(At, 0, 0);
;             PG8_WAIT_V8R; PG8_WAIT_L(0); PG8_BAR; PG8_MMA(0, 0, At, B0); PG8_MMA(0, 1, At, B1); PG8_BAR; PG8_SCHED;
;             if constexpr (!HALFM) { PG8_LDA(At, 0, 1); } PG8_STAGE(PG8_SB(0, 0), b2, voffB); PG8_STAGE(PG8_SB(0, 1), b2 + hstep, voffB); PG8_STAGE(PG8_SA(0, 0), a2, voffA);
;             PG8_WAIT_V8R; PG8_WAIT_L(0); PG8_BAR; if constexpr (!HALFM) { PG8_MMA(1, 0, At, B0); PG8_MMA(1, 1, At, B1); } PG8_BAR; PG8_SCHED;
;             PG8_LDB(B0, 1, 0); PG8_LDB(B1, 1, 1); PG8_SCHED; PG8_LDA(At, 1, 0); PG8_STAGE(PG8_SA(0, 1), a2 + hstepA, voffA);
;             PG8_WAIT_V8R; PG8_WAIT_L(0); PG8_BAR; PG8_MMA(0, 0, At, B0); PG8_MMA(0, 1, At, B1); PG8_BAR; PG8_SCHED;
.LBB0_901:
	ds_read_b128 v[134:137], v149
	ds_read_b128 v[138:141], v149 offset:1024
	ds_read_b128 v[156:159], v149 offset:2048
	ds_read_b128 v[160:163], v149 offset:3072
	ds_read_b128 v[164:167], v150
	ds_read_b128 v[168:171], v150 offset:1024
	ds_read_b128 v[172:175], v150 offset:2048
	ds_read_b128 v[176:179], v150 offset:3072
	s_cmp_eq_u32 s56, 60
	s_cselect_b32 s4, s50, s52
	s_cselect_b32 s5, s23, s53
	s_cselect_b32 s30, s51, s54
	s_cselect_b32 s31, s21, s55
	s_add_u32 s6, s4, 0x8000
	s_addc_u32 s7, s5, 0
	ds_read_b128 v[180:183], v151
	ds_read_b128 v[184:187], v151 offset:1024
	ds_read_b128 v[188:191], v151 offset:2048
	ds_read_b128 v[192:195], v151 offset:3072
	ds_read_b128 v[196:199], v151 offset:4096
	ds_read_b128 v[200:203], v151 offset:5120
	ds_read_b128 v[210:213], v151 offset:6144
	ds_read_b128 v[214:217], v151 offset:7168
	s_waitcnt vmcnt(8)
	s_waitcnt lgkmcnt(0)
	s_barrier
	s_setprio 1
	s_waitcnt lgkmcnt(0)
	v_mfma_f32_16x16x32_bf16 v[126:129], v[134:137], v[180:183], v[126:129]
	v_mfma_f32_16x16x32_bf16 v[126:129], v[138:141], v[184:187], v[126:129]
	v_mfma_f32_16x16x32_bf16 v[122:125], v[160:163], v[184:187], v[122:125]
	v_mfma_f32_16x16x32_bf16 v[122:125], v[156:159], v[180:183], v[122:125]
	v_mfma_f32_16x16x32_bf16 v[114:117], v[156:159], v[188:191], v[114:117]
	v_mfma_f32_16x16x32_bf16 v[114:117], v[160:163], v[192:195], v[114:117]
	v_mfma_f32_16x16x32_bf16 v[118:121], v[138:141], v[192:195], v[118:121]
	v_mfma_f32_16x16x32_bf16 v[118:121], v[134:137], v[188:191], v[118:121]
	v_mfma_f32_16x16x32_bf16 v[106:109], v[134:137], v[196:199], v[106:109]
	v_mfma_f32_16x16x32_bf16 v[106:109], v[138:141], v[200:203], v[106:109]
	v_mfma_f32_16x16x32_bf16 v[98:101], v[160:163], v[200:203], v[98:101]
	v_mfma_f32_16x16x32_bf16 v[98:101], v[156:159], v[196:199], v[98:101]
	v_mfma_f32_16x16x32_bf16 v[78:81], v[156:159], v[210:213], v[78:81]
	v_mfma_f32_16x16x32_bf16 v[78:81], v[160:163], v[214:217], v[78:81]
	v_mfma_f32_16x16x32_bf16 v[82:85], v[138:141], v[214:217], v[82:85]
	v_mfma_f32_16x16x32_bf16 v[82:85], v[134:137], v[210:213], v[82:85]
	s_setprio 0
	s_setprio 1
	v_mfma_f32_16x16x32_bf16 v[70:73], v[164:167], v[210:213], v[70:73]
	v_mfma_f32_16x16x32_bf16 v[70:73], v[168:171], v[214:217], v[70:73]
	v_mfma_f32_16x16x32_bf16 v[66:69], v[176:179], v[214:217], v[66:69]
	v_mfma_f32_16x16x32_bf16 v[66:69], v[172:175], v[210:213], v[66:69]
	v_mfma_f32_16x16x32_bf16 v[74:77], v[172:175], v[196:199], v[74:77]
	v_mfma_f32_16x16x32_bf16 v[74:77], v[176:179], v[200:203], v[74:77]
	v_mfma_f32_16x16x32_bf16 v[86:89], v[168:171], v[200:203], v[86:89]
	v_mfma_f32_16x16x32_bf16 v[86:89], v[164:167], v[196:199], v[86:89]
	v_mfma_f32_16x16x32_bf16 v[94:97], v[164:167], v[188:191], v[94:97]
	v_mfma_f32_16x16x32_bf16 v[94:97], v[168:171], v[192:195], v[94:97]
	v_mfma_f32_16x16x32_bf16 v[90:93], v[176:179], v[192:195], v[90:93]
	v_mfma_f32_16x16x32_bf16 v[90:93], v[172:175], v[188:191], v[90:93]
	v_mfma_f32_16x16x32_bf16 v[102:105], v[172:175], v[180:183], v[102:105]
	v_mfma_f32_16x16x32_bf16 v[102:105], v[176:179], v[184:187], v[102:105]
	v_mfma_f32_16x16x32_bf16 v[110:113], v[168:171], v[184:187], v[110:113]
	v_mfma_f32_16x16x32_bf16 v[110:113], v[164:167], v[180:183], v[110:113]
	s_setprio 0
	s_barrier
	s_add_i32 s57, s46, s36
	s_mov_b64 s[58:59], s[30:31]
	s_mov_b32 m0, s57
	ds_read_b128 v[180:183], v151 offset:16384
	ds_read_b128 v[184:187], v151 offset:17408
	ds_read_b128 v[188:191], v151 offset:18432
	ds_read_b128 v[192:195], v151 offset:19456
	ds_read_b128 v[196:199], v151 offset:20480
	ds_read_b128 v[200:203], v151 offset:21504
	ds_read_b128 v[210:213], v151 offset:22528
	ds_read_b128 v[214:217], v151 offset:23552
	s_nop 0
	global_load_lds_dwordx4 v154, s[58:59]
	s_add_i32 m0, s57, 0x2000
	s_nop 0
	global_load_lds_dwordx4 v153, s[58:59]
	s_add_u32 s58, s30, 0x4000
	s_addc_u32 s59, s31, 0
	s_add_i32 s57, s47, s36
	s_mov_b32 m0, s57
	s_nop 0
	global_load_lds_dwordx4 v154, s[58:59]
	s_add_i32 m0, s57, 0x2000
	s_nop 0
	global_load_lds_dwordx4 v153, s[58:59]
	s_mov_b64 s[58:59], s[4:5]
	s_mov_b32 m0, s37
	s_nop 0
	global_load_lds_dwordx4 v154, s[58:59]
	s_mov_b32 m0, s38
	s_nop 0
	global_load_lds_dwordx4 v153, s[58:59]
	s_waitcnt vmcnt(8)
	s_waitcnt lgkmcnt(0)
	s_barrier
	s_setprio 1
	s_waitcnt lgkmcnt(0)
	v_mfma_f32_16x16x32_bf16 v[62:65], v[134:137], v[180:183], v[62:65]
	v_mfma_f32_16x16x32_bf16 v[62:65], v[138:141], v[184:187], v[62:65]
	v_mfma_f32_16x16x32_bf16 v[58:61], v[160:163], v[184:187], v[58:61]
	v_mfma_f32_16x16x32_bf16 v[58:61], v[156:159], v[180:183], v[58:61]
	v_mfma_f32_16x16x32_bf16 v[46:49], v[156:159], v[188:191], v[46:49]
	v_mfma_f32_16x16x32_bf16 v[46:49], v[160:163], v[192:195], v[46:49]
	v_mfma_f32_16x16x32_bf16 v[50:53], v[138:141], v[192:195], v[50:53]
	v_mfma_f32_16x16x32_bf16 v[50:53], v[134:137], v[188:191], v[50:53]
	v_mfma_f32_16x16x32_bf16 v[34:37], v[134:137], v[196:199], v[34:37]
	v_mfma_f32_16x16x32_bf16 v[34:37], v[138:141], v[200:203], v[34:37]
	v_mfma_f32_16x16x32_bf16 v[30:33], v[160:163], v[200:203], v[30:33]
	v_mfma_f32_16x16x32_bf16 v[30:33], v[156:159], v[196:199], v[30:33]
	v_mfma_f32_16x16x32_bf16 v[14:17], v[156:159], v[210:213], v[14:17]
	v_mfma_f32_16x16x32_bf16 v[14:17], v[160:163], v[214:217], v[14:17]
	v_mfma_f32_16x16x32_bf16 v[18:21], v[138:141], v[214:217], v[18:21]
	v_mfma_f32_16x16x32_bf16 v[18:21], v[134:137], v[210:213], v[18:21]
	s_setprio 0
	s_setprio 1
	v_mfma_f32_16x16x32_bf16 v[6:9], v[164:167], v[210:213], v[6:9]
	v_mfma_f32_16x16x32_bf16 v[6:9], v[168:171], v[214:217], v[6:9]
	v_mfma_f32_16x16x32_bf16 v[2:5], v[176:179], v[214:217], v[2:5]
	v_mfma_f32_16x16x32_bf16 v[2:5], v[172:175], v[210:213], v[2:5]
	v_mfma_f32_16x16x32_bf16 v[10:13], v[172:175], v[196:199], v[10:13]
	v_mfma_f32_16x16x32_bf16 v[10:13], v[176:179], v[200:203], v[10:13]
	v_mfma_f32_16x16x32_bf16 v[22:25], v[168:171], v[200:203], v[22:25]
	v_mfma_f32_16x16x32_bf16 v[22:25], v[164:167], v[196:199], v[22:25]
	v_mfma_f32_16x16x32_bf16 v[38:41], v[164:167], v[188:191], v[38:41]
	v_mfma_f32_16x16x32_bf16 v[38:41], v[168:171], v[192:195], v[38:41]
	v_mfma_f32_16x16x32_bf16 v[26:29], v[176:179], v[192:195], v[26:29]
	v_mfma_f32_16x16x32_bf16 v[26:29], v[172:175], v[188:191], v[26:29]
	v_mfma_f32_16x16x32_bf16 v[42:45], v[172:175], v[180:183], v[42:45]
	v_mfma_f32_16x16x32_bf16 v[42:45], v[176:179], v[184:187], v[42:45]
	v_mfma_f32_16x16x32_bf16 v[54:57], v[168:171], v[184:187], v[54:57]
	v_mfma_f32_16x16x32_bf16 v[54:57], v[164:167], v[180:183], v[54:57]
	s_setprio 0
	s_barrier
; #define PG8_STAGE(bufoff, gbase, voff) do { const char* _gb = (const char*)(gbase); asm volatile("" : "+s"(_gb)); _Pragma("unroll") for (int _i = 0; _i < 2; ++_i) \
;         __builtin_amdgcn_global_load_lds((const unsigned*)(_gb + (voff)[_i]), (PG8_LAS unsigned*)(lds + (bufoff) + ldsw + _i * 8192), 16, 0, 0); } while (0)
; #define PG8_LDA(dst, b, h) do { _Pragma("unroll") for (int m = 0; m < 4; ++m) _Pragma("unroll") for (int k = 0; k < 2; ++k) dst[m][k] = *(const PG8_LAS bf16x8*)(lds + PG8_SA(b, h) + aoff + m * 2048 + k * 1024); } while (0)
; #define PG8_LDB(dst, b, h) do { _Pragma("unroll") for (int n = 0; n < 2; ++n) _Pragma("unroll") for (int k = 0; k < 2; ++k) dst[n][k] = *(const PG8_LAS bf16x8*)(lds + PG8_SB(b, h) + boff + n * 2048 + k * 1024); } while (0)
; #define PG8_MMA(ai, bj, At, Bt) do { __builtin_amdgcn_s_setprio(1); _Pragma("unroll") for (int m = 0; m < 4; ++m) _Pragma("unroll") for (int n = 0; n < 2; ++n) _Pragma("unroll") for (int k = 0; k < 2; ++k) \
;         acc[ai][bj][m][n] = __builtin_amdgcn_mfma_f32_16x16x32_bf16(Bt[n][k], At[m][k], acc[ai][bj][m][n], 0, 0, 0); __builtin_amdgcn_s_setprio(0); } while (0)
; #define PG8_WAIT_V(n) asm volatile("s_waitcnt vmcnt(" #n ")" ::: "memory")
; #define PG8_WAIT_L(n) asm volatile("s_waitcnt lgkmcnt(" #n ")" ::: "memory")
; #define PG8_BAR __builtin_amdgcn_s_barrier()
; #define PG8_SCHED __builtin_amdgcn_sched_barrier(0)
; template <class Epi, class Sched, bool ALIGN_EPI = false, bool SP2 = false, bool HALFM = false>
; __device__ __forceinline__ void gemm_phase(PG8_LAS unsigned char* lds, const Gemm g, const Sched& S, const Epi& E) {
;     ...
;             PG8_LDB(B0, 1, 0); PG8_LDB(B1, 1, 1); PG8_SCHED; PG8_LDA(At, 1, 0); PG8_STAGE(PG8_SA(0, 1), a2 + hstepA, voffA);
;             PG8_WAIT_V8R; PG8_WAIT_L(0); PG8_BAR; PG8_MMA(0, 0, At, B0); PG8_MMA(0, 1, At, B1); PG8_BAR; PG8_SCHED;
;             if constexpr (!HALFM) { PG8_LDA(At, 1, 1); } PG8_STAGE(PG8_SB(1, 0), b3, voffB); PG8_STAGE(PG8_SB(1, 1), b3 + hstep, voffB); PG8_STAGE(PG8_SA(1, 0), a3, voffA);
;             PG8_WAIT_V(8); PG8_WAIT_L(0); PG8_BAR; if constexpr (!HALFM) { PG8_MMA(1, 0, At, B0); PG8_MMA(1, 1, At, B1); } PG8_BAR; PG8_SCHED;
;             PG8_STAGE(PG8_SA(1, 1), a3 + hstepA, voffA);
	s_add_i32 s57, 0, 0x18000
	v_add_u32_e32 v155, s57, v147
	s_add_i32 s60, 0, 0x1c000
	ds_read_b128 v[134:137], v155
	ds_read_b128 v[138:141], v155 offset:1024
	ds_read_b128 v[156:159], v155 offset:2048
	ds_read_b128 v[160:163], v155 offset:3072
	v_add_u32_e32 v155, s60, v147
	ds_read_b128 v[164:167], v155
	ds_read_b128 v[168:171], v155 offset:1024
	ds_read_b128 v[172:175], v155 offset:2048
	ds_read_b128 v[176:179], v155 offset:3072
	s_add_u32 s58, s4, 0x4000
	s_addc_u32 s59, s5, 0
	s_mov_b32 m0, s39
	ds_read_b128 v[180:183], v151 offset:32768
	ds_read_b128 v[184:187], v151 offset:33792
	ds_read_b128 v[188:191], v151 offset:34816
	ds_read_b128 v[192:195], v151 offset:35840
	ds_read_b128 v[196:199], v151 offset:36864
	ds_read_b128 v[200:203], v151 offset:37888
	ds_read_b128 v[210:213], v151 offset:38912
	ds_read_b128 v[214:217], v151 offset:39936
	s_nop 0
	global_load_lds_dwordx4 v154, s[58:59]
	s_mov_b32 m0, s40
	s_nop 0
	global_load_lds_dwordx4 v153, s[58:59]
	s_waitcnt vmcnt(8)
	s_waitcnt lgkmcnt(0)
	s_barrier
	s_setprio 1
	s_waitcnt lgkmcnt(0)
	v_mfma_f32_16x16x32_bf16 v[126:129], v[134:137], v[180:183], v[126:129]
	v_mfma_f32_16x16x32_bf16 v[126:129], v[138:141], v[184:187], v[126:129]
	v_mfma_f32_16x16x32_bf16 v[122:125], v[160:163], v[184:187], v[122:125]
	v_mfma_f32_16x16x32_bf16 v[122:125], v[156:159], v[180:183], v[122:125]
	v_mfma_f32_16x16x32_bf16 v[114:117], v[156:159], v[188:191], v[114:117]
	v_mfma_f32_16x16x32_bf16 v[114:117], v[160:163], v[192:195], v[114:117]
	v_mfma_f32_16x16x32_bf16 v[118:121], v[138:141], v[192:195], v[118:121]
	v_mfma_f32_16x16x32_bf16 v[118:121], v[134:137], v[188:191], v[118:121]
	v_mfma_f32_16x16x32_bf16 v[106:109], v[134:137], v[196:199], v[106:109]
	v_mfma_f32_16x16x32_bf16 v[106:109], v[138:141], v[200:203], v[106:109]
	v_mfma_f32_16x16x32_bf16 v[98:101], v[160:163], v[200:203], v[98:101]
	v_mfma_f32_16x16x32_bf16 v[98:101], v[156:159], v[196:199], v[98:101]
	v_mfma_f32_16x16x32_bf16 v[78:81], v[156:159], v[210:213], v[78:81]
	v_mfma_f32_16x16x32_bf16 v[78:81], v[160:163], v[214:217], v[78:81]
	v_mfma_f32_16x16x32_bf16 v[82:85], v[138:141], v[214:217], v[82:85]
	v_mfma_f32_16x16x32_bf16 v[82:85], v[134:137], v[210:213], v[82:85]
	s_setprio 0
	s_setprio 1
	v_mfma_f32_16x16x32_bf16 v[70:73], v[164:167], v[210:213], v[70:73]
	v_mfma_f32_16x16x32_bf16 v[70:73], v[168:171], v[214:217], v[70:73]
	v_mfma_f32_16x16x32_bf16 v[66:69], v[176:179], v[214:217], v[66:69]
	v_mfma_f32_16x16x32_bf16 v[66:69], v[172:175], v[210:213], v[66:69]
	v_mfma_f32_16x16x32_bf16 v[74:77], v[172:175], v[196:199], v[74:77]
	v_mfma_f32_16x16x32_bf16 v[74:77], v[176:179], v[200:203], v[74:77]
	v_mfma_f32_16x16x32_bf16 v[86:89], v[168:171], v[200:203], v[86:89]
	v_mfma_f32_16x16x32_bf16 v[86:89], v[164:167], v[196:199], v[86:89]
	v_mfma_f32_16x16x32_bf16 v[94:97], v[164:167], v[188:191], v[94:97]
	v_mfma_f32_16x16x32_bf16 v[94:97], v[168:171], v[192:195], v[94:97]
	v_mfma_f32_16x16x32_bf16 v[90:93], v[176:179], v[192:195], v[90:93]
	v_mfma_f32_16x16x32_bf16 v[90:93], v[172:175], v[188:191], v[90:93]
	v_mfma_f32_16x16x32_bf16 v[102:105], v[172:175], v[180:183], v[102:105]
	v_mfma_f32_16x16x32_bf16 v[102:105], v[176:179], v[184:187], v[102:105]
	v_mfma_f32_16x16x32_bf16 v[110:113], v[168:171], v[184:187], v[110:113]
	v_mfma_f32_16x16x32_bf16 v[110:113], v[164:167], v[180:183], v[110:113]
	s_setprio 0
	s_barrier
	s_add_u32 s58, s30, 0x8000
	s_addc_u32 s59, s31, 0
	s_add_i32 s57, s57, s36
	s_mov_b32 m0, s57
	ds_read_b128 v[180:183], v151 offset:49152
	ds_read_b128 v[184:187], v151 offset:50176
	ds_read_b128 v[188:191], v151 offset:51200
	ds_read_b128 v[192:195], v151 offset:52224
	ds_read_b128 v[196:199], v151 offset:53248
	ds_read_b128 v[200:203], v151 offset:54272
	ds_read_b128 v[210:213], v151 offset:55296
	ds_read_b128 v[214:217], v151 offset:56320
	s_nop 0
	global_load_lds_dwordx4 v154, s[58:59]
	s_add_i32 m0, s57, 0x2000
	s_add_u32 s30, s30, 0xc000
	s_addc_u32 s31, s31, 0
	s_add_i32 s57, s60, s36
	global_load_lds_dwordx4 v153, s[58:59]
	s_mov_b32 m0, s57
	s_nop 0
	global_load_lds_dwordx4 v154, s[30:31]
	s_add_i32 m0, s57, 0x2000
	s_nop 0
	global_load_lds_dwordx4 v153, s[30:31]
	s_mov_b32 m0, s42
	s_nop 0
	global_load_lds_dwordx4 v154, s[6:7]
	s_mov_b32 m0, s43
	s_nop 0
	global_load_lds_dwordx4 v153, s[6:7]
	s_waitcnt vmcnt(8)
	s_waitcnt lgkmcnt(0)
	s_barrier
	s_setprio 1
	s_waitcnt lgkmcnt(0)
	v_mfma_f32_16x16x32_bf16 v[62:65], v[134:137], v[180:183], v[62:65]
	v_mfma_f32_16x16x32_bf16 v[62:65], v[138:141], v[184:187], v[62:65]
	v_mfma_f32_16x16x32_bf16 v[58:61], v[160:163], v[184:187], v[58:61]
	v_mfma_f32_16x16x32_bf16 v[58:61], v[156:159], v[180:183], v[58:61]
	v_mfma_f32_16x16x32_bf16 v[46:49], v[156:159], v[188:191], v[46:49]
	v_mfma_f32_16x16x32_bf16 v[46:49], v[160:163], v[192:195], v[46:49]
	v_mfma_f32_16x16x32_bf16 v[50:53], v[138:141], v[192:195], v[50:53]
	v_mfma_f32_16x16x32_bf16 v[50:53], v[134:137], v[188:191], v[50:53]
	v_mfma_f32_16x16x32_bf16 v[34:37], v[134:137], v[196:199], v[34:37]
	v_mfma_f32_16x16x32_bf16 v[34:37], v[138:141], v[200:203], v[34:37]
	v_mfma_f32_16x16x32_bf16 v[30:33], v[160:163], v[200:203], v[30:33]
	v_mfma_f32_16x16x32_bf16 v[30:33], v[156:159], v[196:199], v[30:33]
	v_mfma_f32_16x16x32_bf16 v[14:17], v[156:159], v[210:213], v[14:17]
	v_mfma_f32_16x16x32_bf16 v[14:17], v[160:163], v[214:217], v[14:17]
	v_mfma_f32_16x16x32_bf16 v[18:21], v[138:141], v[214:217], v[18:21]
	v_mfma_f32_16x16x32_bf16 v[18:21], v[134:137], v[210:213], v[18:21]
	s_setprio 0
	s_setprio 1
	v_mfma_f32_16x16x32_bf16 v[6:9], v[164:167], v[210:213], v[6:9]
	v_mfma_f32_16x16x32_bf16 v[6:9], v[168:171], v[214:217], v[6:9]
	v_mfma_f32_16x16x32_bf16 v[2:5], v[176:179], v[214:217], v[2:5]
	v_mfma_f32_16x16x32_bf16 v[2:5], v[172:175], v[210:213], v[2:5]
	v_mfma_f32_16x16x32_bf16 v[10:13], v[172:175], v[196:199], v[10:13]
	v_mfma_f32_16x16x32_bf16 v[10:13], v[176:179], v[200:203], v[10:13]
	v_mfma_f32_16x16x32_bf16 v[22:25], v[168:171], v[200:203], v[22:25]
	v_mfma_f32_16x16x32_bf16 v[22:25], v[164:167], v[196:199], v[22:25]
	v_mfma_f32_16x16x32_bf16 v[38:41], v[164:167], v[188:191], v[38:41]
	v_mfma_f32_16x16x32_bf16 v[38:41], v[168:171], v[192:195], v[38:41]
	v_mfma_f32_16x16x32_bf16 v[26:29], v[176:179], v[192:195], v[26:29]
	v_mfma_f32_16x16x32_bf16 v[26:29], v[172:175], v[188:191], v[26:29]
	v_mfma_f32_16x16x32_bf16 v[42:45], v[172:175], v[180:183], v[42:45]
	v_mfma_f32_16x16x32_bf16 v[42:45], v[176:179], v[184:187], v[42:45]
	v_mfma_f32_16x16x32_bf16 v[54:57], v[168:171], v[184:187], v[54:57]
	v_mfma_f32_16x16x32_bf16 v[54:57], v[164:167], v[180:183], v[54:57]
	s_setprio 0
	s_barrier
	s_add_u32 s4, s4, 0xc000
	s_mov_b32 m0, s44
	s_addc_u32 s5, s5, 0
	s_add_i32 s56, s56, 2
	global_load_lds_dwordx4 v154, s[4:5]
	s_mov_b32 m0, s45
	s_add_u32 s52, s52, 0x10000
	global_load_lds_dwordx4 v153, s[4:5]
	s_addc_u32 s53, s53, 0
	s_add_u32 s54, s54, 0x10000
	s_addc_u32 s55, s55, 0
	s_cmp_gt_u32 s56, 61
	s_cbranch_scc0 .LBB0_901
	s_and_b64 vcc, exec, s[18:19]
	s_cbranch_vccz .LBB0_904
	s_barrier

; #define PG8_STAGE(bufoff, gbase, voff) do { const char* _gb = (const char*)(gbase); asm volatile("" : "+s"(_gb)); _Pragma("unroll") for (int _i = 0; _i < 2; ++_i) \
;         __builtin_amdgcn_global_load_lds((const unsigned*)(_gb + (voff)[_i]), (PG8_LAS unsigned*)(lds + (bufoff) + ldsw + _i * 8192), 16, 0, 0); } while (0)
; #define PG8_LDA(dst, b, h) do { _Pragma("unroll") for (int m = 0; m < 4; ++m) _Pragma("unroll") for (int k = 0; k < 2; ++k) dst[m][k] = *(const PG8_LAS bf16x8*)(lds + PG8_SA(b, h) + aoff + m * 2048 + k * 1024); } while (0)
; #define PG8_LDB(dst, b, h) do { _Pragma("unroll") for (int n = 0; n < 2; ++n) _Pragma("unroll") for (int k = 0; k < 2; ++k) dst[n][k] = *(const PG8_LAS bf16x8*)(lds + PG8_SB(b, h) + boff + n * 2048 + k * 1024); } while (0)
; template <class Epi, class Sched, bool ALIGN_EPI = false, bool SP2 = false, bool HALFM = false>
; __device__ __forceinline__ void gemm_phase(PG8_LAS unsigned char* lds, const Gemm g, const Sched& S, const Epi& E) {
;     ...
;         for (int t = 0; t < nt; t += 2) {
;             const bool last = (t == nt - 2);
;             const char* a1 = cA + (size_t)(t + 1) * kstep;
;             const char* a2 = last ? nA : cA + (size_t)(t + 2) * kstep; const char* b2 = last ? nB : cB + (size_t)(t + 2) * kstep;
;             const char* a3 = a2 + kstep; const char* b3 = b2 + kstep;
;             if (last && has_next) S.a_ready(nxt);
;             if constexpr (Epi::HAS_PREFETCH) { if (last) E.prefetch(cur, wid, lane); }
;             asm volatile("" : "+v"(voffA[0]), "+v"(voffA[1])); voffB[0] = voffA[0]; voffB[1] = voffA[1];
;             if constexpr (SP2) {
;             PG8_LDB(B0, 0, 0); PG8_LDB(B1, 0, 1); PG8_SCHED; PG8_LDA(At, 0, 0);
;             PG8_WAIT_V8R; PG8_WAIT_L(0); PG8_BAR; PG8_MMA(0, 0, At, B0); PG8_MMA(0, 1, At, B1); PG8_BAR; PG8_SCHED;
;             if constexpr (!HALFM) { PG8_LDA(At, 0, 1); } PG8_STAGE(PG8_SB(0, 0), b2, voffB); PG8_STAGE(PG8_SB(0, 1), b2 + hstep, voffB); PG8_STAGE(PG8_SA(0, 0), a2, voffA);
;             PG8_WAIT_V8R; PG8_WAIT_L(0); PG8_BAR; if constexpr (!HALFM) { PG8_MMA(1, 0, At, B0); PG8_MMA(1, 1, At, B1); } PG8_BAR; PG8_SCHED;
;             PG8_LDB(B0, 1, 0); PG8_LDB(B1, 1, 1); PG8_SCHED; PG8_LDA(At, 1, 0); PG8_STAGE(PG8_SA(0, 1), a2 + hstepA, voffA);
;             PG8_WAIT_V8R; PG8_WAIT_L(0); PG8_BAR; PG8_MMA(0, 0, At, B0); PG8_MMA(0, 1, At, B1); PG8_BAR; PG8_SCHED;
.LBB0_918:
	ds_read_b128 v[132:135], v143
	ds_read_b128 v[136:139], v143 offset:1024
	ds_read_b128 v[148:151], v143 offset:2048
	ds_read_b128 v[152:155], v143 offset:3072
	ds_read_b128 v[156:159], v144
	ds_read_b128 v[160:163], v144 offset:1024
	ds_read_b128 v[164:167], v144 offset:2048
	ds_read_b128 v[168:171], v144 offset:3072
	s_cmp_eq_u32 s59, 60
	s_cselect_b32 s4, s53, s55
	s_cselect_b32 s5, s23, s56
	s_cselect_b32 s30, s54, s57
	s_cselect_b32 s31, s21, s58
	s_add_u32 s6, s4, 0x8000
	s_addc_u32 s7, s5, 0
	ds_read_b128 v[172:175], v145
	ds_read_b128 v[176:179], v145 offset:1024
	ds_read_b128 v[180:183], v145 offset:2048
	ds_read_b128 v[184:187], v145 offset:3072
	ds_read_b128 v[188:191], v145 offset:4096
	ds_read_b128 v[192:195], v145 offset:5120
	ds_read_b128 v[196:199], v145 offset:6144
	ds_read_b128 v[200:203], v145 offset:7168
	s_waitcnt vmcnt(8)
	s_waitcnt lgkmcnt(0)
	s_barrier
	s_setprio 1
	s_waitcnt lgkmcnt(0)
	v_mfma_f32_16x16x32_bf16 v[126:129], v[132:135], v[172:175], v[126:129]
	v_mfma_f32_16x16x32_bf16 v[126:129], v[136:139], v[176:179], v[126:129]
	v_mfma_f32_16x16x32_bf16 v[122:125], v[152:155], v[176:179], v[122:125]
	v_mfma_f32_16x16x32_bf16 v[122:125], v[148:151], v[172:175], v[122:125]
	v_mfma_f32_16x16x32_bf16 v[114:117], v[148:151], v[180:183], v[114:117]
	v_mfma_f32_16x16x32_bf16 v[114:117], v[152:155], v[184:187], v[114:117]
	v_mfma_f32_16x16x32_bf16 v[118:121], v[136:139], v[184:187], v[118:121]
	v_mfma_f32_16x16x32_bf16 v[118:121], v[132:135], v[180:183], v[118:121]
	v_mfma_f32_16x16x32_bf16 v[106:109], v[132:135], v[188:191], v[106:109]
	v_mfma_f32_16x16x32_bf16 v[106:109], v[136:139], v[192:195], v[106:109]
	v_mfma_f32_16x16x32_bf16 v[98:101], v[152:155], v[192:195], v[98:101]
	v_mfma_f32_16x16x32_bf16 v[98:101], v[148:151], v[188:191], v[98:101]
	v_mfma_f32_16x16x32_bf16 v[78:81], v[148:151], v[196:199], v[78:81]
	v_mfma_f32_16x16x32_bf16 v[78:81], v[152:155], v[200:203], v[78:81]
	v_mfma_f32_16x16x32_bf16 v[82:85], v[136:139], v[200:203], v[82:85]
	v_mfma_f32_16x16x32_bf16 v[82:85], v[132:135], v[196:199], v[82:85]
	s_setprio 0
	s_setprio 1
	v_mfma_f32_16x16x32_bf16 v[70:73], v[156:159], v[196:199], v[70:73]
	v_mfma_f32_16x16x32_bf16 v[70:73], v[160:163], v[200:203], v[70:73]
	v_mfma_f32_16x16x32_bf16 v[66:69], v[168:171], v[200:203], v[66:69]
	v_mfma_f32_16x16x32_bf16 v[66:69], v[164:167], v[196:199], v[66:69]
	v_mfma_f32_16x16x32_bf16 v[74:77], v[164:167], v[188:191], v[74:77]
	v_mfma_f32_16x16x32_bf16 v[74:77], v[168:171], v[192:195], v[74:77]
	v_mfma_f32_16x16x32_bf16 v[86:89], v[160:163], v[192:195], v[86:89]
	v_mfma_f32_16x16x32_bf16 v[86:89], v[156:159], v[188:191], v[86:89]
	v_mfma_f32_16x16x32_bf16 v[94:97], v[156:159], v[180:183], v[94:97]
	v_mfma_f32_16x16x32_bf16 v[94:97], v[160:163], v[184:187], v[94:97]
	v_mfma_f32_16x16x32_bf16 v[90:93], v[168:171], v[184:187], v[90:93]
	v_mfma_f32_16x16x32_bf16 v[90:93], v[164:167], v[180:183], v[90:93]
	v_mfma_f32_16x16x32_bf16 v[102:105], v[164:167], v[172:175], v[102:105]
	v_mfma_f32_16x16x32_bf16 v[102:105], v[168:171], v[176:179], v[102:105]
	v_mfma_f32_16x16x32_bf16 v[110:113], v[160:163], v[176:179], v[110:113]
	v_mfma_f32_16x16x32_bf16 v[110:113], v[156:159], v[172:175], v[110:113]
	s_setprio 0
	s_barrier
	s_add_i32 s62, s49, s39
	s_mov_b64 s[60:61], s[30:31]
	s_mov_b32 m0, s62
	ds_read_b128 v[172:175], v145 offset:16384
	ds_read_b128 v[176:179], v145 offset:17408
	ds_read_b128 v[180:183], v145 offset:18432
	ds_read_b128 v[184:187], v145 offset:19456
	ds_read_b128 v[188:191], v145 offset:20480
	ds_read_b128 v[192:195], v145 offset:21504
	ds_read_b128 v[196:199], v145 offset:22528
	ds_read_b128 v[200:203], v145 offset:23552
	s_nop 0
	global_load_lds_dwordx4 v130, s[60:61]
	s_add_i32 m0, s62, 0x2000
	s_nop 0
	global_load_lds_dwordx4 v142, s[60:61]
	s_add_u32 s60, s30, 0x4000
	s_addc_u32 s61, s31, 0
	s_add_i32 s62, s50, s39
	s_mov_b32 m0, s62
	s_nop 0
	global_load_lds_dwordx4 v130, s[60:61]
	s_add_i32 m0, s62, 0x2000
	s_nop 0
	global_load_lds_dwordx4 v142, s[60:61]
	s_mov_b64 s[60:61], s[4:5]
	s_mov_b32 m0, s40
	s_nop 0
	global_load_lds_dwordx4 v130, s[60:61]
	s_mov_b32 m0, s41
	s_nop 0
	global_load_lds_dwordx4 v142, s[60:61]
	s_waitcnt vmcnt(8)
	s_waitcnt lgkmcnt(0)
	s_barrier
	s_setprio 1
	s_waitcnt lgkmcnt(0)
	v_mfma_f32_16x16x32_bf16 v[62:65], v[132:135], v[172:175], v[62:65]
	v_mfma_f32_16x16x32_bf16 v[62:65], v[136:139], v[176:179], v[62:65]
	v_mfma_f32_16x16x32_bf16 v[58:61], v[152:155], v[176:179], v[58:61]
	v_mfma_f32_16x16x32_bf16 v[58:61], v[148:151], v[172:175], v[58:61]
	v_mfma_f32_16x16x32_bf16 v[46:49], v[148:151], v[180:183], v[46:49]
	v_mfma_f32_16x16x32_bf16 v[46:49], v[152:155], v[184:187], v[46:49]
	v_mfma_f32_16x16x32_bf16 v[50:53], v[136:139], v[184:187], v[50:53]
	v_mfma_f32_16x16x32_bf16 v[50:53], v[132:135], v[180:183], v[50:53]
	v_mfma_f32_16x16x32_bf16 v[34:37], v[132:135], v[188:191], v[34:37]
	v_mfma_f32_16x16x32_bf16 v[34:37], v[136:139], v[192:195], v[34:37]
	v_mfma_f32_16x16x32_bf16 v[30:33], v[152:155], v[192:195], v[30:33]
	v_mfma_f32_16x16x32_bf16 v[30:33], v[148:151], v[188:191], v[30:33]
	v_mfma_f32_16x16x32_bf16 v[14:17], v[148:151], v[196:199], v[14:17]
	v_mfma_f32_16x16x32_bf16 v[14:17], v[152:155], v[200:203], v[14:17]
	v_mfma_f32_16x16x32_bf16 v[18:21], v[136:139], v[200:203], v[18:21]
	v_mfma_f32_16x16x32_bf16 v[18:21], v[132:135], v[196:199], v[18:21]
	s_setprio 0
	s_setprio 1
	v_mfma_f32_16x16x32_bf16 v[6:9], v[156:159], v[196:199], v[6:9]
	v_mfma_f32_16x16x32_bf16 v[6:9], v[160:163], v[200:203], v[6:9]
	v_mfma_f32_16x16x32_bf16 v[2:5], v[168:171], v[200:203], v[2:5]
	v_mfma_f32_16x16x32_bf16 v[2:5], v[164:167], v[196:199], v[2:5]
	v_mfma_f32_16x16x32_bf16 v[10:13], v[164:167], v[188:191], v[10:13]
	v_mfma_f32_16x16x32_bf16 v[10:13], v[168:171], v[192:195], v[10:13]
	v_mfma_f32_16x16x32_bf16 v[22:25], v[160:163], v[192:195], v[22:25]
	v_mfma_f32_16x16x32_bf16 v[22:25], v[156:159], v[188:191], v[22:25]
	v_mfma_f32_16x16x32_bf16 v[38:41], v[156:159], v[180:183], v[38:41]
	v_mfma_f32_16x16x32_bf16 v[38:41], v[160:163], v[184:187], v[38:41]
	v_mfma_f32_16x16x32_bf16 v[26:29], v[168:171], v[184:187], v[26:29]
	v_mfma_f32_16x16x32_bf16 v[26:29], v[164:167], v[180:183], v[26:29]
	v_mfma_f32_16x16x32_bf16 v[42:45], v[164:167], v[172:175], v[42:45]
	v_mfma_f32_16x16x32_bf16 v[42:45], v[168:171], v[176:179], v[42:45]
	v_mfma_f32_16x16x32_bf16 v[54:57], v[160:163], v[176:179], v[54:57]
	v_mfma_f32_16x16x32_bf16 v[54:57], v[156:159], v[172:175], v[54:57]
	s_setprio 0
	s_barrier
; #define PG8_STAGE(bufoff, gbase, voff) do { const char* _gb = (const char*)(gbase); asm volatile("" : "+s"(_gb)); _Pragma("unroll") for (int _i = 0; _i < 2; ++_i) \
;         __builtin_amdgcn_global_load_lds((const unsigned*)(_gb + (voff)[_i]), (PG8_LAS unsigned*)(lds + (bufoff) + ldsw + _i * 8192), 16, 0, 0); } while (0)
; #define PG8_LDA(dst, b, h) do { _Pragma("unroll") for (int m = 0; m < 4; ++m) _Pragma("unroll") for (int k = 0; k < 2; ++k) dst[m][k] = *(const PG8_LAS bf16x8*)(lds + PG8_SA(b, h) + aoff + m * 2048 + k * 1024); } while (0)
; #define PG8_LDB(dst, b, h) do { _Pragma("unroll") for (int n = 0; n < 2; ++n) _Pragma("unroll") for (int k = 0; k < 2; ++k) dst[n][k] = *(const PG8_LAS bf16x8*)(lds + PG8_SB(b, h) + boff + n * 2048 + k * 1024); } while (0)
; #define PG8_MMA(ai, bj, At, Bt) do { __builtin_amdgcn_s_setprio(1); _Pragma("unroll") for (int m = 0; m < 4; ++m) _Pragma("unroll") for (int n = 0; n < 2; ++n) _Pragma("unroll") for (int k = 0; k < 2; ++k) \
;         acc[ai][bj][m][n] = __builtin_amdgcn_mfma_f32_16x16x32_bf16(Bt[n][k], At[m][k], acc[ai][bj][m][n], 0, 0, 0); __builtin_amdgcn_s_setprio(0); } while (0)
; #define PG8_WAIT_V(n) asm volatile("s_waitcnt vmcnt(" #n ")" ::: "memory")
; #define PG8_WAIT_L(n) asm volatile("s_waitcnt lgkmcnt(" #n ")" ::: "memory")
; #define PG8_BAR __builtin_amdgcn_s_barrier()
; #define PG8_SCHED __builtin_amdgcn_sched_barrier(0)
; template <class Epi, class Sched, bool ALIGN_EPI = false, bool SP2 = false, bool HALFM = false>
; __device__ __forceinline__ void gemm_phase(PG8_LAS unsigned char* lds, const Gemm g, const Sched& S, const Epi& E) {
;     ...
;             PG8_LDB(B0, 1, 0); PG8_LDB(B1, 1, 1); PG8_SCHED; PG8_LDA(At, 1, 0); PG8_STAGE(PG8_SA(0, 1), a2 + hstepA, voffA);
;             PG8_WAIT_V8R; PG8_WAIT_L(0); PG8_BAR; PG8_MMA(0, 0, At, B0); PG8_MMA(0, 1, At, B1); PG8_BAR; PG8_SCHED;
;             if constexpr (!HALFM) { PG8_LDA(At, 1, 1); } PG8_STAGE(PG8_SB(1, 0), b3, voffB); PG8_STAGE(PG8_SB(1, 1), b3 + hstep, voffB); PG8_STAGE(PG8_SA(1, 0), a3, voffA);
;             PG8_WAIT_V(8); PG8_WAIT_L(0); PG8_BAR; if constexpr (!HALFM) { PG8_MMA(1, 0, At, B0); PG8_MMA(1, 1, At, B1); } PG8_BAR; PG8_SCHED;
;             PG8_STAGE(PG8_SA(1, 1), a3 + hstepA, voffA);
	s_add_i32 s62, 0, 0x18000
	v_add_u32_e32 v147, s62, v140
	s_add_i32 s63, 0, 0x1c000
	ds_read_b128 v[132:135], v147
	ds_read_b128 v[136:139], v147 offset:1024
	ds_read_b128 v[148:151], v147 offset:2048
	ds_read_b128 v[152:155], v147 offset:3072
	v_add_u32_e32 v147, s63, v140
	ds_read_b128 v[156:159], v147
	ds_read_b128 v[160:163], v147 offset:1024
	ds_read_b128 v[164:167], v147 offset:2048
	ds_read_b128 v[168:171], v147 offset:3072
	s_add_u32 s60, s4, 0x4000
	s_addc_u32 s61, s5, 0
	s_mov_b32 m0, s42
	ds_read_b128 v[172:175], v145 offset:32768
	ds_read_b128 v[176:179], v145 offset:33792
	ds_read_b128 v[180:183], v145 offset:34816
	ds_read_b128 v[184:187], v145 offset:35840
	ds_read_b128 v[188:191], v145 offset:36864
	ds_read_b128 v[192:195], v145 offset:37888
	ds_read_b128 v[196:199], v145 offset:38912
	ds_read_b128 v[200:203], v145 offset:39936
	s_nop 0
	global_load_lds_dwordx4 v130, s[60:61]
	s_mov_b32 m0, s43
	s_nop 0
	global_load_lds_dwordx4 v142, s[60:61]
	s_waitcnt vmcnt(8)
	s_waitcnt lgkmcnt(0)
	s_barrier
	s_setprio 1
	s_waitcnt lgkmcnt(0)
	v_mfma_f32_16x16x32_bf16 v[126:129], v[132:135], v[172:175], v[126:129]
	v_mfma_f32_16x16x32_bf16 v[126:129], v[136:139], v[176:179], v[126:129]
	v_mfma_f32_16x16x32_bf16 v[122:125], v[152:155], v[176:179], v[122:125]
	v_mfma_f32_16x16x32_bf16 v[122:125], v[148:151], v[172:175], v[122:125]
	v_mfma_f32_16x16x32_bf16 v[114:117], v[148:151], v[180:183], v[114:117]
	v_mfma_f32_16x16x32_bf16 v[114:117], v[152:155], v[184:187], v[114:117]
	v_mfma_f32_16x16x32_bf16 v[118:121], v[136:139], v[184:187], v[118:121]
	v_mfma_f32_16x16x32_bf16 v[118:121], v[132:135], v[180:183], v[118:121]
	v_mfma_f32_16x16x32_bf16 v[106:109], v[132:135], v[188:191], v[106:109]
	v_mfma_f32_16x16x32_bf16 v[106:109], v[136:139], v[192:195], v[106:109]
	v_mfma_f32_16x16x32_bf16 v[98:101], v[152:155], v[192:195], v[98:101]
	v_mfma_f32_16x16x32_bf16 v[98:101], v[148:151], v[188:191], v[98:101]
	v_mfma_f32_16x16x32_bf16 v[78:81], v[148:151], v[196:199], v[78:81]
	v_mfma_f32_16x16x32_bf16 v[78:81], v[152:155], v[200:203], v[78:81]
	v_mfma_f32_16x16x32_bf16 v[82:85], v[136:139], v[200:203], v[82:85]
	v_mfma_f32_16x16x32_bf16 v[82:85], v[132:135], v[196:199], v[82:85]
	s_setprio 0
	s_setprio 1
	v_mfma_f32_16x16x32_bf16 v[70:73], v[156:159], v[196:199], v[70:73]
	v_mfma_f32_16x16x32_bf16 v[70:73], v[160:163], v[200:203], v[70:73]
	v_mfma_f32_16x16x32_bf16 v[66:69], v[168:171], v[200:203], v[66:69]
	v_mfma_f32_16x16x32_bf16 v[66:69], v[164:167], v[196:199], v[66:69]
	v_mfma_f32_16x16x32_bf16 v[74:77], v[164:167], v[188:191], v[74:77]
	v_mfma_f32_16x16x32_bf16 v[74:77], v[168:171], v[192:195], v[74:77]
	v_mfma_f32_16x16x32_bf16 v[86:89], v[160:163], v[192:195], v[86:89]
	v_mfma_f32_16x16x32_bf16 v[86:89], v[156:159], v[188:191], v[86:89]
	v_mfma_f32_16x16x32_bf16 v[94:97], v[156:159], v[180:183], v[94:97]
	v_mfma_f32_16x16x32_bf16 v[94:97], v[160:163], v[184:187], v[94:97]
	v_mfma_f32_16x16x32_bf16 v[90:93], v[168:171], v[184:187], v[90:93]
	v_mfma_f32_16x16x32_bf16 v[90:93], v[164:167], v[180:183], v[90:93]
	v_mfma_f32_16x16x32_bf16 v[102:105], v[164:167], v[172:175], v[102:105]
	v_mfma_f32_16x16x32_bf16 v[102:105], v[168:171], v[176:179], v[102:105]
	v_mfma_f32_16x16x32_bf16 v[110:113], v[160:163], v[176:179], v[110:113]
	v_mfma_f32_16x16x32_bf16 v[110:113], v[156:159], v[172:175], v[110:113]
	s_setprio 0
	s_barrier
	s_add_u32 s60, s30, 0x8000
	s_addc_u32 s61, s31, 0
	s_add_i32 s62, s62, s39
	s_mov_b32 m0, s62
	ds_read_b128 v[172:175], v145 offset:49152
	ds_read_b128 v[176:179], v145 offset:50176
	ds_read_b128 v[180:183], v145 offset:51200
	ds_read_b128 v[184:187], v145 offset:52224
	ds_read_b128 v[188:191], v145 offset:53248
	ds_read_b128 v[192:195], v145 offset:54272
	ds_read_b128 v[196:199], v145 offset:55296
	ds_read_b128 v[200:203], v145 offset:56320
	s_nop 0
	global_load_lds_dwordx4 v130, s[60:61]
	s_add_i32 m0, s62, 0x2000
	s_add_u32 s30, s30, 0xc000
	global_load_lds_dwordx4 v142, s[60:61]
	s_addc_u32 s31, s31, 0
	s_add_i32 s60, s63, s39
	s_mov_b32 m0, s60
	s_nop 0
	global_load_lds_dwordx4 v130, s[30:31]
	s_add_i32 m0, s60, 0x2000
	s_nop 0
	global_load_lds_dwordx4 v142, s[30:31]
	s_mov_b32 m0, s44
	s_nop 0
	global_load_lds_dwordx4 v130, s[6:7]
	s_mov_b32 m0, s45
	s_nop 0
	global_load_lds_dwordx4 v142, s[6:7]
	s_waitcnt vmcnt(8)
	s_waitcnt lgkmcnt(0)
	s_barrier
	s_setprio 1
	s_waitcnt lgkmcnt(0)
	v_mfma_f32_16x16x32_bf16 v[62:65], v[132:135], v[172:175], v[62:65]
	v_mfma_f32_16x16x32_bf16 v[62:65], v[136:139], v[176:179], v[62:65]
	v_mfma_f32_16x16x32_bf16 v[58:61], v[152:155], v[176:179], v[58:61]
	v_mfma_f32_16x16x32_bf16 v[58:61], v[148:151], v[172:175], v[58:61]
	v_mfma_f32_16x16x32_bf16 v[46:49], v[148:151], v[180:183], v[46:49]
	v_mfma_f32_16x16x32_bf16 v[46:49], v[152:155], v[184:187], v[46:49]
	v_mfma_f32_16x16x32_bf16 v[50:53], v[136:139], v[184:187], v[50:53]
	v_mfma_f32_16x16x32_bf16 v[50:53], v[132:135], v[180:183], v[50:53]
	v_mfma_f32_16x16x32_bf16 v[34:37], v[132:135], v[188:191], v[34:37]
	v_mfma_f32_16x16x32_bf16 v[34:37], v[136:139], v[192:195], v[34:37]
	v_mfma_f32_16x16x32_bf16 v[30:33], v[152:155], v[192:195], v[30:33]
	v_mfma_f32_16x16x32_bf16 v[30:33], v[148:151], v[188:191], v[30:33]
	v_mfma_f32_16x16x32_bf16 v[14:17], v[148:151], v[196:199], v[14:17]
	v_mfma_f32_16x16x32_bf16 v[14:17], v[152:155], v[200:203], v[14:17]
	v_mfma_f32_16x16x32_bf16 v[18:21], v[136:139], v[200:203], v[18:21]
	v_mfma_f32_16x16x32_bf16 v[18:21], v[132:135], v[196:199], v[18:21]
	s_setprio 0
	s_setprio 1
	v_mfma_f32_16x16x32_bf16 v[6:9], v[156:159], v[196:199], v[6:9]
	v_mfma_f32_16x16x32_bf16 v[6:9], v[160:163], v[200:203], v[6:9]
	v_mfma_f32_16x16x32_bf16 v[2:5], v[168:171], v[200:203], v[2:5]
	v_mfma_f32_16x16x32_bf16 v[2:5], v[164:167], v[196:199], v[2:5]
	v_mfma_f32_16x16x32_bf16 v[10:13], v[164:167], v[188:191], v[10:13]
	v_mfma_f32_16x16x32_bf16 v[10:13], v[168:171], v[192:195], v[10:13]
	v_mfma_f32_16x16x32_bf16 v[22:25], v[160:163], v[192:195], v[22:25]
	v_mfma_f32_16x16x32_bf16 v[22:25], v[156:159], v[188:191], v[22:25]
	v_mfma_f32_16x16x32_bf16 v[38:41], v[156:159], v[180:183], v[38:41]
	v_mfma_f32_16x16x32_bf16 v[38:41], v[160:163], v[184:187], v[38:41]
	v_mfma_f32_16x16x32_bf16 v[26:29], v[168:171], v[184:187], v[26:29]
	v_mfma_f32_16x16x32_bf16 v[26:29], v[164:167], v[180:183], v[26:29]
	v_mfma_f32_16x16x32_bf16 v[42:45], v[164:167], v[172:175], v[42:45]
	v_mfma_f32_16x16x32_bf16 v[42:45], v[168:171], v[176:179], v[42:45]
	v_mfma_f32_16x16x32_bf16 v[54:57], v[160:163], v[176:179], v[54:57]
	v_mfma_f32_16x16x32_bf16 v[54:57], v[156:159], v[172:175], v[54:57]
	s_setprio 0
	s_barrier
	s_add_u32 s4, s4, 0xc000
	s_mov_b32 m0, s46
	s_addc_u32 s5, s5, 0
	s_add_i32 s59, s59, 2
	global_load_lds_dwordx4 v130, s[4:5]
	s_mov_b32 m0, s47
	s_add_u32 s55, s55, 0x10000
	global_load_lds_dwordx4 v142, s[4:5]
	s_addc_u32 s56, s56, 0
	s_add_u32 s57, s57, 0x10000
	s_addc_u32 s58, s58, 0
	s_cmp_gt_u32 s59, 61
	s_cbranch_scc0 .LBB0_918
	s_and_b64 vcc, exec, s[16:17]
	s_cbranch_vccz .LBB0_921
	s_barrier

; #define PG8_STAGE(bufoff, gbase, voff) do { const char* _gb = (const char*)(gbase); asm volatile("" : "+s"(_gb)); _Pragma("unroll") for (int _i = 0; _i < 2; ++_i) \
;         __builtin_amdgcn_global_load_lds((const unsigned*)(_gb + (voff)[_i]), (PG8_LAS unsigned*)(lds + (bufoff) + ldsw + _i * 8192), 16, 0, 0); } while (0)
; #define PG8_LDA(dst, b, h) do { _Pragma("unroll") for (int m = 0; m < 4; ++m) _Pragma("unroll") for (int k = 0; k < 2; ++k) dst[m][k] = *(const PG8_LAS bf16x8*)(lds + PG8_SA(b, h) + aoff + m * 2048 + k * 1024); } while (0)
; #define PG8_MMA(ai, bj, At, Bt) do { __builtin_amdgcn_s_setprio(1); _Pragma("unroll") for (int m = 0; m < 4; ++m) _Pragma("unroll") for (int n = 0; n < 2; ++n) _Pragma("unroll") for (int k = 0; k < 2; ++k) \
;         acc[ai][bj][m][n] = __builtin_amdgcn_mfma_f32_16x16x32_bf16(Bt[n][k], At[m][k], acc[ai][bj][m][n], 0, 0, 0); __builtin_amdgcn_s_setprio(0); } while (0)
; #define PG8_WAIT_L(n) asm volatile("s_waitcnt lgkmcnt(" #n ")" ::: "memory")
; #define PG8_BAR __builtin_amdgcn_s_barrier()
; #define PG8_SCHED __builtin_amdgcn_sched_barrier(0)
; template <class Epi, class Sched, bool ALIGN_EPI = false, bool SP2 = false, bool HALFM = false>
; __device__ __forceinline__ void gemm_phase(PG8_LAS unsigned char* lds, const Gemm g, const Sched& S, const Epi& E) {
;     ...
;             PG8_WAIT_V8R; PG8_WAIT_L(0); PG8_BAR; PG8_MMA(0, 0, At, B0); PG8_MMA(0, 1, At, B1); PG8_BAR; PG8_SCHED;
;             if constexpr (!HALFM) { PG8_LDA(At, 0, 1); } PG8_STAGE(PG8_SB(0, 0), b2, voffB); PG8_STAGE(PG8_SB(0, 1), b2 + hstep, voffB); PG8_STAGE(PG8_SA(0, 0), a2, voffA);
;             PG8_WAIT_V8R; PG8_WAIT_L(0); PG8_BAR; if constexpr (!HALFM) { PG8_MMA(1, 0, At, B0); PG8_MMA(1, 1, At, B1); } PG8_BAR; PG8_SCHED;
.Lry6:
	s_waitcnt lgkmcnt(0)
	s_barrier
	s_setprio 1
	s_waitcnt lgkmcnt(0)
	v_mfma_f32_16x16x32_bf16 v[126:129], v[130:133], v[162:165], v[126:129]
	v_mfma_f32_16x16x32_bf16 v[126:129], v[134:137], v[166:169], v[126:129]
	v_mfma_f32_16x16x32_bf16 v[122:125], v[142:145], v[166:169], v[122:125]
	v_mfma_f32_16x16x32_bf16 v[122:125], v[138:141], v[162:165], v[122:125]
	v_mfma_f32_16x16x32_bf16 v[106:109], v[138:141], v[174:177], v[106:109]
	v_mfma_f32_16x16x32_bf16 v[106:109], v[142:145], v[178:181], v[106:109]
	v_mfma_f32_16x16x32_bf16 v[110:113], v[134:137], v[178:181], v[110:113]
	v_mfma_f32_16x16x32_bf16 v[110:113], v[130:133], v[174:177], v[110:113]
	v_mfma_f32_16x16x32_bf16 v[94:97], v[130:133], v[182:185], v[94:97]
	v_mfma_f32_16x16x32_bf16 v[94:97], v[134:137], v[186:189], v[94:97]
	v_mfma_f32_16x16x32_bf16 v[90:93], v[142:145], v[186:189], v[90:93]
	v_mfma_f32_16x16x32_bf16 v[90:93], v[138:141], v[182:185], v[90:93]
	v_mfma_f32_16x16x32_bf16 v[74:77], v[138:141], v[190:193], v[74:77]
	v_mfma_f32_16x16x32_bf16 v[74:77], v[142:145], v[194:197], v[74:77]
	v_mfma_f32_16x16x32_bf16 v[78:81], v[134:137], v[194:197], v[78:81]
	v_mfma_f32_16x16x32_bf16 v[78:81], v[130:133], v[190:193], v[78:81]
	s_setprio 0
	s_setprio 1
	v_mfma_f32_16x16x32_bf16 v[70:73], v[146:149], v[190:193], v[70:73]
	v_mfma_f32_16x16x32_bf16 v[70:73], v[150:153], v[194:197], v[70:73]
	v_mfma_f32_16x16x32_bf16 v[66:69], v[158:161], v[194:197], v[66:69]
	v_mfma_f32_16x16x32_bf16 v[66:69], v[154:157], v[190:193], v[66:69]
	v_mfma_f32_16x16x32_bf16 v[82:85], v[154:157], v[182:185], v[82:85]
	v_mfma_f32_16x16x32_bf16 v[82:85], v[158:161], v[186:189], v[82:85]
	v_mfma_f32_16x16x32_bf16 v[86:89], v[150:153], v[186:189], v[86:89]
	v_mfma_f32_16x16x32_bf16 v[86:89], v[146:149], v[182:185], v[86:89]
	v_mfma_f32_16x16x32_bf16 v[102:105], v[146:149], v[174:177], v[102:105]
	v_mfma_f32_16x16x32_bf16 v[102:105], v[150:153], v[178:181], v[102:105]
	v_mfma_f32_16x16x32_bf16 v[98:101], v[158:161], v[178:181], v[98:101]
	v_mfma_f32_16x16x32_bf16 v[98:101], v[154:157], v[174:177], v[98:101]
	v_mfma_f32_16x16x32_bf16 v[114:117], v[154:157], v[162:165], v[114:117]
	v_mfma_f32_16x16x32_bf16 v[114:117], v[158:161], v[166:169], v[114:117]
	v_mfma_f32_16x16x32_bf16 v[118:121], v[150:153], v[166:169], v[118:121]
	v_mfma_f32_16x16x32_bf16 v[118:121], v[146:149], v[162:165], v[118:121]
	s_setprio 0
	s_barrier
	s_add_i32 s69, s54, s3
	s_mov_b64 s[66:67], s[34:35]
	s_mov_b32 m0, s69
	ds_read_b128 v[162:165], v211 offset:16384
	ds_read_b128 v[166:169], v211 offset:17408
	ds_read_b128 v[174:177], v211 offset:18432
	ds_read_b128 v[178:181], v211 offset:19456
	ds_read_b128 v[182:185], v211 offset:20480
	ds_read_b128 v[186:189], v211 offset:21504
	ds_read_b128 v[190:193], v211 offset:22528
	ds_read_b128 v[194:197], v211 offset:23552
	s_nop 0
	global_load_lds_dwordx4 v170, s[66:67]
	s_add_i32 m0, s69, 0x2000
	s_nop 0
	global_load_lds_dwordx4 v171, s[66:67]
	s_add_u32 s66, s34, 0x4000
	s_addc_u32 s67, s35, 0
	s_add_i32 s69, s55, s3
	s_mov_b32 m0, s69
	s_nop 0
	global_load_lds_dwordx4 v170, s[66:67]
	s_add_i32 m0, s69, 0x2000
	s_nop 0
	global_load_lds_dwordx4 v171, s[66:67]
	s_mov_b64 s[66:67], s[28:29]
	s_mov_b32 m0, s25
	s_nop 0
	global_load_lds_dwordx4 v170, s[66:67]
	s_mov_b32 m0, s27
	s_nop 0
	global_load_lds_dwordx4 v171, s[66:67]
	s_cmp_eq_u32 s68, 0
	s_cbranch_scc1 .Lrx7
	s_waitcnt vmcnt(40)
	s_branch .Lry7

; #define PG8_STAGE(bufoff, gbase, voff) do { const char* _gb = (const char*)(gbase); asm volatile("" : "+s"(_gb)); _Pragma("unroll") for (int _i = 0; _i < 2; ++_i) \
;         __builtin_amdgcn_global_load_lds((const unsigned*)(_gb + (voff)[_i]), (PG8_LAS unsigned*)(lds + (bufoff) + ldsw + _i * 8192), 16, 0, 0); } while (0)
; #define PG8_LDA(dst, b, h) do { _Pragma("unroll") for (int m = 0; m < 4; ++m) _Pragma("unroll") for (int k = 0; k < 2; ++k) dst[m][k] = *(const PG8_LAS bf16x8*)(lds + PG8_SA(b, h) + aoff + m * 2048 + k * 1024); } while (0)
; #define PG8_LDB(dst, b, h) do { _Pragma("unroll") for (int n = 0; n < 2; ++n) _Pragma("unroll") for (int k = 0; k < 2; ++k) dst[n][k] = *(const PG8_LAS bf16x8*)(lds + PG8_SB(b, h) + boff + n * 2048 + k * 1024); } while (0)
; #define PG8_MMA(ai, bj, At, Bt) do { __builtin_amdgcn_s_setprio(1); _Pragma("unroll") for (int m = 0; m < 4; ++m) _Pragma("unroll") for (int n = 0; n < 2; ++n) _Pragma("unroll") for (int k = 0; k < 2; ++k) \
;         acc[ai][bj][m][n] = __builtin_amdgcn_mfma_f32_16x16x32_bf16(Bt[n][k], At[m][k], acc[ai][bj][m][n], 0, 0, 0); __builtin_amdgcn_s_setprio(0); } while (0)
; #define PG8_WAIT_L(n) asm volatile("s_waitcnt lgkmcnt(" #n ")" ::: "memory")
; #define PG8_BAR __builtin_amdgcn_s_barrier()
; #define PG8_SCHED __builtin_amdgcn_sched_barrier(0)
; template <class Epi, class Sched, bool ALIGN_EPI = false, bool SP2 = false, bool HALFM = false>
; __device__ __forceinline__ void gemm_phase(PG8_LAS unsigned char* lds, const Gemm g, const Sched& S, const Epi& E) {
;     ...
;             PG8_WAIT_V8R; PG8_WAIT_L(0); PG8_BAR; if constexpr (!HALFM) { PG8_MMA(1, 0, At, B0); PG8_MMA(1, 1, At, B1); } PG8_BAR; PG8_SCHED;
;             PG8_LDB(B0, 1, 0); PG8_LDB(B1, 1, 1); PG8_SCHED; PG8_LDA(At, 1, 0); PG8_STAGE(PG8_SA(0, 1), a2 + hstepA, voffA);
;             PG8_WAIT_V8R; PG8_WAIT_L(0); PG8_BAR; PG8_MMA(0, 0, At, B0); PG8_MMA(0, 1, At, B1); PG8_BAR; PG8_SCHED;
.Lry7:
	s_waitcnt lgkmcnt(0)
	s_barrier
	s_setprio 1
	s_waitcnt lgkmcnt(0)
	v_mfma_f32_16x16x32_bf16 v[62:65], v[130:133], v[162:165], v[62:65]
	v_mfma_f32_16x16x32_bf16 v[62:65], v[134:137], v[166:169], v[62:65]
	v_mfma_f32_16x16x32_bf16 v[58:61], v[142:145], v[166:169], v[58:61]
	v_mfma_f32_16x16x32_bf16 v[58:61], v[138:141], v[162:165], v[58:61]
	v_mfma_f32_16x16x32_bf16 v[42:45], v[138:141], v[174:177], v[42:45]
	v_mfma_f32_16x16x32_bf16 v[42:45], v[142:145], v[178:181], v[42:45]
	v_mfma_f32_16x16x32_bf16 v[46:49], v[134:137], v[178:181], v[46:49]
	v_mfma_f32_16x16x32_bf16 v[46:49], v[130:133], v[174:177], v[46:49]
	v_mfma_f32_16x16x32_bf16 v[30:33], v[130:133], v[182:185], v[30:33]
	v_mfma_f32_16x16x32_bf16 v[30:33], v[134:137], v[186:189], v[30:33]
	v_mfma_f32_16x16x32_bf16 v[26:29], v[142:145], v[186:189], v[26:29]
	v_mfma_f32_16x16x32_bf16 v[26:29], v[138:141], v[182:185], v[26:29]
	v_mfma_f32_16x16x32_bf16 v[10:13], v[138:141], v[190:193], v[10:13]
	v_mfma_f32_16x16x32_bf16 v[10:13], v[142:145], v[194:197], v[10:13]
	v_mfma_f32_16x16x32_bf16 v[14:17], v[134:137], v[194:197], v[14:17]
	v_mfma_f32_16x16x32_bf16 v[14:17], v[130:133], v[190:193], v[14:17]
	s_setprio 0
	s_setprio 1
	v_mfma_f32_16x16x32_bf16 v[6:9], v[146:149], v[190:193], v[6:9]
	v_mfma_f32_16x16x32_bf16 v[6:9], v[150:153], v[194:197], v[6:9]
	v_mfma_f32_16x16x32_bf16 v[2:5], v[158:161], v[194:197], v[2:5]
	v_mfma_f32_16x16x32_bf16 v[2:5], v[154:157], v[190:193], v[2:5]
	v_mfma_f32_16x16x32_bf16 v[18:21], v[154:157], v[182:185], v[18:21]
	v_mfma_f32_16x16x32_bf16 v[18:21], v[158:161], v[186:189], v[18:21]
	v_mfma_f32_16x16x32_bf16 v[22:25], v[150:153], v[186:189], v[22:25]
	v_mfma_f32_16x16x32_bf16 v[22:25], v[146:149], v[182:185], v[22:25]
	v_mfma_f32_16x16x32_bf16 v[38:41], v[146:149], v[174:177], v[38:41]
	v_mfma_f32_16x16x32_bf16 v[38:41], v[150:153], v[178:181], v[38:41]
	v_mfma_f32_16x16x32_bf16 v[34:37], v[158:161], v[178:181], v[34:37]
	v_mfma_f32_16x16x32_bf16 v[34:37], v[154:157], v[174:177], v[34:37]
	v_mfma_f32_16x16x32_bf16 v[50:53], v[154:157], v[162:165], v[50:53]
	v_mfma_f32_16x16x32_bf16 v[50:53], v[158:161], v[166:169], v[50:53]
	v_mfma_f32_16x16x32_bf16 v[54:57], v[150:153], v[166:169], v[54:57]
	v_mfma_f32_16x16x32_bf16 v[54:57], v[146:149], v[162:165], v[54:57]
	s_setprio 0
	s_barrier
	s_add_i32 s69, 0, 0x18000
	s_add_i32 s70, 0, 0x1c000
	v_add_u32_e32 v142, s69, v206
	v_add_u32_e32 v158, s70, v206
	ds_read_b128 v[130:133], v142
	ds_read_b128 v[134:137], v142 offset:1024
	ds_read_b128 v[138:141], v142 offset:2048
	ds_read_b128 v[142:145], v142 offset:3072
	ds_read_b128 v[146:149], v158
	ds_read_b128 v[150:153], v158 offset:1024
	ds_read_b128 v[154:157], v158 offset:2048
	ds_read_b128 v[158:161], v158 offset:3072
	s_add_u32 s66, s28, 0x4000
	s_addc_u32 s67, s29, 0
	s_mov_b32 m0, s39
	ds_read_b128 v[162:165], v211 offset:32768
	ds_read_b128 v[166:169], v211 offset:33792
	ds_read_b128 v[174:177], v211 offset:34816
	ds_read_b128 v[178:181], v211 offset:35840
	ds_read_b128 v[182:185], v211 offset:36864
	ds_read_b128 v[186:189], v211 offset:37888
	ds_read_b128 v[190:193], v211 offset:38912
	ds_read_b128 v[194:197], v211 offset:39936
	s_nop 0
	global_load_lds_dwordx4 v170, s[66:67]
	s_mov_b32 m0, s40
	s_nop 0
	global_load_lds_dwordx4 v171, s[66:67]
	s_cmp_eq_u32 s68, 0
	s_cbranch_scc1 .Lrx8
	s_waitcnt vmcnt(40)
	s_branch .Lry8

; #define PG8_STAGE(bufoff, gbase, voff) do { const char* _gb = (const char*)(gbase); asm volatile("" : "+s"(_gb)); _Pragma("unroll") for (int _i = 0; _i < 2; ++_i) \
;         __builtin_amdgcn_global_load_lds((const unsigned*)(_gb + (voff)[_i]), (PG8_LAS unsigned*)(lds + (bufoff) + ldsw + _i * 8192), 16, 0, 0); } while (0)
; #define PG8_LDA(dst, b, h) do { _Pragma("unroll") for (int m = 0; m < 4; ++m) _Pragma("unroll") for (int k = 0; k < 2; ++k) dst[m][k] = *(const PG8_LAS bf16x8*)(lds + PG8_SA(b, h) + aoff + m * 2048 + k * 1024); } while (0)
; #define PG8_MMA(ai, bj, At, Bt) do { __builtin_amdgcn_s_setprio(1); _Pragma("unroll") for (int m = 0; m < 4; ++m) _Pragma("unroll") for (int n = 0; n < 2; ++n) _Pragma("unroll") for (int k = 0; k < 2; ++k) \
;         acc[ai][bj][m][n] = __builtin_amdgcn_mfma_f32_16x16x32_bf16(Bt[n][k], At[m][k], acc[ai][bj][m][n], 0, 0, 0); __builtin_amdgcn_s_setprio(0); } while (0)
; #define PG8_WAIT_V(n) asm volatile("s_waitcnt vmcnt(" #n ")" ::: "memory")
; #define PG8_WAIT_L(n) asm volatile("s_waitcnt lgkmcnt(" #n ")" ::: "memory")
; #define PG8_BAR __builtin_amdgcn_s_barrier()
; #define PG8_SCHED __builtin_amdgcn_sched_barrier(0)
; template <class Epi, class Sched, bool ALIGN_EPI = false, bool SP2 = false, bool HALFM = false>
; __device__ __forceinline__ void gemm_phase(PG8_LAS unsigned char* lds, const Gemm g, const Sched& S, const Epi& E) {
;     ...
;             PG8_WAIT_V8R; PG8_WAIT_L(0); PG8_BAR; PG8_MMA(0, 0, At, B0); PG8_MMA(0, 1, At, B1); PG8_BAR; PG8_SCHED;
;             if constexpr (!HALFM) { PG8_LDA(At, 1, 1); } PG8_STAGE(PG8_SB(1, 0), b3, voffB); PG8_STAGE(PG8_SB(1, 1), b3 + hstep, voffB); PG8_STAGE(PG8_SA(1, 0), a3, voffA);
;             PG8_WAIT_V(8); PG8_WAIT_L(0); PG8_BAR; if constexpr (!HALFM) { PG8_MMA(1, 0, At, B0); PG8_MMA(1, 1, At, B1); } PG8_BAR; PG8_SCHED;
;             PG8_STAGE(PG8_SA(1, 1), a3 + hstepA, voffA);
.Lry8:
	s_waitcnt lgkmcnt(0)
	s_barrier
	s_setprio 1
	s_waitcnt lgkmcnt(0)
	v_mfma_f32_16x16x32_bf16 v[126:129], v[130:133], v[162:165], v[126:129]
	v_mfma_f32_16x16x32_bf16 v[126:129], v[134:137], v[166:169], v[126:129]
	v_mfma_f32_16x16x32_bf16 v[122:125], v[142:145], v[166:169], v[122:125]
	v_mfma_f32_16x16x32_bf16 v[122:125], v[138:141], v[162:165], v[122:125]
	v_mfma_f32_16x16x32_bf16 v[106:109], v[138:141], v[174:177], v[106:109]
	v_mfma_f32_16x16x32_bf16 v[106:109], v[142:145], v[178:181], v[106:109]
	v_mfma_f32_16x16x32_bf16 v[110:113], v[134:137], v[178:181], v[110:113]
	v_mfma_f32_16x16x32_bf16 v[110:113], v[130:133], v[174:177], v[110:113]
	v_mfma_f32_16x16x32_bf16 v[94:97], v[130:133], v[182:185], v[94:97]
	v_mfma_f32_16x16x32_bf16 v[94:97], v[134:137], v[186:189], v[94:97]
	v_mfma_f32_16x16x32_bf16 v[90:93], v[142:145], v[186:189], v[90:93]
	v_mfma_f32_16x16x32_bf16 v[90:93], v[138:141], v[182:185], v[90:93]
	v_mfma_f32_16x16x32_bf16 v[74:77], v[138:141], v[190:193], v[74:77]
	v_mfma_f32_16x16x32_bf16 v[74:77], v[142:145], v[194:197], v[74:77]
	v_mfma_f32_16x16x32_bf16 v[78:81], v[134:137], v[194:197], v[78:81]
	v_mfma_f32_16x16x32_bf16 v[78:81], v[130:133], v[190:193], v[78:81]
	s_setprio 0
	s_setprio 1
	v_mfma_f32_16x16x32_bf16 v[70:73], v[146:149], v[190:193], v[70:73]
	v_mfma_f32_16x16x32_bf16 v[70:73], v[150:153], v[194:197], v[70:73]
	v_mfma_f32_16x16x32_bf16 v[66:69], v[158:161], v[194:197], v[66:69]
	v_mfma_f32_16x16x32_bf16 v[66:69], v[154:157], v[190:193], v[66:69]
	v_mfma_f32_16x16x32_bf16 v[82:85], v[154:157], v[182:185], v[82:85]
	v_mfma_f32_16x16x32_bf16 v[82:85], v[158:161], v[186:189], v[82:85]
	v_mfma_f32_16x16x32_bf16 v[86:89], v[150:153], v[186:189], v[86:89]
	v_mfma_f32_16x16x32_bf16 v[86:89], v[146:149], v[182:185], v[86:89]
	v_mfma_f32_16x16x32_bf16 v[102:105], v[146:149], v[174:177], v[102:105]
	v_mfma_f32_16x16x32_bf16 v[102:105], v[150:153], v[178:181], v[102:105]
	v_mfma_f32_16x16x32_bf16 v[98:101], v[158:161], v[178:181], v[98:101]
	v_mfma_f32_16x16x32_bf16 v[98:101], v[154:157], v[174:177], v[98:101]
	v_mfma_f32_16x16x32_bf16 v[114:117], v[154:157], v[162:165], v[114:117]
	v_mfma_f32_16x16x32_bf16 v[114:117], v[158:161], v[166:169], v[114:117]
	v_mfma_f32_16x16x32_bf16 v[118:121], v[150:153], v[166:169], v[118:121]
	v_mfma_f32_16x16x32_bf16 v[118:121], v[146:149], v[162:165], v[118:121]
	s_setprio 0
	s_barrier
	s_add_u32 s66, s34, 0x8000
	s_addc_u32 s67, s35, 0
	s_add_i32 s68, s69, s3
	s_mov_b32 m0, s68
	ds_read_b128 v[162:165], v211 offset:49152
	ds_read_b128 v[166:169], v211 offset:50176
	ds_read_b128 v[174:177], v211 offset:51200
	ds_read_b128 v[178:181], v211 offset:52224
	ds_read_b128 v[182:185], v211 offset:53248
	ds_read_b128 v[186:189], v211 offset:54272
	ds_read_b128 v[190:193], v211 offset:55296
	ds_read_b128 v[194:197], v211 offset:56320
	s_nop 0
	global_load_lds_dwordx4 v170, s[66:67]
	s_add_i32 m0, s68, 0x2000
	s_add_u32 s34, s34, 0xc000
	global_load_lds_dwordx4 v171, s[66:67]
	s_addc_u32 s35, s35, 0
	s_add_i32 s66, s70, s3
	s_mov_b32 m0, s66
	s_nop 0
	global_load_lds_dwordx4 v170, s[34:35]
	s_add_i32 m0, s66, 0x2000
	s_nop 0
	global_load_lds_dwordx4 v171, s[34:35]
	s_mov_b32 m0, s45
	s_nop 0
	global_load_lds_dwordx4 v170, s[30:31]
	s_mov_b32 m0, s46
	s_nop 0
	global_load_lds_dwordx4 v171, s[30:31]
	s_waitcnt vmcnt(8)
	s_waitcnt lgkmcnt(0)
	s_barrier
	s_setprio 1
	s_waitcnt lgkmcnt(0)
	v_mfma_f32_16x16x32_bf16 v[62:65], v[130:133], v[162:165], v[62:65]
	v_mfma_f32_16x16x32_bf16 v[62:65], v[134:137], v[166:169], v[62:65]
	v_mfma_f32_16x16x32_bf16 v[58:61], v[142:145], v[166:169], v[58:61]
	v_mfma_f32_16x16x32_bf16 v[58:61], v[138:141], v[162:165], v[58:61]
	v_mfma_f32_16x16x32_bf16 v[42:45], v[138:141], v[174:177], v[42:45]
	v_mfma_f32_16x16x32_bf16 v[42:45], v[142:145], v[178:181], v[42:45]
	v_mfma_f32_16x16x32_bf16 v[46:49], v[134:137], v[178:181], v[46:49]
	v_mfma_f32_16x16x32_bf16 v[46:49], v[130:133], v[174:177], v[46:49]
	v_mfma_f32_16x16x32_bf16 v[30:33], v[130:133], v[182:185], v[30:33]
	v_mfma_f32_16x16x32_bf16 v[30:33], v[134:137], v[186:189], v[30:33]
	v_mfma_f32_16x16x32_bf16 v[26:29], v[142:145], v[186:189], v[26:29]
	v_mfma_f32_16x16x32_bf16 v[26:29], v[138:141], v[182:185], v[26:29]
	v_mfma_f32_16x16x32_bf16 v[10:13], v[138:141], v[190:193], v[10:13]
	v_mfma_f32_16x16x32_bf16 v[10:13], v[142:145], v[194:197], v[10:13]
	v_mfma_f32_16x16x32_bf16 v[14:17], v[134:137], v[194:197], v[14:17]
	v_mfma_f32_16x16x32_bf16 v[14:17], v[130:133], v[190:193], v[14:17]
	s_setprio 0
	s_setprio 1
	v_mfma_f32_16x16x32_bf16 v[6:9], v[146:149], v[190:193], v[6:9]
	v_mfma_f32_16x16x32_bf16 v[6:9], v[150:153], v[194:197], v[6:9]
	v_mfma_f32_16x16x32_bf16 v[2:5], v[158:161], v[194:197], v[2:5]
	v_mfma_f32_16x16x32_bf16 v[2:5], v[154:157], v[190:193], v[2:5]
	v_mfma_f32_16x16x32_bf16 v[18:21], v[154:157], v[182:185], v[18:21]
	v_mfma_f32_16x16x32_bf16 v[18:21], v[158:161], v[186:189], v[18:21]
	v_mfma_f32_16x16x32_bf16 v[22:25], v[150:153], v[186:189], v[22:25]
	v_mfma_f32_16x16x32_bf16 v[22:25], v[146:149], v[182:185], v[22:25]
	v_mfma_f32_16x16x32_bf16 v[38:41], v[146:149], v[174:177], v[38:41]
	v_mfma_f32_16x16x32_bf16 v[38:41], v[150:153], v[178:181], v[38:41]
	v_mfma_f32_16x16x32_bf16 v[34:37], v[158:161], v[178:181], v[34:37]
	v_mfma_f32_16x16x32_bf16 v[34:37], v[154:157], v[174:177], v[34:37]
	v_mfma_f32_16x16x32_bf16 v[50:53], v[154:157], v[162:165], v[50:53]
	v_mfma_f32_16x16x32_bf16 v[50:53], v[158:161], v[166:169], v[50:53]
	v_mfma_f32_16x16x32_bf16 v[54:57], v[150:153], v[166:169], v[54:57]
	v_mfma_f32_16x16x32_bf16 v[54:57], v[146:149], v[162:165], v[54:57]
	s_setprio 0
	s_barrier
	s_add_u32 s28, s28, 0xc000
	s_mov_b32 m0, s47
	s_addc_u32 s29, s29, 0
	s_add_i32 s65, s65, 2
	global_load_lds_dwordx4 v170, s[28:29]
	s_mov_b32 m0, s48
	s_add_u32 s61, s61, 0x10000
	global_load_lds_dwordx4 v171, s[28:29]
	s_addc_u32 s62, s62, 0
	s_add_u32 s63, s63, 0x10000
	s_addc_u32 s64, s64, 0
	s_cmp_gt_u32 s65, 5
	s_cbranch_scc0 .LBB0_1079
	s_and_b64 vcc, exec, s[12:13]
	s_cbranch_vccz .LBB0_1082
	s_barrier

; #define PG8_STAGE(bufoff, gbase, voff) do { const char* _gb = (const char*)(gbase); asm volatile("" : "+s"(_gb)); _Pragma("unroll") for (int _i = 0; _i < 2; ++_i) \
;         __builtin_amdgcn_global_load_lds((const unsigned*)(_gb + (voff)[_i]), (PG8_LAS unsigned*)(lds + (bufoff) + ldsw + _i * 8192), 16, 0, 0); } while (0)
; #define PG8_LDA(dst, b, h) do { _Pragma("unroll") for (int m = 0; m < 4; ++m) _Pragma("unroll") for (int k = 0; k < 2; ++k) dst[m][k] = *(const PG8_LAS bf16x8*)(lds + PG8_SA(b, h) + aoff + m * 2048 + k * 1024); } while (0)
; #define PG8_MMA(ai, bj, At, Bt) do { __builtin_amdgcn_s_setprio(1); _Pragma("unroll") for (int m = 0; m < 4; ++m) _Pragma("unroll") for (int n = 0; n < 2; ++n) _Pragma("unroll") for (int k = 0; k < 2; ++k) \
;         acc[ai][bj][m][n] = __builtin_amdgcn_mfma_f32_16x16x32_bf16(Bt[n][k], At[m][k], acc[ai][bj][m][n], 0, 0, 0); __builtin_amdgcn_s_setprio(0); } while (0)
; #define PG8_WAIT_L(n) asm volatile("s_waitcnt lgkmcnt(" #n ")" ::: "memory")
; #define PG8_BAR __builtin_amdgcn_s_barrier()
; #define PG8_SCHED __builtin_amdgcn_sched_barrier(0)
; template <class Epi, class Sched, bool ALIGN_EPI = false, bool SP2 = false, bool HALFM = false>
; __device__ __forceinline__ void gemm_phase(PG8_LAS unsigned char* lds, const Gemm g, const Sched& S, const Epi& E) {
;     ...
;             PG8_WAIT_V8R; PG8_WAIT_L(0); PG8_BAR; PG8_MMA(0, 0, At, B0); PG8_MMA(0, 1, At, B1); PG8_BAR; PG8_SCHED;
;             if constexpr (!HALFM) { PG8_LDA(At, 0, 1); } PG8_STAGE(PG8_SB(0, 0), b2, voffB); PG8_STAGE(PG8_SB(0, 1), b2 + hstep, voffB); PG8_STAGE(PG8_SA(0, 0), a2, voffA);
;             PG8_WAIT_V8R; PG8_WAIT_L(0); PG8_BAR; if constexpr (!HALFM) { PG8_MMA(1, 0, At, B0); PG8_MMA(1, 1, At, B1); } PG8_BAR; PG8_SCHED;
.Lry9:
	s_waitcnt lgkmcnt(0)
	s_barrier
	s_setprio 1
	s_waitcnt lgkmcnt(0)
	v_mfma_f32_16x16x32_bf16 v[126:129], v[134:137], v[180:183], v[126:129]
	v_mfma_f32_16x16x32_bf16 v[126:129], v[138:141], v[184:187], v[126:129]
	v_mfma_f32_16x16x32_bf16 v[66:69], v[160:163], v[184:187], v[66:69]
	v_mfma_f32_16x16x32_bf16 v[66:69], v[142:145], v[180:183], v[66:69]
	v_mfma_f32_16x16x32_bf16 v[58:61], v[142:145], v[188:191], v[58:61]
	v_mfma_f32_16x16x32_bf16 v[58:61], v[160:163], v[192:195], v[58:61]
	v_mfma_f32_16x16x32_bf16 v[122:125], v[138:141], v[192:195], v[122:125]
	v_mfma_f32_16x16x32_bf16 v[122:125], v[134:137], v[188:191], v[122:125]
	v_mfma_f32_16x16x32_bf16 v[118:121], v[134:137], v[196:199], v[118:121]
	v_mfma_f32_16x16x32_bf16 v[118:121], v[138:141], v[200:203], v[118:121]
	v_mfma_f32_16x16x32_bf16 v[54:57], v[160:163], v[200:203], v[54:57]
	v_mfma_f32_16x16x32_bf16 v[54:57], v[142:145], v[196:199], v[54:57]
	v_mfma_f32_16x16x32_bf16 v[50:53], v[142:145], v[204:207], v[50:53]
	v_mfma_f32_16x16x32_bf16 v[50:53], v[160:163], v[218:221], v[50:53]
	v_mfma_f32_16x16x32_bf16 v[114:117], v[138:141], v[218:221], v[114:117]
	v_mfma_f32_16x16x32_bf16 v[114:117], v[134:137], v[204:207], v[114:117]
	s_setprio 0
	s_setprio 1
	v_mfma_f32_16x16x32_bf16 v[98:101], v[164:167], v[204:207], v[98:101]
	v_mfma_f32_16x16x32_bf16 v[98:101], v[168:171], v[218:221], v[98:101]
	v_mfma_f32_16x16x32_bf16 v[34:37], v[176:179], v[218:221], v[34:37]
	v_mfma_f32_16x16x32_bf16 v[34:37], v[172:175], v[204:207], v[34:37]
	v_mfma_f32_16x16x32_bf16 v[38:41], v[172:175], v[196:199], v[38:41]
	v_mfma_f32_16x16x32_bf16 v[38:41], v[176:179], v[200:203], v[38:41]
	v_mfma_f32_16x16x32_bf16 v[102:105], v[168:171], v[200:203], v[102:105]
	v_mfma_f32_16x16x32_bf16 v[102:105], v[164:167], v[196:199], v[102:105]
	v_mfma_f32_16x16x32_bf16 v[106:109], v[164:167], v[188:191], v[106:109]
	v_mfma_f32_16x16x32_bf16 v[106:109], v[168:171], v[192:195], v[106:109]
	v_mfma_f32_16x16x32_bf16 v[42:45], v[176:179], v[192:195], v[42:45]
	v_mfma_f32_16x16x32_bf16 v[42:45], v[172:175], v[188:191], v[42:45]
	v_mfma_f32_16x16x32_bf16 v[46:49], v[172:175], v[180:183], v[46:49]
	v_mfma_f32_16x16x32_bf16 v[46:49], v[176:179], v[184:187], v[46:49]
	v_mfma_f32_16x16x32_bf16 v[110:113], v[168:171], v[184:187], v[110:113]
	v_mfma_f32_16x16x32_bf16 v[110:113], v[164:167], v[180:183], v[110:113]
	s_setprio 0
	s_barrier
	s_add_i32 vcc_lo, s81, s60
	s_mov_b64 s[96:97], s[46:47]
	s_mov_b32 m0, vcc_lo
	ds_read_b128 v[180:183], v214 offset:16384
	ds_read_b128 v[184:187], v214 offset:17408
	ds_read_b128 v[188:191], v214 offset:18432
	ds_read_b128 v[192:195], v214 offset:19456
	ds_read_b128 v[196:199], v214 offset:20480
	ds_read_b128 v[200:203], v214 offset:21504
	ds_read_b128 v[204:207], v214 offset:22528
	ds_read_b128 v[218:221], v214 offset:23552
	s_nop 0
	global_load_lds_dwordx4 v217, s[96:97]
	s_add_i32 m0, vcc_lo, 0x2000
	s_nop 0
	global_load_lds_dwordx4 v216, s[96:97]
	s_add_u32 s96, s46, 0x4000
	s_addc_u32 s97, s47, 0
	s_add_i32 vcc_lo, s86, s60
	s_mov_b32 m0, vcc_lo
	s_nop 0
	global_load_lds_dwordx4 v217, s[96:97]
	s_add_i32 m0, vcc_lo, 0x2000
	s_nop 0
	global_load_lds_dwordx4 v216, s[96:97]
	s_mov_b64 s[96:97], s[4:5]
	s_mov_b32 m0, s61
	s_nop 0
	global_load_lds_dwordx4 v217, s[96:97]
	s_mov_b32 m0, s62
	s_nop 0
	global_load_lds_dwordx4 v216, s[96:97]
	s_cmp_eq_u32 s95, 0
	s_cbranch_scc1 .Lrx10
	s_waitcnt vmcnt(20)
	s_branch .Lry10

; #define PG8_STAGE(bufoff, gbase, voff) do { const char* _gb = (const char*)(gbase); asm volatile("" : "+s"(_gb)); _Pragma("unroll") for (int _i = 0; _i < 2; ++_i) \
;         __builtin_amdgcn_global_load_lds((const unsigned*)(_gb + (voff)[_i]), (PG8_LAS unsigned*)(lds + (bufoff) + ldsw + _i * 8192), 16, 0, 0); } while (0)
; #define PG8_LDA(dst, b, h) do { _Pragma("unroll") for (int m = 0; m < 4; ++m) _Pragma("unroll") for (int k = 0; k < 2; ++k) dst[m][k] = *(const PG8_LAS bf16x8*)(lds + PG8_SA(b, h) + aoff + m * 2048 + k * 1024); } while (0)
; #define PG8_LDB(dst, b, h) do { _Pragma("unroll") for (int n = 0; n < 2; ++n) _Pragma("unroll") for (int k = 0; k < 2; ++k) dst[n][k] = *(const PG8_LAS bf16x8*)(lds + PG8_SB(b, h) + boff + n * 2048 + k * 1024); } while (0)
; #define PG8_MMA(ai, bj, At, Bt) do { __builtin_amdgcn_s_setprio(1); _Pragma("unroll") for (int m = 0; m < 4; ++m) _Pragma("unroll") for (int n = 0; n < 2; ++n) _Pragma("unroll") for (int k = 0; k < 2; ++k) \
;         acc[ai][bj][m][n] = __builtin_amdgcn_mfma_f32_16x16x32_bf16(Bt[n][k], At[m][k], acc[ai][bj][m][n], 0, 0, 0); __builtin_amdgcn_s_setprio(0); } while (0)
; #define PG8_WAIT_L(n) asm volatile("s_waitcnt lgkmcnt(" #n ")" ::: "memory")
; #define PG8_BAR __builtin_amdgcn_s_barrier()
; #define PG8_SCHED __builtin_amdgcn_sched_barrier(0)
; template <class Epi, class Sched, bool ALIGN_EPI = false, bool SP2 = false, bool HALFM = false>
; __device__ __forceinline__ void gemm_phase(PG8_LAS unsigned char* lds, const Gemm g, const Sched& S, const Epi& E) {
;     ...
;             PG8_WAIT_V8R; PG8_WAIT_L(0); PG8_BAR; if constexpr (!HALFM) { PG8_MMA(1, 0, At, B0); PG8_MMA(1, 1, At, B1); } PG8_BAR; PG8_SCHED;
;             PG8_LDB(B0, 1, 0); PG8_LDB(B1, 1, 1); PG8_SCHED; PG8_LDA(At, 1, 0); PG8_STAGE(PG8_SA(0, 1), a2 + hstepA, voffA);
;             PG8_WAIT_V8R; PG8_WAIT_L(0); PG8_BAR; PG8_MMA(0, 0, At, B0); PG8_MMA(0, 1, At, B1); PG8_BAR; PG8_SCHED;
.Lry10:
	s_waitcnt lgkmcnt(0)
	s_barrier
	s_setprio 1
	s_waitcnt lgkmcnt(0)
	v_mfma_f32_16x16x32_bf16 v[94:97], v[134:137], v[180:183], v[94:97]
	v_mfma_f32_16x16x32_bf16 v[94:97], v[138:141], v[184:187], v[94:97]
	v_mfma_f32_16x16x32_bf16 v[30:33], v[160:163], v[184:187], v[30:33]
	v_mfma_f32_16x16x32_bf16 v[30:33], v[142:145], v[180:183], v[30:33]
	v_mfma_f32_16x16x32_bf16 v[26:29], v[142:145], v[188:191], v[26:29]
	v_mfma_f32_16x16x32_bf16 v[26:29], v[160:163], v[192:195], v[26:29]
	v_mfma_f32_16x16x32_bf16 v[90:93], v[138:141], v[192:195], v[90:93]
	v_mfma_f32_16x16x32_bf16 v[90:93], v[134:137], v[188:191], v[90:93]
	v_mfma_f32_16x16x32_bf16 v[86:89], v[134:137], v[196:199], v[86:89]
	v_mfma_f32_16x16x32_bf16 v[86:89], v[138:141], v[200:203], v[86:89]
	v_mfma_f32_16x16x32_bf16 v[22:25], v[160:163], v[200:203], v[22:25]
	v_mfma_f32_16x16x32_bf16 v[22:25], v[142:145], v[196:199], v[22:25]
	v_mfma_f32_16x16x32_bf16 v[18:21], v[142:145], v[204:207], v[18:21]
	v_mfma_f32_16x16x32_bf16 v[18:21], v[160:163], v[218:221], v[18:21]
	v_mfma_f32_16x16x32_bf16 v[82:85], v[138:141], v[218:221], v[82:85]
	v_mfma_f32_16x16x32_bf16 v[82:85], v[134:137], v[204:207], v[82:85]
	s_setprio 0
	s_setprio 1
	v_mfma_f32_16x16x32_bf16 v[62:65], v[164:167], v[204:207], v[62:65]
	v_mfma_f32_16x16x32_bf16 v[62:65], v[168:171], v[218:221], v[62:65]
	v_mfma_f32_16x16x32_bf16 v[2:5], v[176:179], v[218:221], v[2:5]
	v_mfma_f32_16x16x32_bf16 v[2:5], v[172:175], v[204:207], v[2:5]
	v_mfma_f32_16x16x32_bf16 v[6:9], v[172:175], v[196:199], v[6:9]
	v_mfma_f32_16x16x32_bf16 v[6:9], v[176:179], v[200:203], v[6:9]
	v_mfma_f32_16x16x32_bf16 v[70:73], v[168:171], v[200:203], v[70:73]
	v_mfma_f32_16x16x32_bf16 v[70:73], v[164:167], v[196:199], v[70:73]
	v_mfma_f32_16x16x32_bf16 v[74:77], v[164:167], v[188:191], v[74:77]
	v_mfma_f32_16x16x32_bf16 v[74:77], v[168:171], v[192:195], v[74:77]
	v_mfma_f32_16x16x32_bf16 v[10:13], v[176:179], v[192:195], v[10:13]
	v_mfma_f32_16x16x32_bf16 v[10:13], v[172:175], v[188:191], v[10:13]
	v_mfma_f32_16x16x32_bf16 v[14:17], v[172:175], v[180:183], v[14:17]
	v_mfma_f32_16x16x32_bf16 v[14:17], v[176:179], v[184:187], v[14:17]
	v_mfma_f32_16x16x32_bf16 v[78:81], v[168:171], v[184:187], v[78:81]
	v_mfma_f32_16x16x32_bf16 v[78:81], v[164:167], v[180:183], v[78:81]
	s_setprio 0
	s_barrier
	s_add_i32 vcc_lo, 0, 0x18000
	v_add_u32_e32 v150, vcc_lo, v147
	s_add_i32 vcc_hi, 0, 0x1c000
	ds_read_b128 v[134:137], v150
	ds_read_b128 v[138:141], v150 offset:1024
	ds_read_b128 v[142:145], v150 offset:2048
	ds_read_b128 v[160:163], v150 offset:3072
	v_add_u32_e32 v150, vcc_hi, v147
	ds_read_b128 v[164:167], v150
	ds_read_b128 v[168:171], v150 offset:1024
	ds_read_b128 v[172:175], v150 offset:2048
	ds_read_b128 v[176:179], v150 offset:3072
	s_add_u32 s96, s4, 0x4000
	s_addc_u32 s97, s5, 0
	s_mov_b32 m0, s63
	ds_read_b128 v[180:183], v214 offset:32768
	ds_read_b128 v[184:187], v214 offset:33792
	ds_read_b128 v[188:191], v214 offset:34816
	ds_read_b128 v[192:195], v214 offset:35840
	ds_read_b128 v[196:199], v214 offset:36864
	ds_read_b128 v[200:203], v214 offset:37888
	ds_read_b128 v[204:207], v214 offset:38912
	ds_read_b128 v[218:221], v214 offset:39936
	s_nop 0
	global_load_lds_dwordx4 v217, s[96:97]
	s_mov_b32 m0, s64
	s_nop 0
	global_load_lds_dwordx4 v216, s[96:97]
	s_cmp_eq_u32 s95, 0
	s_cbranch_scc1 .Lrx11
	s_waitcnt vmcnt(20)
	s_branch .Lry11

; #define PG8_STAGE(bufoff, gbase, voff) do { const char* _gb = (const char*)(gbase); asm volatile("" : "+s"(_gb)); _Pragma("unroll") for (int _i = 0; _i < 2; ++_i) \
;         __builtin_amdgcn_global_load_lds((const unsigned*)(_gb + (voff)[_i]), (PG8_LAS unsigned*)(lds + (bufoff) + ldsw + _i * 8192), 16, 0, 0); } while (0)
; #define PG8_LDA(dst, b, h) do { _Pragma("unroll") for (int m = 0; m < 4; ++m) _Pragma("unroll") for (int k = 0; k < 2; ++k) dst[m][k] = *(const PG8_LAS bf16x8*)(lds + PG8_SA(b, h) + aoff + m * 2048 + k * 1024); } while (0)
; #define PG8_MMA(ai, bj, At, Bt) do { __builtin_amdgcn_s_setprio(1); _Pragma("unroll") for (int m = 0; m < 4; ++m) _Pragma("unroll") for (int n = 0; n < 2; ++n) _Pragma("unroll") for (int k = 0; k < 2; ++k) \
;         acc[ai][bj][m][n] = __builtin_amdgcn_mfma_f32_16x16x32_bf16(Bt[n][k], At[m][k], acc[ai][bj][m][n], 0, 0, 0); __builtin_amdgcn_s_setprio(0); } while (0)
; #define PG8_WAIT_V(n) asm volatile("s_waitcnt vmcnt(" #n ")" ::: "memory")
; #define PG8_WAIT_L(n) asm volatile("s_waitcnt lgkmcnt(" #n ")" ::: "memory")
; #define PG8_BAR __builtin_amdgcn_s_barrier()
; #define PG8_SCHED __builtin_amdgcn_sched_barrier(0)
; template <class Epi, class Sched, bool ALIGN_EPI = false, bool SP2 = false, bool HALFM = false>
; __device__ __forceinline__ void gemm_phase(PG8_LAS unsigned char* lds, const Gemm g, const Sched& S, const Epi& E) {
;     ...
;             PG8_WAIT_V8R; PG8_WAIT_L(0); PG8_BAR; PG8_MMA(0, 0, At, B0); PG8_MMA(0, 1, At, B1); PG8_BAR; PG8_SCHED;
;             if constexpr (!HALFM) { PG8_LDA(At, 1, 1); } PG8_STAGE(PG8_SB(1, 0), b3, voffB); PG8_STAGE(PG8_SB(1, 1), b3 + hstep, voffB); PG8_STAGE(PG8_SA(1, 0), a3, voffA);
;             PG8_WAIT_V(8); PG8_WAIT_L(0); PG8_BAR; if constexpr (!HALFM) { PG8_MMA(1, 0, At, B0); PG8_MMA(1, 1, At, B1); } PG8_BAR; PG8_SCHED;
;             PG8_STAGE(PG8_SA(1, 1), a3 + hstepA, voffA);
.Lry11:
	s_waitcnt lgkmcnt(0)
	s_barrier
	s_setprio 1
	s_waitcnt lgkmcnt(0)
	v_mfma_f32_16x16x32_bf16 v[126:129], v[134:137], v[180:183], v[126:129]
	v_mfma_f32_16x16x32_bf16 v[126:129], v[138:141], v[184:187], v[126:129]
	v_mfma_f32_16x16x32_bf16 v[66:69], v[160:163], v[184:187], v[66:69]
	v_mfma_f32_16x16x32_bf16 v[66:69], v[142:145], v[180:183], v[66:69]
	v_mfma_f32_16x16x32_bf16 v[58:61], v[142:145], v[188:191], v[58:61]
	v_mfma_f32_16x16x32_bf16 v[58:61], v[160:163], v[192:195], v[58:61]
	v_mfma_f32_16x16x32_bf16 v[122:125], v[138:141], v[192:195], v[122:125]
	v_mfma_f32_16x16x32_bf16 v[122:125], v[134:137], v[188:191], v[122:125]
	v_mfma_f32_16x16x32_bf16 v[118:121], v[134:137], v[196:199], v[118:121]
	v_mfma_f32_16x16x32_bf16 v[118:121], v[138:141], v[200:203], v[118:121]
	v_mfma_f32_16x16x32_bf16 v[54:57], v[160:163], v[200:203], v[54:57]
	v_mfma_f32_16x16x32_bf16 v[54:57], v[142:145], v[196:199], v[54:57]
	v_mfma_f32_16x16x32_bf16 v[50:53], v[142:145], v[204:207], v[50:53]
	v_mfma_f32_16x16x32_bf16 v[50:53], v[160:163], v[218:221], v[50:53]
	v_mfma_f32_16x16x32_bf16 v[114:117], v[138:141], v[218:221], v[114:117]
	v_mfma_f32_16x16x32_bf16 v[114:117], v[134:137], v[204:207], v[114:117]
	s_setprio 0
	s_setprio 1
	v_mfma_f32_16x16x32_bf16 v[98:101], v[164:167], v[204:207], v[98:101]
	v_mfma_f32_16x16x32_bf16 v[98:101], v[168:171], v[218:221], v[98:101]
	v_mfma_f32_16x16x32_bf16 v[34:37], v[176:179], v[218:221], v[34:37]
	v_mfma_f32_16x16x32_bf16 v[34:37], v[172:175], v[204:207], v[34:37]
	v_mfma_f32_16x16x32_bf16 v[38:41], v[172:175], v[196:199], v[38:41]
	v_mfma_f32_16x16x32_bf16 v[38:41], v[176:179], v[200:203], v[38:41]
	v_mfma_f32_16x16x32_bf16 v[102:105], v[168:171], v[200:203], v[102:105]
	v_mfma_f32_16x16x32_bf16 v[102:105], v[164:167], v[196:199], v[102:105]
	v_mfma_f32_16x16x32_bf16 v[106:109], v[164:167], v[188:191], v[106:109]
	v_mfma_f32_16x16x32_bf16 v[106:109], v[168:171], v[192:195], v[106:109]
	v_mfma_f32_16x16x32_bf16 v[42:45], v[176:179], v[192:195], v[42:45]
	v_mfma_f32_16x16x32_bf16 v[42:45], v[172:175], v[188:191], v[42:45]
	v_mfma_f32_16x16x32_bf16 v[46:49], v[172:175], v[180:183], v[46:49]
	v_mfma_f32_16x16x32_bf16 v[46:49], v[176:179], v[184:187], v[46:49]
	v_mfma_f32_16x16x32_bf16 v[110:113], v[168:171], v[184:187], v[110:113]
	v_mfma_f32_16x16x32_bf16 v[110:113], v[164:167], v[180:183], v[110:113]
	s_setprio 0
	s_barrier
	s_add_i32 s95, vcc_lo, s60
	s_mov_b32 m0, s95
	ds_read_b128 v[180:183], v214 offset:49152
	ds_read_b128 v[184:187], v214 offset:50176
	ds_read_b128 v[188:191], v214 offset:51200
	ds_read_b128 v[192:195], v214 offset:52224
	ds_read_b128 v[196:199], v214 offset:53248
	ds_read_b128 v[200:203], v214 offset:54272
	ds_read_b128 v[204:207], v214 offset:55296
	ds_read_b128 v[218:221], v214 offset:56320
	s_nop 0
	global_load_lds_dwordx4 v217, s[50:51]
	s_add_i32 m0, s95, 0x2000
	s_add_u32 s46, s46, 0xc000
	global_load_lds_dwordx4 v216, s[50:51]
	s_addc_u32 s47, s47, 0
	s_add_i32 s50, vcc_hi, s60
	s_mov_b32 m0, s50
	s_nop 0
	global_load_lds_dwordx4 v217, s[46:47]
	s_add_i32 m0, s50, 0x2000
	s_nop 0
	global_load_lds_dwordx4 v216, s[46:47]
	s_mov_b32 m0, s67
	s_nop 0
	global_load_lds_dwordx4 v217, s[48:49]
	s_mov_b32 m0, s68
	s_nop 0
	global_load_lds_dwordx4 v216, s[48:49]
	s_waitcnt vmcnt(8)
	s_waitcnt lgkmcnt(0)
	s_barrier
	s_setprio 1
	s_waitcnt lgkmcnt(0)
	v_mfma_f32_16x16x32_bf16 v[94:97], v[134:137], v[180:183], v[94:97]
	v_mfma_f32_16x16x32_bf16 v[94:97], v[138:141], v[184:187], v[94:97]
	v_mfma_f32_16x16x32_bf16 v[30:33], v[160:163], v[184:187], v[30:33]
	v_mfma_f32_16x16x32_bf16 v[30:33], v[142:145], v[180:183], v[30:33]
	v_mfma_f32_16x16x32_bf16 v[26:29], v[142:145], v[188:191], v[26:29]
	v_mfma_f32_16x16x32_bf16 v[26:29], v[160:163], v[192:195], v[26:29]
	v_mfma_f32_16x16x32_bf16 v[90:93], v[138:141], v[192:195], v[90:93]
	v_mfma_f32_16x16x32_bf16 v[90:93], v[134:137], v[188:191], v[90:93]
	v_mfma_f32_16x16x32_bf16 v[86:89], v[134:137], v[196:199], v[86:89]
	v_mfma_f32_16x16x32_bf16 v[86:89], v[138:141], v[200:203], v[86:89]
	v_mfma_f32_16x16x32_bf16 v[22:25], v[160:163], v[200:203], v[22:25]
	v_mfma_f32_16x16x32_bf16 v[22:25], v[142:145], v[196:199], v[22:25]
	v_mfma_f32_16x16x32_bf16 v[18:21], v[142:145], v[204:207], v[18:21]
	v_mfma_f32_16x16x32_bf16 v[18:21], v[160:163], v[218:221], v[18:21]
	v_mfma_f32_16x16x32_bf16 v[82:85], v[138:141], v[218:221], v[82:85]
	v_mfma_f32_16x16x32_bf16 v[82:85], v[134:137], v[204:207], v[82:85]
	s_setprio 0
	s_setprio 1
	v_mfma_f32_16x16x32_bf16 v[62:65], v[164:167], v[204:207], v[62:65]
	v_mfma_f32_16x16x32_bf16 v[62:65], v[168:171], v[218:221], v[62:65]
	v_mfma_f32_16x16x32_bf16 v[2:5], v[176:179], v[218:221], v[2:5]
	v_mfma_f32_16x16x32_bf16 v[2:5], v[172:175], v[204:207], v[2:5]
	v_mfma_f32_16x16x32_bf16 v[6:9], v[172:175], v[196:199], v[6:9]
	v_mfma_f32_16x16x32_bf16 v[6:9], v[176:179], v[200:203], v[6:9]
	v_mfma_f32_16x16x32_bf16 v[70:73], v[168:171], v[200:203], v[70:73]
	v_mfma_f32_16x16x32_bf16 v[70:73], v[164:167], v[196:199], v[70:73]
	v_mfma_f32_16x16x32_bf16 v[74:77], v[164:167], v[188:191], v[74:77]
	v_mfma_f32_16x16x32_bf16 v[74:77], v[168:171], v[192:195], v[74:77]
	v_mfma_f32_16x16x32_bf16 v[10:13], v[176:179], v[192:195], v[10:13]
	v_mfma_f32_16x16x32_bf16 v[10:13], v[172:175], v[188:191], v[10:13]
	v_mfma_f32_16x16x32_bf16 v[14:17], v[172:175], v[180:183], v[14:17]
	v_mfma_f32_16x16x32_bf16 v[14:17], v[176:179], v[184:187], v[14:17]
	v_mfma_f32_16x16x32_bf16 v[78:81], v[168:171], v[184:187], v[78:81]
	v_mfma_f32_16x16x32_bf16 v[78:81], v[164:167], v[180:183], v[78:81]
	s_setprio 0
	s_barrier
	s_add_u32 s4, s4, 0xc000
	s_mov_b32 m0, s69
	s_addc_u32 s5, s5, 0
	s_add_i32 s94, s94, 2
	global_load_lds_dwordx4 v217, s[4:5]
	s_mov_b32 m0, s70
	s_add_u32 s13, s13, 0x10000
	global_load_lds_dwordx4 v216, s[4:5]
	s_addc_u32 s15, s15, 0
	s_add_u32 s91, s91, 0x10000
	s_addc_u32 s93, s93, 0
	s_cmp_gt_u32 s94, 61
	s_cbranch_scc1 .LBB0_1175

; #define PG8_STAGE(bufoff, gbase, voff) do { const char* _gb = (const char*)(gbase); asm volatile("" : "+s"(_gb)); _Pragma("unroll") for (int _i = 0; _i < 2; ++_i) \
;         __builtin_amdgcn_global_load_lds((const unsigned*)(_gb + (voff)[_i]), (PG8_LAS unsigned*)(lds + (bufoff) + ldsw + _i * 8192), 16, 0, 0); } while (0)
; #define PG8_LDA(dst, b, h) do { _Pragma("unroll") for (int m = 0; m < 4; ++m) _Pragma("unroll") for (int k = 0; k < 2; ++k) dst[m][k] = *(const PG8_LAS bf16x8*)(lds + PG8_SA(b, h) + aoff + m * 2048 + k * 1024); } while (0)
; #define PG8_LDB(dst, b, h) do { _Pragma("unroll") for (int n = 0; n < 2; ++n) _Pragma("unroll") for (int k = 0; k < 2; ++k) dst[n][k] = *(const PG8_LAS bf16x8*)(lds + PG8_SB(b, h) + boff + n * 2048 + k * 1024); } while (0)
; template <class Epi, class Sched, bool ALIGN_EPI = false, bool SP2 = false, bool HALFM = false>
; __device__ __forceinline__ void gemm_phase(PG8_LAS unsigned char* lds, const Gemm g, const Sched& S, const Epi& E) {
;     ...
;         for (int t = 0; t < nt; t += 2) {
;             const bool last = (t == nt - 2);
;             const char* a1 = cA + (size_t)(t + 1) * kstep;
;             const char* a2 = last ? nA : cA + (size_t)(t + 2) * kstep; const char* b2 = last ? nB : cB + (size_t)(t + 2) * kstep;
;             const char* a3 = a2 + kstep; const char* b3 = b2 + kstep;
;             if (last && has_next) S.a_ready(nxt);
;             if constexpr (Epi::HAS_PREFETCH) { if (last) E.prefetch(cur, wid, lane); }
;             asm volatile("" : "+v"(voffA[0]), "+v"(voffA[1])); voffB[0] = voffA[0]; voffB[1] = voffA[1];
;             if constexpr (SP2) {
;             PG8_LDB(B0, 0, 0); PG8_LDB(B1, 0, 1); PG8_SCHED; PG8_LDA(At, 0, 0);
;             PG8_WAIT_V8R; PG8_WAIT_L(0); PG8_BAR; PG8_MMA(0, 0, At, B0); PG8_MMA(0, 1, At, B1); PG8_BAR; PG8_SCHED;
;             if constexpr (!HALFM) { PG8_LDA(At, 0, 1); } PG8_STAGE(PG8_SB(0, 0), b2, voffB); PG8_STAGE(PG8_SB(0, 1), b2 + hstep, voffB); PG8_STAGE(PG8_SA(0, 0), a2, voffA);
;             PG8_WAIT_V8R; PG8_WAIT_L(0); PG8_BAR; if constexpr (!HALFM) { PG8_MMA(1, 0, At, B0); PG8_MMA(1, 1, At, B1); } PG8_BAR; PG8_SCHED;
;             PG8_LDB(B0, 1, 0); PG8_LDB(B1, 1, 1); PG8_SCHED; PG8_LDA(At, 1, 0); PG8_STAGE(PG8_SA(0, 1), a2 + hstepA, voffA);
;             PG8_WAIT_V8R; PG8_WAIT_L(0); PG8_BAR; PG8_MMA(0, 0, At, B0); PG8_MMA(0, 1, At, B1); PG8_BAR; PG8_SCHED;
.LBB0_1242:
	v_add_u32_e32 v90, s65, v134
	v_add_u32_e32 v106, s66, v134
	ds_read_b128 v[70:73], v90
	ds_read_b128 v[74:77], v90 offset:1024
	ds_read_b128 v[78:81], v90 offset:2048
	ds_read_b128 v[90:93], v90 offset:3072
	ds_read_b128 v[94:97], v106
	ds_read_b128 v[98:101], v106 offset:1024
	ds_read_b128 v[102:105], v106 offset:2048
	ds_read_b128 v[106:109], v106 offset:3072
	s_and_b64 s[14:15], s[14:15], exec
	s_cselect_b32 s14, s70, s5
	s_cselect_b32 s15, s37, s13
	s_cselect_b32 s45, s23, s77
	s_cselect_b32 s44, s71, s76
	s_add_u32 s46, s14, 0x8000
	s_addc_u32 s47, s15, 0
	s_add_u32 s48, s44, 0x8000
	s_addc_u32 s49, s45, 0
	ds_read_b128 v[110:113], v136
	ds_read_b128 v[114:117], v136 offset:1024
	ds_read_b128 v[118:121], v136 offset:2048
	ds_read_b128 v[122:125], v136 offset:3072
	ds_read_b128 v[126:129], v136 offset:4096
	ds_read_b128 v[130:133], v136 offset:5120
	ds_read_b128 v[140:143], v136 offset:6144
	ds_read_b128 v[150:153], v136 offset:7168
	s_waitcnt vmcnt(8)
	s_waitcnt lgkmcnt(0)
	s_barrier
	s_setprio 1
	s_waitcnt lgkmcnt(0)
	v_mfma_f32_16x16x32_bf16 v[62:65], v[70:73], v[110:113], v[62:65]
	v_mfma_f32_16x16x32_bf16 v[62:65], v[74:77], v[114:117], v[62:65]
	v_mfma_f32_16x16x32_bf16 v[30:33], v[90:93], v[114:117], v[30:33]
	v_mfma_f32_16x16x32_bf16 v[30:33], v[78:81], v[110:113], v[30:33]
	v_mfma_f32_16x16x32_bf16 v[26:29], v[78:81], v[118:121], v[26:29]
	v_mfma_f32_16x16x32_bf16 v[26:29], v[90:93], v[122:125], v[26:29]
	v_mfma_f32_16x16x32_bf16 v[58:61], v[74:77], v[122:125], v[58:61]
	v_mfma_f32_16x16x32_bf16 v[58:61], v[70:73], v[118:121], v[58:61]
	v_mfma_f32_16x16x32_bf16 v[54:57], v[70:73], v[126:129], v[54:57]
	v_mfma_f32_16x16x32_bf16 v[54:57], v[74:77], v[130:133], v[54:57]
	v_mfma_f32_16x16x32_bf16 v[22:25], v[90:93], v[130:133], v[22:25]
	v_mfma_f32_16x16x32_bf16 v[22:25], v[78:81], v[126:129], v[22:25]
	v_mfma_f32_16x16x32_bf16 v[18:21], v[78:81], v[140:143], v[18:21]
	v_mfma_f32_16x16x32_bf16 v[18:21], v[90:93], v[150:153], v[18:21]
	v_mfma_f32_16x16x32_bf16 v[50:53], v[74:77], v[150:153], v[50:53]
	v_mfma_f32_16x16x32_bf16 v[50:53], v[70:73], v[140:143], v[50:53]
	s_setprio 0
	s_setprio 1
	v_mfma_f32_16x16x32_bf16 v[34:37], v[94:97], v[140:143], v[34:37]
	v_mfma_f32_16x16x32_bf16 v[34:37], v[98:101], v[150:153], v[34:37]
	v_mfma_f32_16x16x32_bf16 v[2:5], v[106:109], v[150:153], v[2:5]
	v_mfma_f32_16x16x32_bf16 v[2:5], v[102:105], v[140:143], v[2:5]
	v_mfma_f32_16x16x32_bf16 v[6:9], v[102:105], v[126:129], v[6:9]
	v_mfma_f32_16x16x32_bf16 v[6:9], v[106:109], v[130:133], v[6:9]
	v_mfma_f32_16x16x32_bf16 v[38:41], v[98:101], v[130:133], v[38:41]
	v_mfma_f32_16x16x32_bf16 v[38:41], v[94:97], v[126:129], v[38:41]
	v_mfma_f32_16x16x32_bf16 v[42:45], v[94:97], v[118:121], v[42:45]
	v_mfma_f32_16x16x32_bf16 v[42:45], v[98:101], v[122:125], v[42:45]
	v_mfma_f32_16x16x32_bf16 v[10:13], v[106:109], v[122:125], v[10:13]
	v_mfma_f32_16x16x32_bf16 v[10:13], v[102:105], v[118:121], v[10:13]
	v_mfma_f32_16x16x32_bf16 v[14:17], v[102:105], v[110:113], v[14:17]
	v_mfma_f32_16x16x32_bf16 v[14:17], v[106:109], v[114:117], v[14:17]
	v_mfma_f32_16x16x32_bf16 v[46:49], v[98:101], v[114:117], v[46:49]
	v_mfma_f32_16x16x32_bf16 v[46:49], v[94:97], v[110:113], v[46:49]
	s_setprio 0
	s_barrier
	s_add_i32 s88, s65, s3
	s_mov_b64 s[86:87], s[44:45]
	s_mov_b32 m0, s88
	s_nop 0
	global_load_lds_dwordx4 v138, s[86:87]
	s_add_i32 m0, s88, 0x2000
	s_nop 0
	global_load_lds_dwordx4 v149, s[86:87]
	s_add_u32 s86, s44, 0x4000
	s_addc_u32 s87, s45, 0
	s_add_i32 s88, s66, s3
	s_mov_b32 m0, s88
	s_nop 0
	global_load_lds_dwordx4 v138, s[86:87]
	s_add_i32 m0, s88, 0x2000
	s_nop 0
	global_load_lds_dwordx4 v149, s[86:87]
	s_mov_b64 s[86:87], s[14:15]
	s_mov_b32 m0, s33
	s_nop 0
	global_load_lds_dwordx4 v138, s[86:87]
	s_mov_b32 m0, s50
	s_nop 0
	global_load_lds_dwordx4 v149, s[86:87]
	s_waitcnt vmcnt(8)
	s_waitcnt lgkmcnt(0)
	s_barrier
	s_barrier
; #define PG8_STAGE(bufoff, gbase, voff) do { const char* _gb = (const char*)(gbase); asm volatile("" : "+s"(_gb)); _Pragma("unroll") for (int _i = 0; _i < 2; ++_i) \
;         __builtin_amdgcn_global_load_lds((const unsigned*)(_gb + (voff)[_i]), (PG8_LAS unsigned*)(lds + (bufoff) + ldsw + _i * 8192), 16, 0, 0); } while (0)
; #define PG8_LDA(dst, b, h) do { _Pragma("unroll") for (int m = 0; m < 4; ++m) _Pragma("unroll") for (int k = 0; k < 2; ++k) dst[m][k] = *(const PG8_LAS bf16x8*)(lds + PG8_SA(b, h) + aoff + m * 2048 + k * 1024); } while (0)
; #define PG8_LDB(dst, b, h) do { _Pragma("unroll") for (int n = 0; n < 2; ++n) _Pragma("unroll") for (int k = 0; k < 2; ++k) dst[n][k] = *(const PG8_LAS bf16x8*)(lds + PG8_SB(b, h) + boff + n * 2048 + k * 1024); } while (0)
; #define PG8_MMA(ai, bj, At, Bt) do { __builtin_amdgcn_s_setprio(1); _Pragma("unroll") for (int m = 0; m < 4; ++m) _Pragma("unroll") for (int n = 0; n < 2; ++n) _Pragma("unroll") for (int k = 0; k < 2; ++k) \
;         acc[ai][bj][m][n] = __builtin_amdgcn_mfma_f32_16x16x32_bf16(Bt[n][k], At[m][k], acc[ai][bj][m][n], 0, 0, 0); __builtin_amdgcn_s_setprio(0); } while (0)
; #define PG8_WAIT_V(n) asm volatile("s_waitcnt vmcnt(" #n ")" ::: "memory")
; #define PG8_WAIT_L(n) asm volatile("s_waitcnt lgkmcnt(" #n ")" ::: "memory")
; #define PG8_BAR __builtin_amdgcn_s_barrier()
; #define PG8_SCHED __builtin_amdgcn_sched_barrier(0)
; template <class Epi, class Sched, bool ALIGN_EPI = false, bool SP2 = false, bool HALFM = false>
; __device__ __forceinline__ void gemm_phase(PG8_LAS unsigned char* lds, const Gemm g, const Sched& S, const Epi& E) {
;     ...
;             PG8_LDB(B0, 1, 0); PG8_LDB(B1, 1, 1); PG8_SCHED; PG8_LDA(At, 1, 0); PG8_STAGE(PG8_SA(0, 1), a2 + hstepA, voffA);
;             PG8_WAIT_V8R; PG8_WAIT_L(0); PG8_BAR; PG8_MMA(0, 0, At, B0); PG8_MMA(0, 1, At, B1); PG8_BAR; PG8_SCHED;
;             if constexpr (!HALFM) { PG8_LDA(At, 1, 1); } PG8_STAGE(PG8_SB(1, 0), b3, voffB); PG8_STAGE(PG8_SB(1, 1), b3 + hstep, voffB); PG8_STAGE(PG8_SA(1, 0), a3, voffA);
;             PG8_WAIT_V(8); PG8_WAIT_L(0); PG8_BAR; if constexpr (!HALFM) { PG8_MMA(1, 0, At, B0); PG8_MMA(1, 1, At, B1); } PG8_BAR; PG8_SCHED;
;             PG8_STAGE(PG8_SA(1, 1), a3 + hstepA, voffA);
	s_add_i32 s88, 0, 0x18000
	s_add_i32 s89, 0, 0x1c000
	v_add_u32_e32 v90, s88, v134
	v_add_u32_e32 v106, s89, v134
	ds_read_b128 v[70:73], v90
	ds_read_b128 v[74:77], v90 offset:1024
	ds_read_b128 v[78:81], v90 offset:2048
	ds_read_b128 v[90:93], v90 offset:3072
	ds_read_b128 v[94:97], v106
	ds_read_b128 v[98:101], v106 offset:1024
	ds_read_b128 v[102:105], v106 offset:2048
	ds_read_b128 v[106:109], v106 offset:3072
	s_add_u32 s86, s14, 0x4000
	s_addc_u32 s87, s15, 0
	s_mov_b32 m0, s51
	ds_read_b128 v[110:113], v136 offset:32768
	ds_read_b128 v[114:117], v136 offset:33792
	ds_read_b128 v[118:121], v136 offset:34816
	ds_read_b128 v[122:125], v136 offset:35840
	ds_read_b128 v[126:129], v136 offset:36864
	ds_read_b128 v[130:133], v136 offset:37888
	ds_read_b128 v[140:143], v136 offset:38912
	ds_read_b128 v[150:153], v136 offset:39936
	s_nop 0
	global_load_lds_dwordx4 v138, s[86:87]
	s_mov_b32 m0, s56
	s_nop 0
	global_load_lds_dwordx4 v149, s[86:87]
	s_waitcnt vmcnt(8)
	s_waitcnt lgkmcnt(0)
	s_barrier
	s_setprio 1
	s_waitcnt lgkmcnt(0)
	v_mfma_f32_16x16x32_bf16 v[62:65], v[70:73], v[110:113], v[62:65]
	v_mfma_f32_16x16x32_bf16 v[62:65], v[74:77], v[114:117], v[62:65]
	v_mfma_f32_16x16x32_bf16 v[30:33], v[90:93], v[114:117], v[30:33]
	v_mfma_f32_16x16x32_bf16 v[30:33], v[78:81], v[110:113], v[30:33]
	v_mfma_f32_16x16x32_bf16 v[26:29], v[78:81], v[118:121], v[26:29]
	v_mfma_f32_16x16x32_bf16 v[26:29], v[90:93], v[122:125], v[26:29]
	v_mfma_f32_16x16x32_bf16 v[58:61], v[74:77], v[122:125], v[58:61]
	v_mfma_f32_16x16x32_bf16 v[58:61], v[70:73], v[118:121], v[58:61]
	v_mfma_f32_16x16x32_bf16 v[54:57], v[70:73], v[126:129], v[54:57]
	v_mfma_f32_16x16x32_bf16 v[54:57], v[74:77], v[130:133], v[54:57]
	v_mfma_f32_16x16x32_bf16 v[22:25], v[90:93], v[130:133], v[22:25]
	v_mfma_f32_16x16x32_bf16 v[22:25], v[78:81], v[126:129], v[22:25]
	v_mfma_f32_16x16x32_bf16 v[18:21], v[78:81], v[140:143], v[18:21]
	v_mfma_f32_16x16x32_bf16 v[18:21], v[90:93], v[150:153], v[18:21]
	v_mfma_f32_16x16x32_bf16 v[50:53], v[74:77], v[150:153], v[50:53]
	v_mfma_f32_16x16x32_bf16 v[50:53], v[70:73], v[140:143], v[50:53]
	s_setprio 0
	s_setprio 1
	v_mfma_f32_16x16x32_bf16 v[34:37], v[94:97], v[140:143], v[34:37]
	v_mfma_f32_16x16x32_bf16 v[34:37], v[98:101], v[150:153], v[34:37]
	v_mfma_f32_16x16x32_bf16 v[2:5], v[106:109], v[150:153], v[2:5]
	v_mfma_f32_16x16x32_bf16 v[2:5], v[102:105], v[140:143], v[2:5]
	v_mfma_f32_16x16x32_bf16 v[6:9], v[102:105], v[126:129], v[6:9]
	v_mfma_f32_16x16x32_bf16 v[6:9], v[106:109], v[130:133], v[6:9]
	v_mfma_f32_16x16x32_bf16 v[38:41], v[98:101], v[130:133], v[38:41]
	v_mfma_f32_16x16x32_bf16 v[38:41], v[94:97], v[126:129], v[38:41]
	v_mfma_f32_16x16x32_bf16 v[42:45], v[94:97], v[118:121], v[42:45]
	v_mfma_f32_16x16x32_bf16 v[42:45], v[98:101], v[122:125], v[42:45]
	v_mfma_f32_16x16x32_bf16 v[10:13], v[106:109], v[122:125], v[10:13]
	v_mfma_f32_16x16x32_bf16 v[10:13], v[102:105], v[118:121], v[10:13]
	v_mfma_f32_16x16x32_bf16 v[14:17], v[102:105], v[110:113], v[14:17]
	v_mfma_f32_16x16x32_bf16 v[14:17], v[106:109], v[114:117], v[14:17]
	v_mfma_f32_16x16x32_bf16 v[46:49], v[98:101], v[114:117], v[46:49]
	v_mfma_f32_16x16x32_bf16 v[46:49], v[94:97], v[110:113], v[46:49]
	s_setprio 0
	s_barrier
	s_add_i32 s86, s88, s3
	s_mov_b32 m0, s86
	s_nop 0
	global_load_lds_dwordx4 v138, s[48:49]
	s_add_i32 m0, s86, 0x2000
	s_add_u32 s44, s44, 0xc000
	global_load_lds_dwordx4 v149, s[48:49]
	s_addc_u32 s45, s45, 0
	s_add_i32 s48, s89, s3
	s_mov_b32 m0, s48
	s_nop 0
	global_load_lds_dwordx4 v138, s[44:45]
	s_add_i32 m0, s48, 0x2000
	s_nop 0
	global_load_lds_dwordx4 v149, s[44:45]
	s_mov_b32 m0, s59
	s_nop 0
	global_load_lds_dwordx4 v138, s[46:47]
	s_mov_b32 m0, s60
	s_nop 0
	global_load_lds_dwordx4 v149, s[46:47]
	s_waitcnt vmcnt(8)
	s_waitcnt lgkmcnt(0)
	s_barrier
	s_barrier
	s_add_u32 s14, s14, 0xc000
	s_mov_b32 m0, s61
	s_addc_u32 s15, s15, 0
	s_add_i32 s81, s81, 2
	global_load_lds_dwordx4 v138, s[14:15]
	s_mov_b32 m0, s62
	s_add_u32 s5, s5, 0x10000
	global_load_lds_dwordx4 v149, s[14:15]
	s_addc_u32 s13, s13, 0
	s_add_u32 s76, s76, 0x10000
	s_addc_u32 s77, s77, 0
	s_cmp_gt_u32 s81, 61
	s_cbranch_scc1 .LBB0_1246

; #define PG8_STAGE(bufoff, gbase, voff) do { const char* _gb = (const char*)(gbase); asm volatile("" : "+s"(_gb)); _Pragma("unroll") for (int _i = 0; _i < 2; ++_i) \
;         __builtin_amdgcn_global_load_lds((const unsigned*)(_gb + (voff)[_i]), (PG8_LAS unsigned*)(lds + (bufoff) + ldsw + _i * 8192), 16, 0, 0); } while (0)
; #define PG8_LDA(dst, b, h) do { _Pragma("unroll") for (int m = 0; m < 4; ++m) _Pragma("unroll") for (int k = 0; k < 2; ++k) dst[m][k] = *(const PG8_LAS bf16x8*)(lds + PG8_SA(b, h) + aoff + m * 2048 + k * 1024); } while (0)
; #define PG8_MMA(ai, bj, At, Bt) do { __builtin_amdgcn_s_setprio(1); _Pragma("unroll") for (int m = 0; m < 4; ++m) _Pragma("unroll") for (int n = 0; n < 2; ++n) _Pragma("unroll") for (int k = 0; k < 2; ++k) \
;         acc[ai][bj][m][n] = __builtin_amdgcn_mfma_f32_16x16x32_bf16(Bt[n][k], At[m][k], acc[ai][bj][m][n], 0, 0, 0); __builtin_amdgcn_s_setprio(0); } while (0)
; #define PG8_WAIT_L(n) asm volatile("s_waitcnt lgkmcnt(" #n ")" ::: "memory")
; #define PG8_BAR __builtin_amdgcn_s_barrier()
; #define PG8_SCHED __builtin_amdgcn_sched_barrier(0)
; template <class Epi, class Sched, bool ALIGN_EPI = false, bool SP2 = false, bool HALFM = false>
; __device__ __forceinline__ void gemm_phase(PG8_LAS unsigned char* lds, const Gemm g, const Sched& S, const Epi& E) {
;     ...
;             PG8_WAIT_V8R; PG8_WAIT_L(0); PG8_BAR; PG8_MMA(0, 0, At, B0); PG8_MMA(0, 1, At, B1); PG8_BAR; PG8_SCHED;
;             if constexpr (!HALFM) { PG8_LDA(At, 0, 1); } PG8_STAGE(PG8_SB(0, 0), b2, voffB); PG8_STAGE(PG8_SB(0, 1), b2 + hstep, voffB); PG8_STAGE(PG8_SA(0, 0), a2, voffA);
.Lry12:
	s_waitcnt lgkmcnt(0)
	s_barrier
	s_setprio 1
	s_waitcnt lgkmcnt(0)
	v_mfma_f32_16x16x32_bf16 v[124:127], v[134:137], v[166:169], v[124:127]
	v_mfma_f32_16x16x32_bf16 v[124:127], v[138:141], v[170:173], v[124:127]
	v_mfma_f32_16x16x32_bf16 v[120:123], v[146:149], v[170:173], v[120:123]
	v_mfma_f32_16x16x32_bf16 v[120:123], v[142:145], v[166:169], v[120:123]
	v_mfma_f32_16x16x32_bf16 v[104:107], v[142:145], v[174:177], v[104:107]
	v_mfma_f32_16x16x32_bf16 v[104:107], v[146:149], v[178:181], v[104:107]
	v_mfma_f32_16x16x32_bf16 v[112:115], v[138:141], v[178:181], v[112:115]
	v_mfma_f32_16x16x32_bf16 v[112:115], v[134:137], v[174:177], v[112:115]
	v_mfma_f32_16x16x32_bf16 v[92:95], v[134:137], v[182:185], v[92:95]
	v_mfma_f32_16x16x32_bf16 v[92:95], v[138:141], v[198:201], v[92:95]
	v_mfma_f32_16x16x32_bf16 v[88:91], v[146:149], v[198:201], v[88:91]
	v_mfma_f32_16x16x32_bf16 v[88:91], v[142:145], v[182:185], v[88:91]
	v_mfma_f32_16x16x32_bf16 v[72:75], v[142:145], v[202:205], v[72:75]
	v_mfma_f32_16x16x32_bf16 v[72:75], v[146:149], v[206:209], v[72:75]
	v_mfma_f32_16x16x32_bf16 v[80:83], v[138:141], v[206:209], v[80:83]
	v_mfma_f32_16x16x32_bf16 v[80:83], v[134:137], v[202:205], v[80:83]
	s_setprio 0
	s_setprio 1
	v_mfma_f32_16x16x32_bf16 v[68:71], v[150:153], v[202:205], v[68:71]
	v_mfma_f32_16x16x32_bf16 v[68:71], v[154:157], v[206:209], v[68:71]
	v_mfma_f32_16x16x32_bf16 v[64:67], v[162:165], v[206:209], v[64:67]
	v_mfma_f32_16x16x32_bf16 v[64:67], v[158:161], v[202:205], v[64:67]
	v_mfma_f32_16x16x32_bf16 v[76:79], v[158:161], v[182:185], v[76:79]
	v_mfma_f32_16x16x32_bf16 v[76:79], v[162:165], v[198:201], v[76:79]
	v_mfma_f32_16x16x32_bf16 v[84:87], v[154:157], v[198:201], v[84:87]
	v_mfma_f32_16x16x32_bf16 v[84:87], v[150:153], v[182:185], v[84:87]
	v_mfma_f32_16x16x32_bf16 v[100:103], v[150:153], v[174:177], v[100:103]
	v_mfma_f32_16x16x32_bf16 v[100:103], v[154:157], v[178:181], v[100:103]
	v_mfma_f32_16x16x32_bf16 v[96:99], v[162:165], v[178:181], v[96:99]
	v_mfma_f32_16x16x32_bf16 v[96:99], v[158:161], v[174:177], v[96:99]
	v_mfma_f32_16x16x32_bf16 v[108:111], v[158:161], v[166:169], v[108:111]
	v_mfma_f32_16x16x32_bf16 v[108:111], v[162:165], v[170:173], v[108:111]
	v_mfma_f32_16x16x32_bf16 v[116:119], v[154:157], v[170:173], v[116:119]
	v_mfma_f32_16x16x32_bf16 v[116:119], v[150:153], v[166:169], v[116:119]
	s_setprio 0
	s_barrier
	s_add_i32 s58, s43, s20
	s_mov_b64 s[56:57], s[18:19]
	s_mov_b32 m0, s58
	ds_read_b128 v[166:169], v196 offset:16384
	ds_read_b128 v[170:173], v196 offset:17408
	ds_read_b128 v[174:177], v196 offset:18432
	ds_read_b128 v[178:181], v196 offset:19456
	ds_read_b128 v[182:185], v196 offset:20480
	ds_read_b128 v[198:201], v196 offset:21504
	ds_read_b128 v[202:205], v196 offset:22528
	ds_read_b128 v[206:209], v196 offset:23552
	s_nop 0
	global_load_lds_dwordx4 v197, s[56:57]
	s_add_i32 m0, s58, 0x2000
	s_nop 0
	global_load_lds_dwordx4 v186, s[56:57]
	s_add_u32 s56, s18, 0x4000
	s_addc_u32 s57, s19, 0
	s_add_i32 s58, s44, s20
	s_mov_b32 m0, s58
	s_nop 0
	global_load_lds_dwordx4 v197, s[56:57]
	s_add_i32 m0, s58, 0x2000
	s_nop 0
	global_load_lds_dwordx4 v186, s[56:57]
	s_mov_b64 s[56:57], s[14:15]
	s_mov_b32 m0, s25
	s_nop 0
	global_load_lds_dwordx4 v197, s[56:57]
	s_mov_b32 m0, s26
	s_nop 0
	global_load_lds_dwordx4 v186, s[56:57]
	s_cmp_eq_u32 s55, 0
	s_cbranch_scc1 .Lrx13
	s_waitcnt vmcnt(56)
	s_branch .Lry13

; #define PG8_STAGE(bufoff, gbase, voff) do { const char* _gb = (const char*)(gbase); asm volatile("" : "+s"(_gb)); _Pragma("unroll") for (int _i = 0; _i < 2; ++_i) \
;         __builtin_amdgcn_global_load_lds((const unsigned*)(_gb + (voff)[_i]), (PG8_LAS unsigned*)(lds + (bufoff) + ldsw + _i * 8192), 16, 0, 0); } while (0)
; #define PG8_LDA(dst, b, h) do { _Pragma("unroll") for (int m = 0; m < 4; ++m) _Pragma("unroll") for (int k = 0; k < 2; ++k) dst[m][k] = *(const PG8_LAS bf16x8*)(lds + PG8_SA(b, h) + aoff + m * 2048 + k * 1024); } while (0)
; #define PG8_LDB(dst, b, h) do { _Pragma("unroll") for (int n = 0; n < 2; ++n) _Pragma("unroll") for (int k = 0; k < 2; ++k) dst[n][k] = *(const PG8_LAS bf16x8*)(lds + PG8_SB(b, h) + boff + n * 2048 + k * 1024); } while (0)
; #define PG8_MMA(ai, bj, At, Bt) do { __builtin_amdgcn_s_setprio(1); _Pragma("unroll") for (int m = 0; m < 4; ++m) _Pragma("unroll") for (int n = 0; n < 2; ++n) _Pragma("unroll") for (int k = 0; k < 2; ++k) \
;         acc[ai][bj][m][n] = __builtin_amdgcn_mfma_f32_16x16x32_bf16(Bt[n][k], At[m][k], acc[ai][bj][m][n], 0, 0, 0); __builtin_amdgcn_s_setprio(0); } while (0)
; #define PG8_WAIT_L(n) asm volatile("s_waitcnt lgkmcnt(" #n ")" ::: "memory")
; #define PG8_BAR __builtin_amdgcn_s_barrier()
; #define PG8_SCHED __builtin_amdgcn_sched_barrier(0)
; template <class Epi, class Sched, bool ALIGN_EPI = false, bool SP2 = false, bool HALFM = false>
; __device__ __forceinline__ void gemm_phase(PG8_LAS unsigned char* lds, const Gemm g, const Sched& S, const Epi& E) {
;     ...
;             PG8_WAIT_V8R; PG8_WAIT_L(0); PG8_BAR; if constexpr (!HALFM) { PG8_MMA(1, 0, At, B0); PG8_MMA(1, 1, At, B1); } PG8_BAR; PG8_SCHED;
;             PG8_LDB(B0, 1, 0); PG8_LDB(B1, 1, 1); PG8_SCHED; PG8_LDA(At, 1, 0); PG8_STAGE(PG8_SA(0, 1), a2 + hstepA, voffA);
.Lry13:
	s_waitcnt lgkmcnt(0)
	s_barrier
	s_setprio 1
	s_waitcnt lgkmcnt(0)
	v_mfma_f32_16x16x32_bf16 v[60:63], v[134:137], v[166:169], v[60:63]
	v_mfma_f32_16x16x32_bf16 v[60:63], v[138:141], v[170:173], v[60:63]
	v_mfma_f32_16x16x32_bf16 v[56:59], v[146:149], v[170:173], v[56:59]
	v_mfma_f32_16x16x32_bf16 v[56:59], v[142:145], v[166:169], v[56:59]
	v_mfma_f32_16x16x32_bf16 v[40:43], v[142:145], v[174:177], v[40:43]
	v_mfma_f32_16x16x32_bf16 v[40:43], v[146:149], v[178:181], v[40:43]
	v_mfma_f32_16x16x32_bf16 v[48:51], v[138:141], v[178:181], v[48:51]
	v_mfma_f32_16x16x32_bf16 v[48:51], v[134:137], v[174:177], v[48:51]
	v_mfma_f32_16x16x32_bf16 v[32:35], v[134:137], v[182:185], v[32:35]
	v_mfma_f32_16x16x32_bf16 v[32:35], v[138:141], v[198:201], v[32:35]
	v_mfma_f32_16x16x32_bf16 v[24:27], v[146:149], v[198:201], v[24:27]
	v_mfma_f32_16x16x32_bf16 v[24:27], v[142:145], v[182:185], v[24:27]
	v_mfma_f32_16x16x32_bf16 v[8:11], v[142:145], v[202:205], v[8:11]
	v_mfma_f32_16x16x32_bf16 v[8:11], v[146:149], v[206:209], v[8:11]
	v_mfma_f32_16x16x32_bf16 v[16:19], v[138:141], v[206:209], v[16:19]
	v_mfma_f32_16x16x32_bf16 v[16:19], v[134:137], v[202:205], v[16:19]
	s_setprio 0
	s_setprio 1
	v_mfma_f32_16x16x32_bf16 v[4:7], v[150:153], v[202:205], v[4:7]
	v_mfma_f32_16x16x32_bf16 v[4:7], v[154:157], v[206:209], v[4:7]
	v_mfma_f32_16x16x32_bf16 v[0:3], v[162:165], v[206:209], v[0:3]
	v_mfma_f32_16x16x32_bf16 v[0:3], v[158:161], v[202:205], v[0:3]
	v_mfma_f32_16x16x32_bf16 v[12:15], v[158:161], v[182:185], v[12:15]
	v_mfma_f32_16x16x32_bf16 v[12:15], v[162:165], v[198:201], v[12:15]
	v_mfma_f32_16x16x32_bf16 v[20:23], v[154:157], v[198:201], v[20:23]
	v_mfma_f32_16x16x32_bf16 v[20:23], v[150:153], v[182:185], v[20:23]
	v_mfma_f32_16x16x32_bf16 v[36:39], v[150:153], v[174:177], v[36:39]
	v_mfma_f32_16x16x32_bf16 v[36:39], v[154:157], v[178:181], v[36:39]
	v_mfma_f32_16x16x32_bf16 v[28:31], v[162:165], v[178:181], v[28:31]
	v_mfma_f32_16x16x32_bf16 v[28:31], v[158:161], v[174:177], v[28:31]
	v_mfma_f32_16x16x32_bf16 v[44:47], v[158:161], v[166:169], v[44:47]
	v_mfma_f32_16x16x32_bf16 v[44:47], v[162:165], v[170:173], v[44:47]
	v_mfma_f32_16x16x32_bf16 v[52:55], v[154:157], v[170:173], v[52:55]
	v_mfma_f32_16x16x32_bf16 v[52:55], v[150:153], v[166:169], v[52:55]
	s_setprio 0
	s_barrier
	s_add_i32 s58, 0, 0x18000
	v_add_u32_e32 v128, s58, v189
	s_add_i32 s59, 0, 0x1c000
	ds_read_b128 v[134:137], v128
	ds_read_b128 v[138:141], v128 offset:1024
	ds_read_b128 v[142:145], v128 offset:2048
	ds_read_b128 v[146:149], v128 offset:3072
	v_add_u32_e32 v128, s59, v189
	ds_read_b128 v[150:153], v128
	ds_read_b128 v[154:157], v128 offset:1024
	ds_read_b128 v[158:161], v128 offset:2048
	ds_read_b128 v[162:165], v128 offset:3072
	s_add_u32 s56, s14, 0x4000
	s_addc_u32 s57, s15, 0
	s_mov_b32 m0, s27
	ds_read_b128 v[166:169], v196 offset:32768
	ds_read_b128 v[170:173], v196 offset:33792
	ds_read_b128 v[174:177], v196 offset:34816
	ds_read_b128 v[178:181], v196 offset:35840
	ds_read_b128 v[182:185], v196 offset:36864
	ds_read_b128 v[198:201], v196 offset:37888
	ds_read_b128 v[202:205], v196 offset:38912
	ds_read_b128 v[206:209], v196 offset:39936
	s_nop 0
	global_load_lds_dwordx4 v197, s[56:57]
	s_mov_b32 m0, s28
	s_nop 0
	global_load_lds_dwordx4 v186, s[56:57]
	s_cmp_eq_u32 s55, 0
	s_cbranch_scc1 .Lrx14
	s_waitcnt vmcnt(56)
	s_branch .Lry14

; #define PG8_STAGE(bufoff, gbase, voff) do { const char* _gb = (const char*)(gbase); asm volatile("" : "+s"(_gb)); _Pragma("unroll") for (int _i = 0; _i < 2; ++_i) \
;         __builtin_amdgcn_global_load_lds((const unsigned*)(_gb + (voff)[_i]), (PG8_LAS unsigned*)(lds + (bufoff) + ldsw + _i * 8192), 16, 0, 0); } while (0)
; #define PG8_LDA(dst, b, h) do { _Pragma("unroll") for (int m = 0; m < 4; ++m) _Pragma("unroll") for (int k = 0; k < 2; ++k) dst[m][k] = *(const PG8_LAS bf16x8*)(lds + PG8_SA(b, h) + aoff + m * 2048 + k * 1024); } while (0)
; #define PG8_MMA(ai, bj, At, Bt) do { __builtin_amdgcn_s_setprio(1); _Pragma("unroll") for (int m = 0; m < 4; ++m) _Pragma("unroll") for (int n = 0; n < 2; ++n) _Pragma("unroll") for (int k = 0; k < 2; ++k) \
;         acc[ai][bj][m][n] = __builtin_amdgcn_mfma_f32_16x16x32_bf16(Bt[n][k], At[m][k], acc[ai][bj][m][n], 0, 0, 0); __builtin_amdgcn_s_setprio(0); } while (0)
; #define PG8_WAIT_V(n) asm volatile("s_waitcnt vmcnt(" #n ")" ::: "memory")
; #define PG8_WAIT_L(n) asm volatile("s_waitcnt lgkmcnt(" #n ")" ::: "memory")
; #define PG8_BAR __builtin_amdgcn_s_barrier()
; #define PG8_SCHED __builtin_amdgcn_sched_barrier(0)
; template <class Epi, class Sched, bool ALIGN_EPI = false, bool SP2 = false, bool HALFM = false>
; __device__ __forceinline__ void gemm_phase(PG8_LAS unsigned char* lds, const Gemm g, const Sched& S, const Epi& E) {
;     ...
;             PG8_WAIT_V8R; PG8_WAIT_L(0); PG8_BAR; PG8_MMA(0, 0, At, B0); PG8_MMA(0, 1, At, B1); PG8_BAR; PG8_SCHED;
;             if constexpr (!HALFM) { PG8_LDA(At, 1, 1); } PG8_STAGE(PG8_SB(1, 0), b3, voffB); PG8_STAGE(PG8_SB(1, 1), b3 + hstep, voffB); PG8_STAGE(PG8_SA(1, 0), a3, voffA);
;             PG8_WAIT_V(8); PG8_WAIT_L(0); PG8_BAR; if constexpr (!HALFM) { PG8_MMA(1, 0, At, B0); PG8_MMA(1, 1, At, B1); } PG8_BAR; PG8_SCHED;
;             PG8_STAGE(PG8_SA(1, 1), a3 + hstepA, voffA);
.Lry14:
	s_waitcnt lgkmcnt(0)
	s_barrier
	s_setprio 1
	s_waitcnt lgkmcnt(0)
	v_mfma_f32_16x16x32_bf16 v[124:127], v[134:137], v[166:169], v[124:127]
	v_mfma_f32_16x16x32_bf16 v[124:127], v[138:141], v[170:173], v[124:127]
	v_mfma_f32_16x16x32_bf16 v[120:123], v[146:149], v[170:173], v[120:123]
	v_mfma_f32_16x16x32_bf16 v[120:123], v[142:145], v[166:169], v[120:123]
	v_mfma_f32_16x16x32_bf16 v[104:107], v[142:145], v[174:177], v[104:107]
	v_mfma_f32_16x16x32_bf16 v[104:107], v[146:149], v[178:181], v[104:107]
	v_mfma_f32_16x16x32_bf16 v[112:115], v[138:141], v[178:181], v[112:115]
	v_mfma_f32_16x16x32_bf16 v[112:115], v[134:137], v[174:177], v[112:115]
	v_mfma_f32_16x16x32_bf16 v[92:95], v[134:137], v[182:185], v[92:95]
	v_mfma_f32_16x16x32_bf16 v[92:95], v[138:141], v[198:201], v[92:95]
	v_mfma_f32_16x16x32_bf16 v[88:91], v[146:149], v[198:201], v[88:91]
	v_mfma_f32_16x16x32_bf16 v[88:91], v[142:145], v[182:185], v[88:91]
	v_mfma_f32_16x16x32_bf16 v[72:75], v[142:145], v[202:205], v[72:75]
	v_mfma_f32_16x16x32_bf16 v[72:75], v[146:149], v[206:209], v[72:75]
	v_mfma_f32_16x16x32_bf16 v[80:83], v[138:141], v[206:209], v[80:83]
	v_mfma_f32_16x16x32_bf16 v[80:83], v[134:137], v[202:205], v[80:83]
	s_setprio 0
	s_setprio 1
	v_mfma_f32_16x16x32_bf16 v[68:71], v[150:153], v[202:205], v[68:71]
	v_mfma_f32_16x16x32_bf16 v[68:71], v[154:157], v[206:209], v[68:71]
	v_mfma_f32_16x16x32_bf16 v[64:67], v[162:165], v[206:209], v[64:67]
	v_mfma_f32_16x16x32_bf16 v[64:67], v[158:161], v[202:205], v[64:67]
	v_mfma_f32_16x16x32_bf16 v[76:79], v[158:161], v[182:185], v[76:79]
	v_mfma_f32_16x16x32_bf16 v[76:79], v[162:165], v[198:201], v[76:79]
	v_mfma_f32_16x16x32_bf16 v[84:87], v[154:157], v[198:201], v[84:87]
	v_mfma_f32_16x16x32_bf16 v[84:87], v[150:153], v[182:185], v[84:87]
	v_mfma_f32_16x16x32_bf16 v[100:103], v[150:153], v[174:177], v[100:103]
	v_mfma_f32_16x16x32_bf16 v[100:103], v[154:157], v[178:181], v[100:103]
	v_mfma_f32_16x16x32_bf16 v[96:99], v[162:165], v[178:181], v[96:99]
	v_mfma_f32_16x16x32_bf16 v[96:99], v[158:161], v[174:177], v[96:99]
	v_mfma_f32_16x16x32_bf16 v[108:111], v[158:161], v[166:169], v[108:111]
	v_mfma_f32_16x16x32_bf16 v[108:111], v[162:165], v[170:173], v[108:111]
	v_mfma_f32_16x16x32_bf16 v[116:119], v[154:157], v[170:173], v[116:119]
	v_mfma_f32_16x16x32_bf16 v[116:119], v[150:153], v[166:169], v[116:119]
	s_setprio 0
	s_barrier
	s_add_u32 s56, s18, 0x8000
	s_addc_u32 s57, s19, 0
	s_add_i32 s55, s58, s20
	s_mov_b32 m0, s55
	ds_read_b128 v[166:169], v196 offset:49152
	ds_read_b128 v[170:173], v196 offset:50176
	ds_read_b128 v[174:177], v196 offset:51200
	ds_read_b128 v[178:181], v196 offset:52224
	ds_read_b128 v[182:185], v196 offset:53248
	ds_read_b128 v[198:201], v196 offset:54272
	ds_read_b128 v[202:205], v196 offset:55296
	ds_read_b128 v[206:209], v196 offset:56320
	s_nop 0
	global_load_lds_dwordx4 v197, s[56:57]
	s_add_i32 m0, s55, 0x2000
	s_add_u32 s18, s18, 0xc000
	s_addc_u32 s19, s19, 0
	s_add_i32 s55, s59, s20
	global_load_lds_dwordx4 v186, s[56:57]
	s_mov_b32 m0, s55
	s_nop 0
	global_load_lds_dwordx4 v197, s[18:19]
	s_add_i32 m0, s55, 0x2000
	s_nop 0
	global_load_lds_dwordx4 v186, s[18:19]
	s_mov_b32 m0, s34
	s_nop 0
	global_load_lds_dwordx4 v197, s[16:17]
	s_mov_b32 m0, s35
	s_nop 0
	global_load_lds_dwordx4 v186, s[16:17]
	s_waitcnt vmcnt(8)
	s_waitcnt lgkmcnt(0)
	s_barrier
	s_setprio 1
	s_waitcnt lgkmcnt(0)
	v_mfma_f32_16x16x32_bf16 v[60:63], v[134:137], v[166:169], v[60:63]
	v_mfma_f32_16x16x32_bf16 v[60:63], v[138:141], v[170:173], v[60:63]
	v_mfma_f32_16x16x32_bf16 v[56:59], v[146:149], v[170:173], v[56:59]
	v_mfma_f32_16x16x32_bf16 v[56:59], v[142:145], v[166:169], v[56:59]
	v_mfma_f32_16x16x32_bf16 v[40:43], v[142:145], v[174:177], v[40:43]
	v_mfma_f32_16x16x32_bf16 v[40:43], v[146:149], v[178:181], v[40:43]
	v_mfma_f32_16x16x32_bf16 v[48:51], v[138:141], v[178:181], v[48:51]
	v_mfma_f32_16x16x32_bf16 v[48:51], v[134:137], v[174:177], v[48:51]
	v_mfma_f32_16x16x32_bf16 v[32:35], v[134:137], v[182:185], v[32:35]
	v_mfma_f32_16x16x32_bf16 v[32:35], v[138:141], v[198:201], v[32:35]
	v_mfma_f32_16x16x32_bf16 v[24:27], v[146:149], v[198:201], v[24:27]
	v_mfma_f32_16x16x32_bf16 v[24:27], v[142:145], v[182:185], v[24:27]
	v_mfma_f32_16x16x32_bf16 v[8:11], v[142:145], v[202:205], v[8:11]
	v_mfma_f32_16x16x32_bf16 v[8:11], v[146:149], v[206:209], v[8:11]
	v_mfma_f32_16x16x32_bf16 v[16:19], v[138:141], v[206:209], v[16:19]
	v_mfma_f32_16x16x32_bf16 v[16:19], v[134:137], v[202:205], v[16:19]
	s_setprio 0
	s_setprio 1
	v_mfma_f32_16x16x32_bf16 v[4:7], v[150:153], v[202:205], v[4:7]
	v_mfma_f32_16x16x32_bf16 v[4:7], v[154:157], v[206:209], v[4:7]
	v_mfma_f32_16x16x32_bf16 v[0:3], v[162:165], v[206:209], v[0:3]
	v_mfma_f32_16x16x32_bf16 v[0:3], v[158:161], v[202:205], v[0:3]
	v_mfma_f32_16x16x32_bf16 v[12:15], v[158:161], v[182:185], v[12:15]
	v_mfma_f32_16x16x32_bf16 v[12:15], v[162:165], v[198:201], v[12:15]
	v_mfma_f32_16x16x32_bf16 v[20:23], v[154:157], v[198:201], v[20:23]
	v_mfma_f32_16x16x32_bf16 v[20:23], v[150:153], v[182:185], v[20:23]
	v_mfma_f32_16x16x32_bf16 v[36:39], v[150:153], v[174:177], v[36:39]
	v_mfma_f32_16x16x32_bf16 v[36:39], v[154:157], v[178:181], v[36:39]
	v_mfma_f32_16x16x32_bf16 v[28:31], v[162:165], v[178:181], v[28:31]
	v_mfma_f32_16x16x32_bf16 v[28:31], v[158:161], v[174:177], v[28:31]
	v_mfma_f32_16x16x32_bf16 v[44:47], v[158:161], v[166:169], v[44:47]
	v_mfma_f32_16x16x32_bf16 v[44:47], v[162:165], v[170:173], v[44:47]
	v_mfma_f32_16x16x32_bf16 v[52:55], v[154:157], v[170:173], v[52:55]
	v_mfma_f32_16x16x32_bf16 v[52:55], v[150:153], v[166:169], v[52:55]
	s_setprio 0
	s_barrier
	s_add_u32 s14, s14, 0xc000
	s_mov_b32 m0, s36
	s_addc_u32 s15, s15, 0
	s_add_i32 s54, s54, 2
	global_load_lds_dwordx4 v197, s[14:15]
	s_mov_b32 m0, s37
	s_add_u32 s50, s50, 0x10000
	global_load_lds_dwordx4 v186, s[14:15]
	s_addc_u32 s51, s51, 0
	s_add_u32 s52, s52, 0x10000
	s_addc_u32 s53, s53, 0
	s_cmpk_gt_u32 s54, 0xa9
	s_cbranch_scc0 .LBB0_1422
	s_and_b64 vcc, exec, s[6:7]
	s_cbranch_vccz .LBB0_1425
	s_barrier
